# vH_e1
# baseline (speedup 1.0000x reference)
.Lsp_skip:
	s_or_b64 exec, exec, s[36:37]
	v_mov_b32_e32 v244, v245
	v_mov_b32_e32 v245, v187
	s_add_u32 s58, s58, 1
	s_cmp_lt_u32 s58, 2
	s_cbranch_scc1 .Lsp_loop
	s_waitcnt vmcnt(17)
	v_cvt_pk_f16_f32 v204, v204, v205
	v_cvt_pk_f16_f32 v205, v206, v207
	ds_write_b64 v237, v[204:205]
	s_waitcnt vmcnt(16)
	v_cvt_pk_f16_f32 v208, v208, v209
	v_cvt_pk_f16_f32 v209, v210, v211
	ds_write_b64 v237, v[208:209] offset:4352
	s_waitcnt vmcnt(15)
	v_cvt_pk_f16_f32 v212, v212, v213
	v_cvt_pk_f16_f32 v213, v214, v215
	ds_write_b64 v237, v[212:213] offset:8704
	s_waitcnt vmcnt(14)
	v_cvt_pk_f16_f32 v216, v216, v217
	v_cvt_pk_f16_f32 v217, v218, v219
	ds_write_b64 v237, v[216:217] offset:13056
	s_waitcnt vmcnt(13)
	v_cvt_pk_f16_f32 v220, v220, v221
	v_cvt_pk_f16_f32 v221, v222, v223
	ds_write_b64 v237, v[220:221] offset:17408
	s_waitcnt vmcnt(12)
	v_cvt_pk_f16_f32 v224, v224, v225
	v_cvt_pk_f16_f32 v225, v226, v227
	ds_write_b64 v237, v[224:225] offset:21760
	s_waitcnt vmcnt(11)
	v_cvt_pk_f16_f32 v228, v228, v229
	v_cvt_pk_f16_f32 v229, v230, v231
	ds_write_b64 v237, v[228:229] offset:26112
	s_waitcnt vmcnt(10)
	v_cvt_pk_f16_f32 v232, v232, v233
	v_cvt_pk_f16_f32 v233, v234, v235
	ds_write_b64 v237, v[232:233] offset:30464
	global_load_dwordx4 v[204:207], v238, s[40:41] offset:512
	global_load_dwordx4 v[208:211], v238, s[42:43] offset:512
	global_load_dwordx4 v[212:215], v238, s[44:45] offset:512
	global_load_dwordx4 v[216:219], v238, s[46:47] offset:512
	global_load_dwordx4 v[220:223], v238, s[48:49] offset:512
	global_load_dwordx4 v[224:227], v238, s[50:51] offset:512
	global_load_dwordx4 v[228:231], v238, s[52:53] offset:512
	global_load_dwordx4 v[232:235], v238, s[54:55] offset:512
	s_waitcnt lgkmcnt(0)
	s_barrier
	ds_read_b128 v[130:133], v236
	ds_read_b128 v[134:137], v236 offset:4352
	ds_read_b128 v[138:141], v236 offset:8704
	ds_read_b128 v[142:145], v236 offset:13056
	s_waitcnt vmcnt(16)
	s_waitcnt lgkmcnt(3)
	v_mfma_f32_32x32x16_f16 v[82:97], v[130:133], v[146:149], 0
	v_mfma_f32_32x32x16_f16 v[50:65], v[130:133], v[150:153], 0
	ds_read_b128 v[130:133], v236 offset:32
	s_waitcnt lgkmcnt(3)
	v_mfma_f32_32x32x16_f16 v[114:129], v[134:137], v[146:149], 0
	v_mfma_f32_32x32x16_f16 v[34:49], v[134:137], v[150:153], 0
	ds_read_b128 v[134:137], v236 offset:4384
	s_waitcnt lgkmcnt(3)
	v_mfma_f32_32x32x16_f16 v[98:113], v[138:141], v[146:149], 0
	v_mfma_f32_32x32x16_f16 v[18:33], v[138:141], v[150:153], 0
	ds_read_b128 v[138:141], v236 offset:8736
	s_waitcnt lgkmcnt(3)
	v_mfma_f32_32x32x16_f16 v[66:81], v[142:145], v[146:149], 0
	v_mfma_f32_32x32x16_f16 v[2:17], v[142:145], v[150:153], 0
	ds_read_b128 v[142:145], v236 offset:13088
	global_load_dwordx4 v[146:149], v239, s[56:57]
	global_load_dwordx4 v[150:153], v239, s[56:57] offset:512
	s_add_u32 s56, s56, 0x4000
	s_addc_u32 s57, s57, 0
	s_waitcnt vmcnt(16)
	s_waitcnt lgkmcnt(3)
	v_mfma_f32_32x32x16_f16 v[82:97], v[130:133], v[154:157], v[82:97]
	v_mfma_f32_32x32x16_f16 v[50:65], v[130:133], v[158:161], v[50:65]
	ds_read_b128 v[130:133], v236 offset:64
	s_waitcnt lgkmcnt(3)
	v_mfma_f32_32x32x16_f16 v[114:129], v[134:137], v[154:157], v[114:129]
	v_mfma_f32_32x32x16_f16 v[34:49], v[134:137], v[158:161], v[34:49]
	ds_read_b128 v[134:137], v236 offset:4416
	s_waitcnt lgkmcnt(3)
	v_mfma_f32_32x32x16_f16 v[98:113], v[138:141], v[154:157], v[98:113]
	v_mfma_f32_32x32x16_f16 v[18:33], v[138:141], v[158:161], v[18:33]
	ds_read_b128 v[138:141], v236 offset:8768
	s_waitcnt lgkmcnt(3)
	v_mfma_f32_32x32x16_f16 v[66:81], v[142:145], v[154:157], v[66:81]
	v_mfma_f32_32x32x16_f16 v[2:17], v[142:145], v[158:161], v[2:17]
	ds_read_b128 v[142:145], v236 offset:13120
	global_load_dwordx4 v[154:157], v239, s[56:57]
	global_load_dwordx4 v[158:161], v239, s[56:57] offset:512
	s_add_u32 s56, s56, 0x4000
	s_addc_u32 s57, s57, 0
	s_waitcnt vmcnt(16)
	s_waitcnt lgkmcnt(3)
	v_mfma_f32_32x32x16_f16 v[82:97], v[130:133], v[162:165], v[82:97]
	v_mfma_f32_32x32x16_f16 v[50:65], v[130:133], v[166:169], v[50:65]
	ds_read_b128 v[130:133], v236 offset:96
	s_waitcnt lgkmcnt(3)
	v_mfma_f32_32x32x16_f16 v[114:129], v[134:137], v[162:165], v[114:129]
	v_mfma_f32_32x32x16_f16 v[34:49], v[134:137], v[166:169], v[34:49]
	ds_read_b128 v[134:137], v236 offset:4448
	s_waitcnt lgkmcnt(3)
	v_mfma_f32_32x32x16_f16 v[98:113], v[138:141], v[162:165], v[98:113]
	v_mfma_f32_32x32x16_f16 v[18:33], v[138:141], v[166:169], v[18:33]
	ds_read_b128 v[138:141], v236 offset:8800
	s_waitcnt lgkmcnt(3)
	v_mfma_f32_32x32x16_f16 v[66:81], v[142:145], v[162:165], v[66:81]
	v_mfma_f32_32x32x16_f16 v[2:17], v[142:145], v[166:169], v[2:17]
	ds_read_b128 v[142:145], v236 offset:13152
	global_load_dwordx4 v[162:165], v239, s[56:57]
	global_load_dwordx4 v[166:169], v239, s[56:57] offset:512
	s_add_u32 s56, s56, 0x4000
	s_addc_u32 s57, s57, 0
	s_waitcnt vmcnt(16)
	s_waitcnt lgkmcnt(3)
	v_mfma_f32_32x32x16_f16 v[82:97], v[130:133], v[170:173], v[82:97]
	v_mfma_f32_32x32x16_f16 v[50:65], v[130:133], v[174:177], v[50:65]
	ds_read_b128 v[130:133], v236 offset:128
	s_waitcnt lgkmcnt(3)
	v_mfma_f32_32x32x16_f16 v[114:129], v[134:137], v[170:173], v[114:129]
	v_mfma_f32_32x32x16_f16 v[34:49], v[134:137], v[174:177], v[34:49]
	ds_read_b128 v[134:137], v236 offset:4480
	s_waitcnt lgkmcnt(3)
	v_mfma_f32_32x32x16_f16 v[98:113], v[138:141], v[170:173], v[98:113]
	v_mfma_f32_32x32x16_f16 v[18:33], v[138:141], v[174:177], v[18:33]
	ds_read_b128 v[138:141], v236 offset:8832
	s_waitcnt lgkmcnt(3)
	v_mfma_f32_32x32x16_f16 v[66:81], v[142:145], v[170:173], v[66:81]
	v_mfma_f32_32x32x16_f16 v[2:17], v[142:145], v[174:177], v[2:17]
	ds_read_b128 v[142:145], v236 offset:13184
	global_load_dwordx4 v[170:173], v239, s[56:57]
	global_load_dwordx4 v[174:177], v239, s[56:57] offset:512
	s_add_u32 s56, s56, 0x4000
	s_addc_u32 s57, s57, 0
	s_waitcnt vmcnt(16)
	s_waitcnt lgkmcnt(3)
	v_mfma_f32_32x32x16_f16 v[82:97], v[130:133], v[178:181], v[82:97]
	v_mfma_f32_32x32x16_f16 v[50:65], v[130:133], v[182:185], v[50:65]
	ds_read_b128 v[130:133], v236 offset:160
	s_waitcnt lgkmcnt(3)
	v_mfma_f32_32x32x16_f16 v[114:129], v[134:137], v[178:181], v[114:129]
	v_mfma_f32_32x32x16_f16 v[34:49], v[134:137], v[182:185], v[34:49]
	ds_read_b128 v[134:137], v236 offset:4512
	s_waitcnt lgkmcnt(3)
	v_mfma_f32_32x32x16_f16 v[98:113], v[138:141], v[178:181], v[98:113]
	v_mfma_f32_32x32x16_f16 v[18:33], v[138:141], v[182:185], v[18:33]
	ds_read_b128 v[138:141], v236 offset:8864
	s_waitcnt lgkmcnt(3)
	v_mfma_f32_32x32x16_f16 v[66:81], v[142:145], v[178:181], v[66:81]
	v_mfma_f32_32x32x16_f16 v[2:17], v[142:145], v[182:185], v[2:17]
	ds_read_b128 v[142:145], v236 offset:13216
	global_load_dwordx4 v[178:181], v239, s[56:57]
	global_load_dwordx4 v[182:185], v239, s[56:57] offset:512
	s_add_u32 s56, s56, 0x4000
	s_addc_u32 s57, s57, 0
	s_waitcnt vmcnt(8)
	s_waitcnt lgkmcnt(3)
	v_mfma_f32_32x32x16_f16 v[82:97], v[130:133], v[146:149], v[82:97]
	v_mfma_f32_32x32x16_f16 v[50:65], v[130:133], v[150:153], v[50:65]
	ds_read_b128 v[130:133], v236 offset:192
	s_waitcnt lgkmcnt(3)
	v_mfma_f32_32x32x16_f16 v[114:129], v[134:137], v[146:149], v[114:129]
	v_mfma_f32_32x32x16_f16 v[34:49], v[134:137], v[150:153], v[34:49]
	ds_read_b128 v[134:137], v236 offset:4544
	s_waitcnt lgkmcnt(3)
	v_mfma_f32_32x32x16_f16 v[98:113], v[138:141], v[146:149], v[98:113]
	v_mfma_f32_32x32x16_f16 v[18:33], v[138:141], v[150:153], v[18:33]
	ds_read_b128 v[138:141], v236 offset:8896
	s_waitcnt lgkmcnt(3)
	v_mfma_f32_32x32x16_f16 v[66:81], v[142:145], v[146:149], v[66:81]
	v_mfma_f32_32x32x16_f16 v[2:17], v[142:145], v[150:153], v[2:17]
	ds_read_b128 v[142:145], v236 offset:13248
	global_load_dwordx4 v[146:149], v239, s[56:57]
	global_load_dwordx4 v[150:153], v239, s[56:57] offset:512
	s_add_u32 s56, s56, 0x4000
	s_addc_u32 s57, s57, 0
	s_waitcnt vmcnt(19)
	v_cvt_pk_f16_f32 v204, v204, v205
	v_cvt_pk_f16_f32 v205, v206, v207
	ds_write_b64 v237, v[204:205] offset:34816
	s_waitcnt vmcnt(18)
	v_cvt_pk_f16_f32 v208, v208, v209
	v_cvt_pk_f16_f32 v209, v210, v211
	ds_write_b64 v237, v[208:209] offset:39168
	s_waitcnt vmcnt(17)
	v_cvt_pk_f16_f32 v212, v212, v213
	v_cvt_pk_f16_f32 v213, v214, v215
	ds_write_b64 v237, v[212:213] offset:43520
	s_waitcnt vmcnt(16)
	v_cvt_pk_f16_f32 v216, v216, v217
	v_cvt_pk_f16_f32 v217, v218, v219
	ds_write_b64 v237, v[216:217] offset:47872
	s_waitcnt vmcnt(15)
	v_cvt_pk_f16_f32 v220, v220, v221
	v_cvt_pk_f16_f32 v221, v222, v223
	ds_write_b64 v237, v[220:221] offset:52224
	s_waitcnt vmcnt(14)
	v_cvt_pk_f16_f32 v224, v224, v225
	v_cvt_pk_f16_f32 v225, v226, v227
	ds_write_b64 v237, v[224:225] offset:56576
	s_waitcnt vmcnt(13)
	v_cvt_pk_f16_f32 v228, v228, v229
	v_cvt_pk_f16_f32 v229, v230, v231
	ds_write_b64 v237, v[228:229] offset:60928
	s_waitcnt vmcnt(12)
	v_cvt_pk_f16_f32 v232, v232, v233
	v_cvt_pk_f16_f32 v233, v234, v235
	ds_write_b64 v237, v[232:233] offset:65280
	global_load_dwordx4 v[204:207], v238, s[40:41] offset:1024
	global_load_dwordx4 v[208:211], v238, s[42:43] offset:1024
	global_load_dwordx4 v[212:215], v238, s[44:45] offset:1024
	global_load_dwordx4 v[216:219], v238, s[46:47] offset:1024
	global_load_dwordx4 v[220:223], v238, s[48:49] offset:1024
	global_load_dwordx4 v[224:227], v238, s[50:51] offset:1024
	global_load_dwordx4 v[228:231], v238, s[52:53] offset:1024
	global_load_dwordx4 v[232:235], v238, s[54:55] offset:1024
	s_waitcnt vmcnt(16)
	s_waitcnt lgkmcnt(11)
	v_mfma_f32_32x32x16_f16 v[82:97], v[130:133], v[154:157], v[82:97]
	v_mfma_f32_32x32x16_f16 v[50:65], v[130:133], v[158:161], v[50:65]
	ds_read_b128 v[130:133], v236 offset:224
	s_waitcnt lgkmcnt(11)
	v_mfma_f32_32x32x16_f16 v[114:129], v[134:137], v[154:157], v[114:129]
	v_mfma_f32_32x32x16_f16 v[34:49], v[134:137], v[158:161], v[34:49]
	ds_read_b128 v[134:137], v236 offset:4576
	s_waitcnt lgkmcnt(11)
	v_mfma_f32_32x32x16_f16 v[98:113], v[138:141], v[154:157], v[98:113]
	v_mfma_f32_32x32x16_f16 v[18:33], v[138:141], v[158:161], v[18:33]
	ds_read_b128 v[138:141], v236 offset:8928
	s_waitcnt lgkmcnt(11)
	v_mfma_f32_32x32x16_f16 v[66:81], v[142:145], v[154:157], v[66:81]
	v_mfma_f32_32x32x16_f16 v[2:17], v[142:145], v[158:161], v[2:17]
	ds_read_b128 v[142:145], v236 offset:13280
	global_load_dwordx4 v[154:157], v239, s[56:57]
	global_load_dwordx4 v[158:161], v239, s[56:57] offset:512
	s_add_u32 s56, s56, 0x4000
	s_addc_u32 s57, s57, 0
	s_waitcnt vmcnt(16)
	s_waitcnt lgkmcnt(3)
	v_mfma_f32_32x32x16_f16 v[82:97], v[130:133], v[162:165], v[82:97]
	v_mfma_f32_32x32x16_f16 v[50:65], v[130:133], v[166:169], v[50:65]
	s_waitcnt lgkmcnt(2)
	v_mfma_f32_32x32x16_f16 v[114:129], v[134:137], v[162:165], v[114:129]
	v_mfma_f32_32x32x16_f16 v[34:49], v[134:137], v[166:169], v[34:49]
	s_waitcnt lgkmcnt(1)
	v_mfma_f32_32x32x16_f16 v[98:113], v[138:141], v[162:165], v[98:113]
	v_mfma_f32_32x32x16_f16 v[18:33], v[138:141], v[166:169], v[18:33]
	s_waitcnt lgkmcnt(0)
	v_mfma_f32_32x32x16_f16 v[66:81], v[142:145], v[162:165], v[66:81]
	v_mfma_f32_32x32x16_f16 v[2:17], v[142:145], v[166:169], v[2:17]
	global_load_dwordx4 v[162:165], v239, s[56:57]
	global_load_dwordx4 v[166:169], v239, s[56:57] offset:512
	s_add_u32 s56, s56, 0x4000
	s_addc_u32 s57, s57, 0
	s_waitcnt lgkmcnt(0)
	s_barrier
	ds_read_b128 v[130:133], v236 offset:34816
	ds_read_b128 v[134:137], v236 offset:39168
	ds_read_b128 v[138:141], v236 offset:43520
	ds_read_b128 v[142:145], v236 offset:47872
	s_waitcnt vmcnt(16)
	s_waitcnt lgkmcnt(3)
	v_mfma_f32_32x32x16_f16 v[82:97], v[130:133], v[170:173], v[82:97]
	v_mfma_f32_32x32x16_f16 v[50:65], v[130:133], v[174:177], v[50:65]
	ds_read_b128 v[130:133], v236 offset:34848
	s_waitcnt lgkmcnt(3)
	v_mfma_f32_32x32x16_f16 v[114:129], v[134:137], v[170:173], v[114:129]
	v_mfma_f32_32x32x16_f16 v[34:49], v[134:137], v[174:177], v[34:49]
	ds_read_b128 v[134:137], v236 offset:39200
	s_waitcnt lgkmcnt(3)
	v_mfma_f32_32x32x16_f16 v[98:113], v[138:141], v[170:173], v[98:113]
	v_mfma_f32_32x32x16_f16 v[18:33], v[138:141], v[174:177], v[18:33]
	ds_read_b128 v[138:141], v236 offset:43552
	s_waitcnt lgkmcnt(3)
	v_mfma_f32_32x32x16_f16 v[66:81], v[142:145], v[170:173], v[66:81]
	v_mfma_f32_32x32x16_f16 v[2:17], v[142:145], v[174:177], v[2:17]
	ds_read_b128 v[142:145], v236 offset:47904
	global_load_dwordx4 v[170:173], v239, s[56:57]
	global_load_dwordx4 v[174:177], v239, s[56:57] offset:512
	s_add_u32 s56, s56, 0x4000
	s_addc_u32 s57, s57, 0
	s_waitcnt vmcnt(16)
	s_waitcnt lgkmcnt(3)
	v_mfma_f32_32x32x16_f16 v[82:97], v[130:133], v[178:181], v[82:97]
	v_mfma_f32_32x32x16_f16 v[50:65], v[130:133], v[182:185], v[50:65]
	ds_read_b128 v[130:133], v236 offset:34880
	s_waitcnt lgkmcnt(3)
	v_mfma_f32_32x32x16_f16 v[114:129], v[134:137], v[178:181], v[114:129]
	v_mfma_f32_32x32x16_f16 v[34:49], v[134:137], v[182:185], v[34:49]
	ds_read_b128 v[134:137], v236 offset:39232
	s_waitcnt lgkmcnt(3)
	v_mfma_f32_32x32x16_f16 v[98:113], v[138:141], v[178:181], v[98:113]
	v_mfma_f32_32x32x16_f16 v[18:33], v[138:141], v[182:185], v[18:33]
	ds_read_b128 v[138:141], v236 offset:43584
	s_waitcnt lgkmcnt(3)
	v_mfma_f32_32x32x16_f16 v[66:81], v[142:145], v[178:181], v[66:81]
	v_mfma_f32_32x32x16_f16 v[2:17], v[142:145], v[182:185], v[2:17]
	ds_read_b128 v[142:145], v236 offset:47936
	global_load_dwordx4 v[178:181], v239, s[56:57]
	global_load_dwordx4 v[182:185], v239, s[56:57] offset:512
	s_add_u32 s56, s56, 0x4000
	s_addc_u32 s57, s57, 0
	s_waitcnt vmcnt(16)
	s_waitcnt lgkmcnt(3)
	v_mfma_f32_32x32x16_f16 v[82:97], v[130:133], v[146:149], v[82:97]
	v_mfma_f32_32x32x16_f16 v[50:65], v[130:133], v[150:153], v[50:65]
	ds_read_b128 v[130:133], v236 offset:34912
	s_waitcnt lgkmcnt(3)
	v_mfma_f32_32x32x16_f16 v[114:129], v[134:137], v[146:149], v[114:129]
	v_mfma_f32_32x32x16_f16 v[34:49], v[134:137], v[150:153], v[34:49]
	ds_read_b128 v[134:137], v236 offset:39264
	s_waitcnt lgkmcnt(3)
	v_mfma_f32_32x32x16_f16 v[98:113], v[138:141], v[146:149], v[98:113]
	v_mfma_f32_32x32x16_f16 v[18:33], v[138:141], v[150:153], v[18:33]
	ds_read_b128 v[138:141], v236 offset:43616
	s_waitcnt lgkmcnt(3)
	v_mfma_f32_32x32x16_f16 v[66:81], v[142:145], v[146:149], v[66:81]
	v_mfma_f32_32x32x16_f16 v[2:17], v[142:145], v[150:153], v[2:17]
	ds_read_b128 v[142:145], v236 offset:47968
	global_load_dwordx4 v[146:149], v239, s[56:57]
	global_load_dwordx4 v[150:153], v239, s[56:57] offset:512
	s_add_u32 s56, s56, 0x4000
	s_addc_u32 s57, s57, 0
	s_waitcnt vmcnt(8)
	s_waitcnt lgkmcnt(3)
	v_mfma_f32_32x32x16_f16 v[82:97], v[130:133], v[154:157], v[82:97]
	v_mfma_f32_32x32x16_f16 v[50:65], v[130:133], v[158:161], v[50:65]
	ds_read_b128 v[130:133], v236 offset:34944
	s_waitcnt lgkmcnt(3)
	v_mfma_f32_32x32x16_f16 v[114:129], v[134:137], v[154:157], v[114:129]
	v_mfma_f32_32x32x16_f16 v[34:49], v[134:137], v[158:161], v[34:49]
	ds_read_b128 v[134:137], v236 offset:39296
	s_waitcnt lgkmcnt(3)
	v_mfma_f32_32x32x16_f16 v[98:113], v[138:141], v[154:157], v[98:113]
	v_mfma_f32_32x32x16_f16 v[18:33], v[138:141], v[158:161], v[18:33]
	ds_read_b128 v[138:141], v236 offset:43648
	s_waitcnt lgkmcnt(3)
	v_mfma_f32_32x32x16_f16 v[66:81], v[142:145], v[154:157], v[66:81]
	v_mfma_f32_32x32x16_f16 v[2:17], v[142:145], v[158:161], v[2:17]
	ds_read_b128 v[142:145], v236 offset:48000
	global_load_dwordx4 v[154:157], v239, s[56:57]
	global_load_dwordx4 v[158:161], v239, s[56:57] offset:512
	s_add_u32 s56, s56, 0x4000
	s_addc_u32 s57, s57, 0
	s_waitcnt vmcnt(8)
	s_waitcnt lgkmcnt(3)
	v_mfma_f32_32x32x16_f16 v[82:97], v[130:133], v[162:165], v[82:97]
	v_mfma_f32_32x32x16_f16 v[50:65], v[130:133], v[166:169], v[50:65]
	ds_read_b128 v[130:133], v236 offset:34976
	s_waitcnt lgkmcnt(3)
	v_mfma_f32_32x32x16_f16 v[114:129], v[134:137], v[162:165], v[114:129]
	v_mfma_f32_32x32x16_f16 v[34:49], v[134:137], v[166:169], v[34:49]
	ds_read_b128 v[134:137], v236 offset:39328
	s_waitcnt lgkmcnt(3)
	v_mfma_f32_32x32x16_f16 v[98:113], v[138:141], v[162:165], v[98:113]
	v_mfma_f32_32x32x16_f16 v[18:33], v[138:141], v[166:169], v[18:33]
	ds_read_b128 v[138:141], v236 offset:43680
	s_waitcnt lgkmcnt(3)
	v_mfma_f32_32x32x16_f16 v[66:81], v[142:145], v[162:165], v[66:81]
	v_mfma_f32_32x32x16_f16 v[2:17], v[142:145], v[166:169], v[2:17]
	ds_read_b128 v[142:145], v236 offset:48032
	global_load_dwordx4 v[162:165], v239, s[56:57]
	global_load_dwordx4 v[166:169], v239, s[56:57] offset:512
	s_add_u32 s56, s56, 0x4000
	s_addc_u32 s57, s57, 0
	s_waitcnt vmcnt(8)
	s_waitcnt lgkmcnt(3)
	v_mfma_f32_32x32x16_f16 v[82:97], v[130:133], v[170:173], v[82:97]
	v_mfma_f32_32x32x16_f16 v[50:65], v[130:133], v[174:177], v[50:65]
	ds_read_b128 v[130:133], v236 offset:35008
	s_waitcnt lgkmcnt(3)
	v_mfma_f32_32x32x16_f16 v[114:129], v[134:137], v[170:173], v[114:129]
	v_mfma_f32_32x32x16_f16 v[34:49], v[134:137], v[174:177], v[34:49]
	ds_read_b128 v[134:137], v236 offset:39360
	s_waitcnt lgkmcnt(3)
	v_mfma_f32_32x32x16_f16 v[98:113], v[138:141], v[170:173], v[98:113]
	v_mfma_f32_32x32x16_f16 v[18:33], v[138:141], v[174:177], v[18:33]
	ds_read_b128 v[138:141], v236 offset:43712
	s_waitcnt lgkmcnt(3)
	v_mfma_f32_32x32x16_f16 v[66:81], v[142:145], v[170:173], v[66:81]
	v_mfma_f32_32x32x16_f16 v[2:17], v[142:145], v[174:177], v[2:17]
	ds_read_b128 v[142:145], v236 offset:48064
	global_load_dwordx4 v[170:173], v239, s[56:57]
	global_load_dwordx4 v[174:177], v239, s[56:57] offset:512
	s_add_u32 s56, s56, 0x4000
	s_addc_u32 s57, s57, 0
	s_waitcnt vmcnt(23)
	v_cvt_pk_f16_f32 v204, v204, v205
	v_cvt_pk_f16_f32 v205, v206, v207
	ds_write_b64 v237, v[204:205]
	s_waitcnt vmcnt(22)
	v_cvt_pk_f16_f32 v208, v208, v209
	v_cvt_pk_f16_f32 v209, v210, v211
	ds_write_b64 v237, v[208:209] offset:4352
	s_waitcnt vmcnt(21)
	v_cvt_pk_f16_f32 v212, v212, v213
	v_cvt_pk_f16_f32 v213, v214, v215
	ds_write_b64 v237, v[212:213] offset:8704
	s_waitcnt vmcnt(20)
	v_cvt_pk_f16_f32 v216, v216, v217
	v_cvt_pk_f16_f32 v217, v218, v219
	ds_write_b64 v237, v[216:217] offset:13056
	s_waitcnt vmcnt(19)
	v_cvt_pk_f16_f32 v220, v220, v221
	v_cvt_pk_f16_f32 v221, v222, v223
	ds_write_b64 v237, v[220:221] offset:17408
	s_waitcnt vmcnt(18)
	v_cvt_pk_f16_f32 v224, v224, v225
	v_cvt_pk_f16_f32 v225, v226, v227
	ds_write_b64 v237, v[224:225] offset:21760
	s_waitcnt vmcnt(17)
	v_cvt_pk_f16_f32 v228, v228, v229
	v_cvt_pk_f16_f32 v229, v230, v231
	ds_write_b64 v237, v[228:229] offset:26112
	s_waitcnt vmcnt(16)
	v_cvt_pk_f16_f32 v232, v232, v233
	v_cvt_pk_f16_f32 v233, v234, v235
	ds_write_b64 v237, v[232:233] offset:30464
	global_load_dwordx4 v[204:207], v238, s[40:41] offset:1536
	global_load_dwordx4 v[208:211], v238, s[42:43] offset:1536
	global_load_dwordx4 v[212:215], v238, s[44:45] offset:1536
	global_load_dwordx4 v[216:219], v238, s[46:47] offset:1536
	global_load_dwordx4 v[220:223], v238, s[48:49] offset:1536
	global_load_dwordx4 v[224:227], v238, s[50:51] offset:1536
	global_load_dwordx4 v[228:231], v238, s[52:53] offset:1536
	global_load_dwordx4 v[232:235], v238, s[54:55] offset:1536
	s_waitcnt vmcnt(16)
	s_waitcnt lgkmcnt(11)
	v_mfma_f32_32x32x16_f16 v[82:97], v[130:133], v[178:181], v[82:97]
	v_mfma_f32_32x32x16_f16 v[50:65], v[130:133], v[182:185], v[50:65]
	ds_read_b128 v[130:133], v236 offset:35040
	s_waitcnt lgkmcnt(11)
	v_mfma_f32_32x32x16_f16 v[114:129], v[134:137], v[178:181], v[114:129]
	v_mfma_f32_32x32x16_f16 v[34:49], v[134:137], v[182:185], v[34:49]
	ds_read_b128 v[134:137], v236 offset:39392
	s_waitcnt lgkmcnt(11)
	v_mfma_f32_32x32x16_f16 v[98:113], v[138:141], v[178:181], v[98:113]
	v_mfma_f32_32x32x16_f16 v[18:33], v[138:141], v[182:185], v[18:33]
	ds_read_b128 v[138:141], v236 offset:43744
	s_waitcnt lgkmcnt(11)
	v_mfma_f32_32x32x16_f16 v[66:81], v[142:145], v[178:181], v[66:81]
	v_mfma_f32_32x32x16_f16 v[2:17], v[142:145], v[182:185], v[2:17]
	ds_read_b128 v[142:145], v236 offset:48096
	global_load_dwordx4 v[178:181], v239, s[56:57]
	global_load_dwordx4 v[182:185], v239, s[56:57] offset:512
	s_add_u32 s56, s56, 0x4000
	s_addc_u32 s57, s57, 0
	s_waitcnt vmcnt(16)
	s_waitcnt lgkmcnt(3)
	v_mfma_f32_32x32x16_f16 v[82:97], v[130:133], v[146:149], v[82:97]
	v_mfma_f32_32x32x16_f16 v[50:65], v[130:133], v[150:153], v[50:65]
	s_waitcnt lgkmcnt(2)
	v_mfma_f32_32x32x16_f16 v[114:129], v[134:137], v[146:149], v[114:129]
	v_mfma_f32_32x32x16_f16 v[34:49], v[134:137], v[150:153], v[34:49]
	s_waitcnt lgkmcnt(1)
	v_mfma_f32_32x32x16_f16 v[98:113], v[138:141], v[146:149], v[98:113]
	v_mfma_f32_32x32x16_f16 v[18:33], v[138:141], v[150:153], v[18:33]
	s_waitcnt lgkmcnt(0)
	v_mfma_f32_32x32x16_f16 v[66:81], v[142:145], v[146:149], v[66:81]
	v_mfma_f32_32x32x16_f16 v[2:17], v[142:145], v[150:153], v[2:17]
	global_load_dwordx4 v[146:149], v239, s[56:57]
	global_load_dwordx4 v[150:153], v239, s[56:57] offset:512
	s_add_u32 s56, s56, 0x4000
	s_addc_u32 s57, s57, 0
	s_waitcnt lgkmcnt(0)
	s_barrier
	ds_read_b128 v[130:133], v236
	ds_read_b128 v[134:137], v236 offset:4352
	ds_read_b128 v[138:141], v236 offset:8704
	ds_read_b128 v[142:145], v236 offset:13056
	s_waitcnt vmcnt(16)
	s_waitcnt lgkmcnt(3)
	v_mfma_f32_32x32x16_f16 v[82:97], v[130:133], v[154:157], v[82:97]
	v_mfma_f32_32x32x16_f16 v[50:65], v[130:133], v[158:161], v[50:65]
	ds_read_b128 v[130:133], v236 offset:32
	s_waitcnt lgkmcnt(3)
	v_mfma_f32_32x32x16_f16 v[114:129], v[134:137], v[154:157], v[114:129]
	v_mfma_f32_32x32x16_f16 v[34:49], v[134:137], v[158:161], v[34:49]
	ds_read_b128 v[134:137], v236 offset:4384
	s_waitcnt lgkmcnt(3)
	v_mfma_f32_32x32x16_f16 v[98:113], v[138:141], v[154:157], v[98:113]
	v_mfma_f32_32x32x16_f16 v[18:33], v[138:141], v[158:161], v[18:33]
	ds_read_b128 v[138:141], v236 offset:8736
	s_waitcnt lgkmcnt(3)
	v_mfma_f32_32x32x16_f16 v[66:81], v[142:145], v[154:157], v[66:81]
	v_mfma_f32_32x32x16_f16 v[2:17], v[142:145], v[158:161], v[2:17]
	ds_read_b128 v[142:145], v236 offset:13088
	global_load_dwordx4 v[154:157], v239, s[56:57]
	global_load_dwordx4 v[158:161], v239, s[56:57] offset:512
	s_add_u32 s56, s56, 0x4000
	s_addc_u32 s57, s57, 0
	s_waitcnt vmcnt(16)
	s_waitcnt lgkmcnt(3)
	v_mfma_f32_32x32x16_f16 v[82:97], v[130:133], v[162:165], v[82:97]
	v_mfma_f32_32x32x16_f16 v[50:65], v[130:133], v[166:169], v[50:65]
	ds_read_b128 v[130:133], v236 offset:64
	s_waitcnt lgkmcnt(3)
	v_mfma_f32_32x32x16_f16 v[114:129], v[134:137], v[162:165], v[114:129]
	v_mfma_f32_32x32x16_f16 v[34:49], v[134:137], v[166:169], v[34:49]
	ds_read_b128 v[134:137], v236 offset:4416
	s_waitcnt lgkmcnt(3)
	v_mfma_f32_32x32x16_f16 v[98:113], v[138:141], v[162:165], v[98:113]
	v_mfma_f32_32x32x16_f16 v[18:33], v[138:141], v[166:169], v[18:33]
	ds_read_b128 v[138:141], v236 offset:8768
	s_waitcnt lgkmcnt(3)
	v_mfma_f32_32x32x16_f16 v[66:81], v[142:145], v[162:165], v[66:81]
	v_mfma_f32_32x32x16_f16 v[2:17], v[142:145], v[166:169], v[2:17]
	ds_read_b128 v[142:145], v236 offset:13120
	global_load_dwordx4 v[162:165], v239, s[56:57]
	global_load_dwordx4 v[166:169], v239, s[56:57] offset:512
	s_add_u32 s56, s56, 0x4000
	s_addc_u32 s57, s57, 0
	s_waitcnt vmcnt(16)
	s_waitcnt lgkmcnt(3)
	v_mfma_f32_32x32x16_f16 v[82:97], v[130:133], v[170:173], v[82:97]
	v_mfma_f32_32x32x16_f16 v[50:65], v[130:133], v[174:177], v[50:65]
	ds_read_b128 v[130:133], v236 offset:96
	s_waitcnt lgkmcnt(3)
	v_mfma_f32_32x32x16_f16 v[114:129], v[134:137], v[170:173], v[114:129]
	v_mfma_f32_32x32x16_f16 v[34:49], v[134:137], v[174:177], v[34:49]
	ds_read_b128 v[134:137], v236 offset:4448
	s_waitcnt lgkmcnt(3)
	v_mfma_f32_32x32x16_f16 v[98:113], v[138:141], v[170:173], v[98:113]
	v_mfma_f32_32x32x16_f16 v[18:33], v[138:141], v[174:177], v[18:33]
	ds_read_b128 v[138:141], v236 offset:8800
	s_waitcnt lgkmcnt(3)
	v_mfma_f32_32x32x16_f16 v[66:81], v[142:145], v[170:173], v[66:81]
	v_mfma_f32_32x32x16_f16 v[2:17], v[142:145], v[174:177], v[2:17]
	ds_read_b128 v[142:145], v236 offset:13152
	global_load_dwordx4 v[170:173], v239, s[56:57]
	global_load_dwordx4 v[174:177], v239, s[56:57] offset:512
	s_add_u32 s56, s56, 0x4000
	s_addc_u32 s57, s57, 0
	s_waitcnt vmcnt(8)
	s_waitcnt lgkmcnt(3)
	v_mfma_f32_32x32x16_f16 v[82:97], v[130:133], v[178:181], v[82:97]
	v_mfma_f32_32x32x16_f16 v[50:65], v[130:133], v[182:185], v[50:65]
	ds_read_b128 v[130:133], v236 offset:128
	s_waitcnt lgkmcnt(3)
	v_mfma_f32_32x32x16_f16 v[114:129], v[134:137], v[178:181], v[114:129]
	v_mfma_f32_32x32x16_f16 v[34:49], v[134:137], v[182:185], v[34:49]
	ds_read_b128 v[134:137], v236 offset:4480
	s_waitcnt lgkmcnt(3)
	v_mfma_f32_32x32x16_f16 v[98:113], v[138:141], v[178:181], v[98:113]
	v_mfma_f32_32x32x16_f16 v[18:33], v[138:141], v[182:185], v[18:33]
	ds_read_b128 v[138:141], v236 offset:8832
	s_waitcnt lgkmcnt(3)
	v_mfma_f32_32x32x16_f16 v[66:81], v[142:145], v[178:181], v[66:81]
	v_mfma_f32_32x32x16_f16 v[2:17], v[142:145], v[182:185], v[2:17]
	ds_read_b128 v[142:145], v236 offset:13184
	global_load_dwordx4 v[178:181], v239, s[56:57]
	global_load_dwordx4 v[182:185], v239, s[56:57] offset:512
	s_add_u32 s56, s56, 0x4000
	s_addc_u32 s57, s57, 0
	s_waitcnt vmcnt(8)
	s_waitcnt lgkmcnt(3)
	v_mfma_f32_32x32x16_f16 v[82:97], v[130:133], v[146:149], v[82:97]
	v_mfma_f32_32x32x16_f16 v[50:65], v[130:133], v[150:153], v[50:65]
	ds_read_b128 v[130:133], v236 offset:160
	s_waitcnt lgkmcnt(3)
	v_mfma_f32_32x32x16_f16 v[114:129], v[134:137], v[146:149], v[114:129]
	v_mfma_f32_32x32x16_f16 v[34:49], v[134:137], v[150:153], v[34:49]
	ds_read_b128 v[134:137], v236 offset:4512
	s_waitcnt lgkmcnt(3)
	v_mfma_f32_32x32x16_f16 v[98:113], v[138:141], v[146:149], v[98:113]
	v_mfma_f32_32x32x16_f16 v[18:33], v[138:141], v[150:153], v[18:33]
	ds_read_b128 v[138:141], v236 offset:8864
	s_waitcnt lgkmcnt(3)
	v_mfma_f32_32x32x16_f16 v[66:81], v[142:145], v[146:149], v[66:81]
	v_mfma_f32_32x32x16_f16 v[2:17], v[142:145], v[150:153], v[2:17]
	ds_read_b128 v[142:145], v236 offset:13216
	global_load_dwordx4 v[146:149], v239, s[56:57]
	global_load_dwordx4 v[150:153], v239, s[56:57] offset:512
	s_add_u32 s56, s56, 0x4000
	s_addc_u32 s57, s57, 0
	s_waitcnt vmcnt(8)
	s_waitcnt lgkmcnt(3)
	v_mfma_f32_32x32x16_f16 v[82:97], v[130:133], v[154:157], v[82:97]
	v_mfma_f32_32x32x16_f16 v[50:65], v[130:133], v[158:161], v[50:65]
	ds_read_b128 v[130:133], v236 offset:192
	s_waitcnt lgkmcnt(3)
	v_mfma_f32_32x32x16_f16 v[114:129], v[134:137], v[154:157], v[114:129]
	v_mfma_f32_32x32x16_f16 v[34:49], v[134:137], v[158:161], v[34:49]
	ds_read_b128 v[134:137], v236 offset:4544
	s_waitcnt lgkmcnt(3)
	v_mfma_f32_32x32x16_f16 v[98:113], v[138:141], v[154:157], v[98:113]
	v_mfma_f32_32x32x16_f16 v[18:33], v[138:141], v[158:161], v[18:33]
	ds_read_b128 v[138:141], v236 offset:8896
	s_waitcnt lgkmcnt(3)
	v_mfma_f32_32x32x16_f16 v[66:81], v[142:145], v[154:157], v[66:81]
	v_mfma_f32_32x32x16_f16 v[2:17], v[142:145], v[158:161], v[2:17]
	ds_read_b128 v[142:145], v236 offset:13248
	global_load_dwordx4 v[154:157], v239, s[56:57]
	global_load_dwordx4 v[158:161], v239, s[56:57] offset:512
	s_add_u32 s56, s56, 0x4000
	s_addc_u32 s57, s57, 0
	s_waitcnt vmcnt(23)
	v_cvt_pk_f16_f32 v204, v204, v205
	v_cvt_pk_f16_f32 v205, v206, v207
	ds_write_b64 v237, v[204:205] offset:34816
	s_waitcnt vmcnt(22)
	v_cvt_pk_f16_f32 v208, v208, v209
	v_cvt_pk_f16_f32 v209, v210, v211
	ds_write_b64 v237, v[208:209] offset:39168
	s_waitcnt vmcnt(21)
	v_cvt_pk_f16_f32 v212, v212, v213
	v_cvt_pk_f16_f32 v213, v214, v215
	ds_write_b64 v237, v[212:213] offset:43520
	s_waitcnt vmcnt(20)
	v_cvt_pk_f16_f32 v216, v216, v217
	v_cvt_pk_f16_f32 v217, v218, v219
	ds_write_b64 v237, v[216:217] offset:47872
	s_waitcnt vmcnt(19)
	v_cvt_pk_f16_f32 v220, v220, v221
	v_cvt_pk_f16_f32 v221, v222, v223
	ds_write_b64 v237, v[220:221] offset:52224
	s_waitcnt vmcnt(18)
	v_cvt_pk_f16_f32 v224, v224, v225
	v_cvt_pk_f16_f32 v225, v226, v227
	ds_write_b64 v237, v[224:225] offset:56576
	s_waitcnt vmcnt(17)
	v_cvt_pk_f16_f32 v228, v228, v229
	v_cvt_pk_f16_f32 v229, v230, v231
	ds_write_b64 v237, v[228:229] offset:60928
	s_waitcnt vmcnt(16)
	v_cvt_pk_f16_f32 v232, v232, v233
	v_cvt_pk_f16_f32 v233, v234, v235
	ds_write_b64 v237, v[232:233] offset:65280
	global_load_dwordx4 v[204:207], v238, s[40:41] offset:2048
	global_load_dwordx4 v[208:211], v238, s[42:43] offset:2048
	global_load_dwordx4 v[212:215], v238, s[44:45] offset:2048
	global_load_dwordx4 v[216:219], v238, s[46:47] offset:2048
	global_load_dwordx4 v[220:223], v238, s[48:49] offset:2048
	global_load_dwordx4 v[224:227], v238, s[50:51] offset:2048
	global_load_dwordx4 v[228:231], v238, s[52:53] offset:2048
	global_load_dwordx4 v[232:235], v238, s[54:55] offset:2048
	s_waitcnt vmcnt(16)
	s_waitcnt lgkmcnt(11)
	v_mfma_f32_32x32x16_f16 v[82:97], v[130:133], v[162:165], v[82:97]
	v_mfma_f32_32x32x16_f16 v[50:65], v[130:133], v[166:169], v[50:65]
	ds_read_b128 v[130:133], v236 offset:224
	s_waitcnt lgkmcnt(11)
	v_mfma_f32_32x32x16_f16 v[114:129], v[134:137], v[162:165], v[114:129]
	v_mfma_f32_32x32x16_f16 v[34:49], v[134:137], v[166:169], v[34:49]
	ds_read_b128 v[134:137], v236 offset:4576
	s_waitcnt lgkmcnt(11)
	v_mfma_f32_32x32x16_f16 v[98:113], v[138:141], v[162:165], v[98:113]
	v_mfma_f32_32x32x16_f16 v[18:33], v[138:141], v[166:169], v[18:33]
	ds_read_b128 v[138:141], v236 offset:8928
	s_waitcnt lgkmcnt(11)
	v_mfma_f32_32x32x16_f16 v[66:81], v[142:145], v[162:165], v[66:81]
	v_mfma_f32_32x32x16_f16 v[2:17], v[142:145], v[166:169], v[2:17]
	ds_read_b128 v[142:145], v236 offset:13280
	global_load_dwordx4 v[162:165], v239, s[56:57]
	global_load_dwordx4 v[166:169], v239, s[56:57] offset:512
	s_add_u32 s56, s56, 0x4000
	s_addc_u32 s57, s57, 0
	s_waitcnt vmcnt(16)
	s_waitcnt lgkmcnt(3)
	v_mfma_f32_32x32x16_f16 v[82:97], v[130:133], v[170:173], v[82:97]
	v_mfma_f32_32x32x16_f16 v[50:65], v[130:133], v[174:177], v[50:65]
	s_waitcnt lgkmcnt(2)
	v_mfma_f32_32x32x16_f16 v[114:129], v[134:137], v[170:173], v[114:129]
	v_mfma_f32_32x32x16_f16 v[34:49], v[134:137], v[174:177], v[34:49]
	s_waitcnt lgkmcnt(1)
	v_mfma_f32_32x32x16_f16 v[98:113], v[138:141], v[170:173], v[98:113]
	v_mfma_f32_32x32x16_f16 v[18:33], v[138:141], v[174:177], v[18:33]
	s_waitcnt lgkmcnt(0)
	v_mfma_f32_32x32x16_f16 v[66:81], v[142:145], v[170:173], v[66:81]
	v_mfma_f32_32x32x16_f16 v[2:17], v[142:145], v[174:177], v[2:17]
	global_load_dwordx4 v[170:173], v239, s[56:57]
	global_load_dwordx4 v[174:177], v239, s[56:57] offset:512
	s_add_u32 s56, s56, 0x4000
	s_addc_u32 s57, s57, 0
	s_waitcnt lgkmcnt(0)
	s_barrier
	ds_read_b128 v[130:133], v236 offset:34816
	ds_read_b128 v[134:137], v236 offset:39168
	ds_read_b128 v[138:141], v236 offset:43520
	ds_read_b128 v[142:145], v236 offset:47872
	s_waitcnt vmcnt(16)
	s_waitcnt lgkmcnt(3)
	v_mfma_f32_32x32x16_f16 v[82:97], v[130:133], v[178:181], v[82:97]
	v_mfma_f32_32x32x16_f16 v[50:65], v[130:133], v[182:185], v[50:65]
	ds_read_b128 v[130:133], v236 offset:34848
	s_waitcnt lgkmcnt(3)
	v_mfma_f32_32x32x16_f16 v[114:129], v[134:137], v[178:181], v[114:129]
	v_mfma_f32_32x32x16_f16 v[34:49], v[134:137], v[182:185], v[34:49]
	ds_read_b128 v[134:137], v236 offset:39200
	s_waitcnt lgkmcnt(3)
	v_mfma_f32_32x32x16_f16 v[98:113], v[138:141], v[178:181], v[98:113]
	v_mfma_f32_32x32x16_f16 v[18:33], v[138:141], v[182:185], v[18:33]
	ds_read_b128 v[138:141], v236 offset:43552
	s_waitcnt lgkmcnt(3)
	v_mfma_f32_32x32x16_f16 v[66:81], v[142:145], v[178:181], v[66:81]
	v_mfma_f32_32x32x16_f16 v[2:17], v[142:145], v[182:185], v[2:17]
	ds_read_b128 v[142:145], v236 offset:47904
	global_load_dwordx4 v[178:181], v239, s[56:57]
	global_load_dwordx4 v[182:185], v239, s[56:57] offset:512
	s_add_u32 s56, s56, 0x4000
	s_addc_u32 s57, s57, 0
	s_waitcnt vmcnt(16)
	s_waitcnt lgkmcnt(3)
	v_mfma_f32_32x32x16_f16 v[82:97], v[130:133], v[146:149], v[82:97]
	v_mfma_f32_32x32x16_f16 v[50:65], v[130:133], v[150:153], v[50:65]
	ds_read_b128 v[130:133], v236 offset:34880
	s_waitcnt lgkmcnt(3)
	v_mfma_f32_32x32x16_f16 v[114:129], v[134:137], v[146:149], v[114:129]
	v_mfma_f32_32x32x16_f16 v[34:49], v[134:137], v[150:153], v[34:49]
	ds_read_b128 v[134:137], v236 offset:39232
	s_waitcnt lgkmcnt(3)
	v_mfma_f32_32x32x16_f16 v[98:113], v[138:141], v[146:149], v[98:113]
	v_mfma_f32_32x32x16_f16 v[18:33], v[138:141], v[150:153], v[18:33]
	ds_read_b128 v[138:141], v236 offset:43584
	s_waitcnt lgkmcnt(3)
	v_mfma_f32_32x32x16_f16 v[66:81], v[142:145], v[146:149], v[66:81]
	v_mfma_f32_32x32x16_f16 v[2:17], v[142:145], v[150:153], v[2:17]
	ds_read_b128 v[142:145], v236 offset:47936
	global_load_dwordx4 v[146:149], v239, s[56:57]
	global_load_dwordx4 v[150:153], v239, s[56:57] offset:512
	s_add_u32 s56, s56, 0x4000
	s_addc_u32 s57, s57, 0
	s_waitcnt vmcnt(16)
	s_waitcnt lgkmcnt(3)
	v_mfma_f32_32x32x16_f16 v[82:97], v[130:133], v[154:157], v[82:97]
	v_mfma_f32_32x32x16_f16 v[50:65], v[130:133], v[158:161], v[50:65]
	ds_read_b128 v[130:133], v236 offset:34912
	s_waitcnt lgkmcnt(3)
	v_mfma_f32_32x32x16_f16 v[114:129], v[134:137], v[154:157], v[114:129]
	v_mfma_f32_32x32x16_f16 v[34:49], v[134:137], v[158:161], v[34:49]
	ds_read_b128 v[134:137], v236 offset:39264
	s_waitcnt lgkmcnt(3)
	v_mfma_f32_32x32x16_f16 v[98:113], v[138:141], v[154:157], v[98:113]
	v_mfma_f32_32x32x16_f16 v[18:33], v[138:141], v[158:161], v[18:33]
	ds_read_b128 v[138:141], v236 offset:43616
	s_waitcnt lgkmcnt(3)
	v_mfma_f32_32x32x16_f16 v[66:81], v[142:145], v[154:157], v[66:81]
	v_mfma_f32_32x32x16_f16 v[2:17], v[142:145], v[158:161], v[2:17]
	ds_read_b128 v[142:145], v236 offset:47968
	global_load_dwordx4 v[154:157], v239, s[56:57]
	global_load_dwordx4 v[158:161], v239, s[56:57] offset:512
	s_add_u32 s56, s56, 0x4000
	s_addc_u32 s57, s57, 0
	s_waitcnt vmcnt(8)
	s_waitcnt lgkmcnt(3)
	v_mfma_f32_32x32x16_f16 v[82:97], v[130:133], v[162:165], v[82:97]
	v_mfma_f32_32x32x16_f16 v[50:65], v[130:133], v[166:169], v[50:65]
	ds_read_b128 v[130:133], v236 offset:34944
	s_waitcnt lgkmcnt(3)
	v_mfma_f32_32x32x16_f16 v[114:129], v[134:137], v[162:165], v[114:129]
	v_mfma_f32_32x32x16_f16 v[34:49], v[134:137], v[166:169], v[34:49]
	ds_read_b128 v[134:137], v236 offset:39296
	s_waitcnt lgkmcnt(3)
	v_mfma_f32_32x32x16_f16 v[98:113], v[138:141], v[162:165], v[98:113]
	v_mfma_f32_32x32x16_f16 v[18:33], v[138:141], v[166:169], v[18:33]
	ds_read_b128 v[138:141], v236 offset:43648
	s_waitcnt lgkmcnt(3)
	v_mfma_f32_32x32x16_f16 v[66:81], v[142:145], v[162:165], v[66:81]
	v_mfma_f32_32x32x16_f16 v[2:17], v[142:145], v[166:169], v[2:17]
	ds_read_b128 v[142:145], v236 offset:48000
	global_load_dwordx4 v[162:165], v239, s[56:57]
	global_load_dwordx4 v[166:169], v239, s[56:57] offset:512
	s_add_u32 s56, s56, 0x4000
	s_addc_u32 s57, s57, 0
	s_waitcnt vmcnt(8)
	s_waitcnt lgkmcnt(3)
	v_mfma_f32_32x32x16_f16 v[82:97], v[130:133], v[170:173], v[82:97]
	v_mfma_f32_32x32x16_f16 v[50:65], v[130:133], v[174:177], v[50:65]
	ds_read_b128 v[130:133], v236 offset:34976
	s_waitcnt lgkmcnt(3)
	v_mfma_f32_32x32x16_f16 v[114:129], v[134:137], v[170:173], v[114:129]
	v_mfma_f32_32x32x16_f16 v[34:49], v[134:137], v[174:177], v[34:49]
	ds_read_b128 v[134:137], v236 offset:39328
	s_waitcnt lgkmcnt(3)
	v_mfma_f32_32x32x16_f16 v[98:113], v[138:141], v[170:173], v[98:113]
	v_mfma_f32_32x32x16_f16 v[18:33], v[138:141], v[174:177], v[18:33]
	ds_read_b128 v[138:141], v236 offset:43680
	s_waitcnt lgkmcnt(3)
	v_mfma_f32_32x32x16_f16 v[66:81], v[142:145], v[170:173], v[66:81]
	v_mfma_f32_32x32x16_f16 v[2:17], v[142:145], v[174:177], v[2:17]
	ds_read_b128 v[142:145], v236 offset:48032
	global_load_dwordx4 v[170:173], v239, s[56:57]
	global_load_dwordx4 v[174:177], v239, s[56:57] offset:512
	s_add_u32 s56, s56, 0x4000
	s_addc_u32 s57, s57, 0
	s_waitcnt vmcnt(8)
	s_waitcnt lgkmcnt(3)
	v_mfma_f32_32x32x16_f16 v[82:97], v[130:133], v[178:181], v[82:97]
	v_mfma_f32_32x32x16_f16 v[50:65], v[130:133], v[182:185], v[50:65]
	ds_read_b128 v[130:133], v236 offset:35008
	s_waitcnt lgkmcnt(3)
	v_mfma_f32_32x32x16_f16 v[114:129], v[134:137], v[178:181], v[114:129]
	v_mfma_f32_32x32x16_f16 v[34:49], v[134:137], v[182:185], v[34:49]
	ds_read_b128 v[134:137], v236 offset:39360
	s_waitcnt lgkmcnt(3)
	v_mfma_f32_32x32x16_f16 v[98:113], v[138:141], v[178:181], v[98:113]
	v_mfma_f32_32x32x16_f16 v[18:33], v[138:141], v[182:185], v[18:33]
	ds_read_b128 v[138:141], v236 offset:43712
	s_waitcnt lgkmcnt(3)
	v_mfma_f32_32x32x16_f16 v[66:81], v[142:145], v[178:181], v[66:81]
	v_mfma_f32_32x32x16_f16 v[2:17], v[142:145], v[182:185], v[2:17]
	ds_read_b128 v[142:145], v236 offset:48064
	global_load_dwordx4 v[178:181], v239, s[56:57]
	global_load_dwordx4 v[182:185], v239, s[56:57] offset:512
	s_add_u32 s56, s56, 0x4000
	s_addc_u32 s57, s57, 0
	s_waitcnt vmcnt(23)
	v_cvt_pk_f16_f32 v204, v204, v205
	v_cvt_pk_f16_f32 v205, v206, v207
	ds_write_b64 v237, v[204:205]
	s_waitcnt vmcnt(22)
	v_cvt_pk_f16_f32 v208, v208, v209
	v_cvt_pk_f16_f32 v209, v210, v211
	ds_write_b64 v237, v[208:209] offset:4352
	s_waitcnt vmcnt(21)
	v_cvt_pk_f16_f32 v212, v212, v213
	v_cvt_pk_f16_f32 v213, v214, v215
	ds_write_b64 v237, v[212:213] offset:8704
	s_waitcnt vmcnt(20)
	v_cvt_pk_f16_f32 v216, v216, v217
	v_cvt_pk_f16_f32 v217, v218, v219
	ds_write_b64 v237, v[216:217] offset:13056
	s_waitcnt vmcnt(19)
	v_cvt_pk_f16_f32 v220, v220, v221
	v_cvt_pk_f16_f32 v221, v222, v223
	ds_write_b64 v237, v[220:221] offset:17408
	s_waitcnt vmcnt(18)
	v_cvt_pk_f16_f32 v224, v224, v225
	v_cvt_pk_f16_f32 v225, v226, v227
	ds_write_b64 v237, v[224:225] offset:21760
	s_waitcnt vmcnt(17)
	v_cvt_pk_f16_f32 v228, v228, v229
	v_cvt_pk_f16_f32 v229, v230, v231
	ds_write_b64 v237, v[228:229] offset:26112
	s_waitcnt vmcnt(16)
	v_cvt_pk_f16_f32 v232, v232, v233
	v_cvt_pk_f16_f32 v233, v234, v235
	ds_write_b64 v237, v[232:233] offset:30464
	global_load_dwordx4 v[204:207], v238, s[40:41] offset:2560
	global_load_dwordx4 v[208:211], v238, s[42:43] offset:2560
	global_load_dwordx4 v[212:215], v238, s[44:45] offset:2560
	global_load_dwordx4 v[216:219], v238, s[46:47] offset:2560
	global_load_dwordx4 v[220:223], v238, s[48:49] offset:2560
	global_load_dwordx4 v[224:227], v238, s[50:51] offset:2560
	global_load_dwordx4 v[228:231], v238, s[52:53] offset:2560
	global_load_dwordx4 v[232:235], v238, s[54:55] offset:2560
	s_waitcnt vmcnt(16)
	s_waitcnt lgkmcnt(11)
	v_mfma_f32_32x32x16_f16 v[82:97], v[130:133], v[146:149], v[82:97]
	v_mfma_f32_32x32x16_f16 v[50:65], v[130:133], v[150:153], v[50:65]
	ds_read_b128 v[130:133], v236 offset:35040
	s_waitcnt lgkmcnt(11)
	v_mfma_f32_32x32x16_f16 v[114:129], v[134:137], v[146:149], v[114:129]
	v_mfma_f32_32x32x16_f16 v[34:49], v[134:137], v[150:153], v[34:49]
	ds_read_b128 v[134:137], v236 offset:39392
	s_waitcnt lgkmcnt(11)
	v_mfma_f32_32x32x16_f16 v[98:113], v[138:141], v[146:149], v[98:113]
	v_mfma_f32_32x32x16_f16 v[18:33], v[138:141], v[150:153], v[18:33]
	ds_read_b128 v[138:141], v236 offset:43744
	s_waitcnt lgkmcnt(11)
	v_mfma_f32_32x32x16_f16 v[66:81], v[142:145], v[146:149], v[66:81]
	v_mfma_f32_32x32x16_f16 v[2:17], v[142:145], v[150:153], v[2:17]
	ds_read_b128 v[142:145], v236 offset:48096
	global_load_dwordx4 v[146:149], v239, s[56:57]
	global_load_dwordx4 v[150:153], v239, s[56:57] offset:512
	s_add_u32 s56, s56, 0x4000
	s_addc_u32 s57, s57, 0
	s_waitcnt vmcnt(16)
	s_waitcnt lgkmcnt(3)
	v_mfma_f32_32x32x16_f16 v[82:97], v[130:133], v[154:157], v[82:97]
	v_mfma_f32_32x32x16_f16 v[50:65], v[130:133], v[158:161], v[50:65]
	s_waitcnt lgkmcnt(2)
	v_mfma_f32_32x32x16_f16 v[114:129], v[134:137], v[154:157], v[114:129]
	v_mfma_f32_32x32x16_f16 v[34:49], v[134:137], v[158:161], v[34:49]
	s_waitcnt lgkmcnt(1)
	v_mfma_f32_32x32x16_f16 v[98:113], v[138:141], v[154:157], v[98:113]
	v_mfma_f32_32x32x16_f16 v[18:33], v[138:141], v[158:161], v[18:33]
	s_waitcnt lgkmcnt(0)
	v_mfma_f32_32x32x16_f16 v[66:81], v[142:145], v[154:157], v[66:81]
	v_mfma_f32_32x32x16_f16 v[2:17], v[142:145], v[158:161], v[2:17]
	global_load_dwordx4 v[154:157], v239, s[56:57]
	global_load_dwordx4 v[158:161], v239, s[56:57] offset:512
	s_add_u32 s56, s56, 0x4000
	s_addc_u32 s57, s57, 0
	s_waitcnt lgkmcnt(0)
	s_barrier
	ds_read_b128 v[130:133], v236
	ds_read_b128 v[134:137], v236 offset:4352
	ds_read_b128 v[138:141], v236 offset:8704
	ds_read_b128 v[142:145], v236 offset:13056
	s_waitcnt vmcnt(16)
	s_waitcnt lgkmcnt(3)
	v_mfma_f32_32x32x16_f16 v[82:97], v[130:133], v[162:165], v[82:97]
	v_mfma_f32_32x32x16_f16 v[50:65], v[130:133], v[166:169], v[50:65]
	ds_read_b128 v[130:133], v236 offset:32
	s_waitcnt lgkmcnt(3)
	v_mfma_f32_32x32x16_f16 v[114:129], v[134:137], v[162:165], v[114:129]
	v_mfma_f32_32x32x16_f16 v[34:49], v[134:137], v[166:169], v[34:49]
	ds_read_b128 v[134:137], v236 offset:4384
	s_waitcnt lgkmcnt(3)
	v_mfma_f32_32x32x16_f16 v[98:113], v[138:141], v[162:165], v[98:113]
	v_mfma_f32_32x32x16_f16 v[18:33], v[138:141], v[166:169], v[18:33]
	ds_read_b128 v[138:141], v236 offset:8736
	s_waitcnt lgkmcnt(3)
	v_mfma_f32_32x32x16_f16 v[66:81], v[142:145], v[162:165], v[66:81]
	v_mfma_f32_32x32x16_f16 v[2:17], v[142:145], v[166:169], v[2:17]
	ds_read_b128 v[142:145], v236 offset:13088
	global_load_dwordx4 v[162:165], v239, s[56:57]
	global_load_dwordx4 v[166:169], v239, s[56:57] offset:512
	s_add_u32 s56, s56, 0x4000
	s_addc_u32 s57, s57, 0
	s_waitcnt vmcnt(16)
	s_waitcnt lgkmcnt(3)
	v_mfma_f32_32x32x16_f16 v[82:97], v[130:133], v[170:173], v[82:97]
	v_mfma_f32_32x32x16_f16 v[50:65], v[130:133], v[174:177], v[50:65]
	ds_read_b128 v[130:133], v236 offset:64
	s_waitcnt lgkmcnt(3)
	v_mfma_f32_32x32x16_f16 v[114:129], v[134:137], v[170:173], v[114:129]
	v_mfma_f32_32x32x16_f16 v[34:49], v[134:137], v[174:177], v[34:49]
	ds_read_b128 v[134:137], v236 offset:4416
	s_waitcnt lgkmcnt(3)
	v_mfma_f32_32x32x16_f16 v[98:113], v[138:141], v[170:173], v[98:113]
	v_mfma_f32_32x32x16_f16 v[18:33], v[138:141], v[174:177], v[18:33]
	ds_read_b128 v[138:141], v236 offset:8768
	s_waitcnt lgkmcnt(3)
	v_mfma_f32_32x32x16_f16 v[66:81], v[142:145], v[170:173], v[66:81]
	v_mfma_f32_32x32x16_f16 v[2:17], v[142:145], v[174:177], v[2:17]
	ds_read_b128 v[142:145], v236 offset:13120
	global_load_dwordx4 v[170:173], v239, s[56:57]
	global_load_dwordx4 v[174:177], v239, s[56:57] offset:512
	s_add_u32 s56, s56, 0x4000
	s_addc_u32 s57, s57, 0
	s_waitcnt vmcnt(16)
	s_waitcnt lgkmcnt(3)
	v_mfma_f32_32x32x16_f16 v[82:97], v[130:133], v[178:181], v[82:97]
	v_mfma_f32_32x32x16_f16 v[50:65], v[130:133], v[182:185], v[50:65]
	ds_read_b128 v[130:133], v236 offset:96
	s_waitcnt lgkmcnt(3)
	v_mfma_f32_32x32x16_f16 v[114:129], v[134:137], v[178:181], v[114:129]
	v_mfma_f32_32x32x16_f16 v[34:49], v[134:137], v[182:185], v[34:49]
	ds_read_b128 v[134:137], v236 offset:4448
	s_waitcnt lgkmcnt(3)
	v_mfma_f32_32x32x16_f16 v[98:113], v[138:141], v[178:181], v[98:113]
	v_mfma_f32_32x32x16_f16 v[18:33], v[138:141], v[182:185], v[18:33]
	ds_read_b128 v[138:141], v236 offset:8800
	s_waitcnt lgkmcnt(3)
	v_mfma_f32_32x32x16_f16 v[66:81], v[142:145], v[178:181], v[66:81]
	v_mfma_f32_32x32x16_f16 v[2:17], v[142:145], v[182:185], v[2:17]
	ds_read_b128 v[142:145], v236 offset:13152
	global_load_dwordx4 v[178:181], v239, s[56:57]
	global_load_dwordx4 v[182:185], v239, s[56:57] offset:512
	s_add_u32 s56, s56, 0x4000
	s_addc_u32 s57, s57, 0
	s_waitcnt vmcnt(8)
	s_waitcnt lgkmcnt(3)
	v_mfma_f32_32x32x16_f16 v[82:97], v[130:133], v[146:149], v[82:97]
	v_mfma_f32_32x32x16_f16 v[50:65], v[130:133], v[150:153], v[50:65]
	ds_read_b128 v[130:133], v236 offset:128
	s_waitcnt lgkmcnt(3)
	v_mfma_f32_32x32x16_f16 v[114:129], v[134:137], v[146:149], v[114:129]
	v_mfma_f32_32x32x16_f16 v[34:49], v[134:137], v[150:153], v[34:49]
	ds_read_b128 v[134:137], v236 offset:4480
	s_waitcnt lgkmcnt(3)
	v_mfma_f32_32x32x16_f16 v[98:113], v[138:141], v[146:149], v[98:113]
	v_mfma_f32_32x32x16_f16 v[18:33], v[138:141], v[150:153], v[18:33]
	ds_read_b128 v[138:141], v236 offset:8832
	s_waitcnt lgkmcnt(3)
	v_mfma_f32_32x32x16_f16 v[66:81], v[142:145], v[146:149], v[66:81]
	v_mfma_f32_32x32x16_f16 v[2:17], v[142:145], v[150:153], v[2:17]
	ds_read_b128 v[142:145], v236 offset:13184
	global_load_dwordx4 v[146:149], v239, s[56:57]
	global_load_dwordx4 v[150:153], v239, s[56:57] offset:512
	s_add_u32 s56, s56, 0x4000
	s_addc_u32 s57, s57, 0
	s_waitcnt vmcnt(8)
	s_waitcnt lgkmcnt(3)
	v_mfma_f32_32x32x16_f16 v[82:97], v[130:133], v[154:157], v[82:97]
	v_mfma_f32_32x32x16_f16 v[50:65], v[130:133], v[158:161], v[50:65]
	ds_read_b128 v[130:133], v236 offset:160
	s_waitcnt lgkmcnt(3)
	v_mfma_f32_32x32x16_f16 v[114:129], v[134:137], v[154:157], v[114:129]
	v_mfma_f32_32x32x16_f16 v[34:49], v[134:137], v[158:161], v[34:49]
	ds_read_b128 v[134:137], v236 offset:4512
	s_waitcnt lgkmcnt(3)
	v_mfma_f32_32x32x16_f16 v[98:113], v[138:141], v[154:157], v[98:113]
	v_mfma_f32_32x32x16_f16 v[18:33], v[138:141], v[158:161], v[18:33]
	ds_read_b128 v[138:141], v236 offset:8864
	s_waitcnt lgkmcnt(3)
	v_mfma_f32_32x32x16_f16 v[66:81], v[142:145], v[154:157], v[66:81]
	v_mfma_f32_32x32x16_f16 v[2:17], v[142:145], v[158:161], v[2:17]
	ds_read_b128 v[142:145], v236 offset:13216
	global_load_dwordx4 v[154:157], v239, s[56:57]
	global_load_dwordx4 v[158:161], v239, s[56:57] offset:512
	s_add_u32 s56, s56, 0x4000
	s_addc_u32 s57, s57, 0
	s_waitcnt vmcnt(8)
	s_waitcnt lgkmcnt(3)
	v_mfma_f32_32x32x16_f16 v[82:97], v[130:133], v[162:165], v[82:97]
	v_mfma_f32_32x32x16_f16 v[50:65], v[130:133], v[166:169], v[50:65]
	ds_read_b128 v[130:133], v236 offset:192
	s_waitcnt lgkmcnt(3)
	v_mfma_f32_32x32x16_f16 v[114:129], v[134:137], v[162:165], v[114:129]
	v_mfma_f32_32x32x16_f16 v[34:49], v[134:137], v[166:169], v[34:49]
	ds_read_b128 v[134:137], v236 offset:4544
	s_waitcnt lgkmcnt(3)
	v_mfma_f32_32x32x16_f16 v[98:113], v[138:141], v[162:165], v[98:113]
	v_mfma_f32_32x32x16_f16 v[18:33], v[138:141], v[166:169], v[18:33]
	ds_read_b128 v[138:141], v236 offset:8896
	s_waitcnt lgkmcnt(3)
	v_mfma_f32_32x32x16_f16 v[66:81], v[142:145], v[162:165], v[66:81]
	v_mfma_f32_32x32x16_f16 v[2:17], v[142:145], v[166:169], v[2:17]
	ds_read_b128 v[142:145], v236 offset:13248
	global_load_dwordx4 v[162:165], v239, s[56:57]
	global_load_dwordx4 v[166:169], v239, s[56:57] offset:512
	s_add_u32 s56, s56, 0x4000
	s_addc_u32 s57, s57, 0
	s_waitcnt vmcnt(23)
	v_cvt_pk_f16_f32 v204, v204, v205
	v_cvt_pk_f16_f32 v205, v206, v207
	ds_write_b64 v237, v[204:205] offset:34816
	s_waitcnt vmcnt(22)
	v_cvt_pk_f16_f32 v208, v208, v209
	v_cvt_pk_f16_f32 v209, v210, v211
	ds_write_b64 v237, v[208:209] offset:39168
	s_waitcnt vmcnt(21)
	v_cvt_pk_f16_f32 v212, v212, v213
	v_cvt_pk_f16_f32 v213, v214, v215
	ds_write_b64 v237, v[212:213] offset:43520
	s_waitcnt vmcnt(20)
	v_cvt_pk_f16_f32 v216, v216, v217
	v_cvt_pk_f16_f32 v217, v218, v219
	ds_write_b64 v237, v[216:217] offset:47872
	s_waitcnt vmcnt(19)
	v_cvt_pk_f16_f32 v220, v220, v221
	v_cvt_pk_f16_f32 v221, v222, v223
	ds_write_b64 v237, v[220:221] offset:52224
	s_waitcnt vmcnt(18)
	v_cvt_pk_f16_f32 v224, v224, v225
	v_cvt_pk_f16_f32 v225, v226, v227
	ds_write_b64 v237, v[224:225] offset:56576
	s_waitcnt vmcnt(17)
	v_cvt_pk_f16_f32 v228, v228, v229
	v_cvt_pk_f16_f32 v229, v230, v231
	ds_write_b64 v237, v[228:229] offset:60928
	s_waitcnt vmcnt(16)
	v_cvt_pk_f16_f32 v232, v232, v233
	v_cvt_pk_f16_f32 v233, v234, v235
	ds_write_b64 v237, v[232:233] offset:65280
	global_load_dwordx4 v[204:207], v238, s[40:41] offset:3072
	global_load_dwordx4 v[208:211], v238, s[42:43] offset:3072
	global_load_dwordx4 v[212:215], v238, s[44:45] offset:3072
	global_load_dwordx4 v[216:219], v238, s[46:47] offset:3072
	global_load_dwordx4 v[220:223], v238, s[48:49] offset:3072
	global_load_dwordx4 v[224:227], v238, s[50:51] offset:3072
	global_load_dwordx4 v[228:231], v238, s[52:53] offset:3072
	global_load_dwordx4 v[232:235], v238, s[54:55] offset:3072
	s_waitcnt vmcnt(16)
	s_waitcnt lgkmcnt(11)
	v_mfma_f32_32x32x16_f16 v[82:97], v[130:133], v[170:173], v[82:97]
	v_mfma_f32_32x32x16_f16 v[50:65], v[130:133], v[174:177], v[50:65]
	ds_read_b128 v[130:133], v236 offset:224
	s_waitcnt lgkmcnt(11)
	v_mfma_f32_32x32x16_f16 v[114:129], v[134:137], v[170:173], v[114:129]
	v_mfma_f32_32x32x16_f16 v[34:49], v[134:137], v[174:177], v[34:49]
	ds_read_b128 v[134:137], v236 offset:4576
	s_waitcnt lgkmcnt(11)
	v_mfma_f32_32x32x16_f16 v[98:113], v[138:141], v[170:173], v[98:113]
	v_mfma_f32_32x32x16_f16 v[18:33], v[138:141], v[174:177], v[18:33]
	ds_read_b128 v[138:141], v236 offset:8928
	s_waitcnt lgkmcnt(11)
	v_mfma_f32_32x32x16_f16 v[66:81], v[142:145], v[170:173], v[66:81]
	v_mfma_f32_32x32x16_f16 v[2:17], v[142:145], v[174:177], v[2:17]
	ds_read_b128 v[142:145], v236 offset:13280
	global_load_dwordx4 v[170:173], v239, s[56:57]
	global_load_dwordx4 v[174:177], v239, s[56:57] offset:512
	s_add_u32 s56, s56, 0x4000
	s_addc_u32 s57, s57, 0
	s_waitcnt vmcnt(16)
	s_waitcnt lgkmcnt(3)
	v_mfma_f32_32x32x16_f16 v[82:97], v[130:133], v[178:181], v[82:97]
	v_mfma_f32_32x32x16_f16 v[50:65], v[130:133], v[182:185], v[50:65]
	s_waitcnt lgkmcnt(2)
	v_mfma_f32_32x32x16_f16 v[114:129], v[134:137], v[178:181], v[114:129]
	v_mfma_f32_32x32x16_f16 v[34:49], v[134:137], v[182:185], v[34:49]
	s_waitcnt lgkmcnt(1)
	v_mfma_f32_32x32x16_f16 v[98:113], v[138:141], v[178:181], v[98:113]
	v_mfma_f32_32x32x16_f16 v[18:33], v[138:141], v[182:185], v[18:33]
	s_waitcnt lgkmcnt(0)
	v_mfma_f32_32x32x16_f16 v[66:81], v[142:145], v[178:181], v[66:81]
	v_mfma_f32_32x32x16_f16 v[2:17], v[142:145], v[182:185], v[2:17]
	global_load_dwordx4 v[178:181], v239, s[56:57]
	global_load_dwordx4 v[182:185], v239, s[56:57] offset:512
	s_add_u32 s56, s56, 0x4000
	s_addc_u32 s57, s57, 0
	s_waitcnt lgkmcnt(0)
	s_barrier
	ds_read_b128 v[130:133], v236 offset:34816
	ds_read_b128 v[134:137], v236 offset:39168
	ds_read_b128 v[138:141], v236 offset:43520
	ds_read_b128 v[142:145], v236 offset:47872
	s_waitcnt vmcnt(16)
	s_waitcnt lgkmcnt(3)
	v_mfma_f32_32x32x16_f16 v[82:97], v[130:133], v[146:149], v[82:97]
	v_mfma_f32_32x32x16_f16 v[50:65], v[130:133], v[150:153], v[50:65]
	ds_read_b128 v[130:133], v236 offset:34848
	s_waitcnt lgkmcnt(3)
	v_mfma_f32_32x32x16_f16 v[114:129], v[134:137], v[146:149], v[114:129]
	v_mfma_f32_32x32x16_f16 v[34:49], v[134:137], v[150:153], v[34:49]
	ds_read_b128 v[134:137], v236 offset:39200
	s_waitcnt lgkmcnt(3)
	v_mfma_f32_32x32x16_f16 v[98:113], v[138:141], v[146:149], v[98:113]
	v_mfma_f32_32x32x16_f16 v[18:33], v[138:141], v[150:153], v[18:33]
	ds_read_b128 v[138:141], v236 offset:43552
	s_waitcnt lgkmcnt(3)
	v_mfma_f32_32x32x16_f16 v[66:81], v[142:145], v[146:149], v[66:81]
	v_mfma_f32_32x32x16_f16 v[2:17], v[142:145], v[150:153], v[2:17]
	ds_read_b128 v[142:145], v236 offset:47904
	global_load_dwordx4 v[146:149], v239, s[56:57]
	global_load_dwordx4 v[150:153], v239, s[56:57] offset:512
	s_add_u32 s56, s56, 0x4000
	s_addc_u32 s57, s57, 0
	s_waitcnt vmcnt(16)
	s_waitcnt lgkmcnt(3)
	v_mfma_f32_32x32x16_f16 v[82:97], v[130:133], v[154:157], v[82:97]
	v_mfma_f32_32x32x16_f16 v[50:65], v[130:133], v[158:161], v[50:65]
	ds_read_b128 v[130:133], v236 offset:34880
	s_waitcnt lgkmcnt(3)
	v_mfma_f32_32x32x16_f16 v[114:129], v[134:137], v[154:157], v[114:129]
	v_mfma_f32_32x32x16_f16 v[34:49], v[134:137], v[158:161], v[34:49]
	ds_read_b128 v[134:137], v236 offset:39232
	s_waitcnt lgkmcnt(3)
	v_mfma_f32_32x32x16_f16 v[98:113], v[138:141], v[154:157], v[98:113]
	v_mfma_f32_32x32x16_f16 v[18:33], v[138:141], v[158:161], v[18:33]
	ds_read_b128 v[138:141], v236 offset:43584
	s_waitcnt lgkmcnt(3)
	v_mfma_f32_32x32x16_f16 v[66:81], v[142:145], v[154:157], v[66:81]
	v_mfma_f32_32x32x16_f16 v[2:17], v[142:145], v[158:161], v[2:17]
	ds_read_b128 v[142:145], v236 offset:47936
	global_load_dwordx4 v[154:157], v239, s[56:57]
	global_load_dwordx4 v[158:161], v239, s[56:57] offset:512
	s_add_u32 s56, s56, 0x4000
	s_addc_u32 s57, s57, 0
	s_waitcnt vmcnt(16)
	s_waitcnt lgkmcnt(3)
	v_mfma_f32_32x32x16_f16 v[82:97], v[130:133], v[162:165], v[82:97]
	v_mfma_f32_32x32x16_f16 v[50:65], v[130:133], v[166:169], v[50:65]
	ds_read_b128 v[130:133], v236 offset:34912
	s_waitcnt lgkmcnt(3)
	v_mfma_f32_32x32x16_f16 v[114:129], v[134:137], v[162:165], v[114:129]
	v_mfma_f32_32x32x16_f16 v[34:49], v[134:137], v[166:169], v[34:49]
	ds_read_b128 v[134:137], v236 offset:39264
	s_waitcnt lgkmcnt(3)
	v_mfma_f32_32x32x16_f16 v[98:113], v[138:141], v[162:165], v[98:113]
	v_mfma_f32_32x32x16_f16 v[18:33], v[138:141], v[166:169], v[18:33]
	ds_read_b128 v[138:141], v236 offset:43616
	s_waitcnt lgkmcnt(3)
	v_mfma_f32_32x32x16_f16 v[66:81], v[142:145], v[162:165], v[66:81]
	v_mfma_f32_32x32x16_f16 v[2:17], v[142:145], v[166:169], v[2:17]
	ds_read_b128 v[142:145], v236 offset:47968
	global_load_dwordx4 v[162:165], v239, s[56:57]
	global_load_dwordx4 v[166:169], v239, s[56:57] offset:512
	s_add_u32 s56, s56, 0x4000
	s_addc_u32 s57, s57, 0
	s_waitcnt vmcnt(8)
	s_waitcnt lgkmcnt(3)
	v_mfma_f32_32x32x16_f16 v[82:97], v[130:133], v[170:173], v[82:97]
	v_mfma_f32_32x32x16_f16 v[50:65], v[130:133], v[174:177], v[50:65]
	ds_read_b128 v[130:133], v236 offset:34944
	s_waitcnt lgkmcnt(3)
	v_mfma_f32_32x32x16_f16 v[114:129], v[134:137], v[170:173], v[114:129]
	v_mfma_f32_32x32x16_f16 v[34:49], v[134:137], v[174:177], v[34:49]
	ds_read_b128 v[134:137], v236 offset:39296
	s_waitcnt lgkmcnt(3)
	v_mfma_f32_32x32x16_f16 v[98:113], v[138:141], v[170:173], v[98:113]
	v_mfma_f32_32x32x16_f16 v[18:33], v[138:141], v[174:177], v[18:33]
	ds_read_b128 v[138:141], v236 offset:43648
	s_waitcnt lgkmcnt(3)
	v_mfma_f32_32x32x16_f16 v[66:81], v[142:145], v[170:173], v[66:81]
	v_mfma_f32_32x32x16_f16 v[2:17], v[142:145], v[174:177], v[2:17]
	ds_read_b128 v[142:145], v236 offset:48000
	global_load_dwordx4 v[170:173], v239, s[56:57]
	global_load_dwordx4 v[174:177], v239, s[56:57] offset:512
	s_add_u32 s56, s56, 0x4000
	s_addc_u32 s57, s57, 0
	s_waitcnt vmcnt(8)
	s_waitcnt lgkmcnt(3)
	v_mfma_f32_32x32x16_f16 v[82:97], v[130:133], v[178:181], v[82:97]
	v_mfma_f32_32x32x16_f16 v[50:65], v[130:133], v[182:185], v[50:65]
	ds_read_b128 v[130:133], v236 offset:34976
	s_waitcnt lgkmcnt(3)
	v_mfma_f32_32x32x16_f16 v[114:129], v[134:137], v[178:181], v[114:129]
	v_mfma_f32_32x32x16_f16 v[34:49], v[134:137], v[182:185], v[34:49]
	ds_read_b128 v[134:137], v236 offset:39328
	s_waitcnt lgkmcnt(3)
	v_mfma_f32_32x32x16_f16 v[98:113], v[138:141], v[178:181], v[98:113]
	v_mfma_f32_32x32x16_f16 v[18:33], v[138:141], v[182:185], v[18:33]
	ds_read_b128 v[138:141], v236 offset:43680
	s_waitcnt lgkmcnt(3)
	v_mfma_f32_32x32x16_f16 v[66:81], v[142:145], v[178:181], v[66:81]
	v_mfma_f32_32x32x16_f16 v[2:17], v[142:145], v[182:185], v[2:17]
	ds_read_b128 v[142:145], v236 offset:48032
	global_load_dwordx4 v[178:181], v239, s[56:57]
	global_load_dwordx4 v[182:185], v239, s[56:57] offset:512
	s_add_u32 s56, s56, 0x4000
	s_addc_u32 s57, s57, 0
	s_waitcnt vmcnt(8)
	s_waitcnt lgkmcnt(3)
	v_mfma_f32_32x32x16_f16 v[82:97], v[130:133], v[146:149], v[82:97]
	v_mfma_f32_32x32x16_f16 v[50:65], v[130:133], v[150:153], v[50:65]
	ds_read_b128 v[130:133], v236 offset:35008
	s_waitcnt lgkmcnt(3)
	v_mfma_f32_32x32x16_f16 v[114:129], v[134:137], v[146:149], v[114:129]
	v_mfma_f32_32x32x16_f16 v[34:49], v[134:137], v[150:153], v[34:49]
	ds_read_b128 v[134:137], v236 offset:39360
	s_waitcnt lgkmcnt(3)
	v_mfma_f32_32x32x16_f16 v[98:113], v[138:141], v[146:149], v[98:113]
	v_mfma_f32_32x32x16_f16 v[18:33], v[138:141], v[150:153], v[18:33]
	ds_read_b128 v[138:141], v236 offset:43712
	s_waitcnt lgkmcnt(3)
	v_mfma_f32_32x32x16_f16 v[66:81], v[142:145], v[146:149], v[66:81]
	v_mfma_f32_32x32x16_f16 v[2:17], v[142:145], v[150:153], v[2:17]
	ds_read_b128 v[142:145], v236 offset:48064
	global_load_dwordx4 v[146:149], v239, s[56:57]
	global_load_dwordx4 v[150:153], v239, s[56:57] offset:512
	s_add_u32 s56, s56, 0x4000
	s_addc_u32 s57, s57, 0
	s_waitcnt vmcnt(23)
	v_cvt_pk_f16_f32 v204, v204, v205
	v_cvt_pk_f16_f32 v205, v206, v207
	ds_write_b64 v237, v[204:205]
	s_waitcnt vmcnt(22)
	v_cvt_pk_f16_f32 v208, v208, v209
	v_cvt_pk_f16_f32 v209, v210, v211
	ds_write_b64 v237, v[208:209] offset:4352
	s_waitcnt vmcnt(21)
	v_cvt_pk_f16_f32 v212, v212, v213
	v_cvt_pk_f16_f32 v213, v214, v215
	ds_write_b64 v237, v[212:213] offset:8704
	s_waitcnt vmcnt(20)
	v_cvt_pk_f16_f32 v216, v216, v217
	v_cvt_pk_f16_f32 v217, v218, v219
	ds_write_b64 v237, v[216:217] offset:13056
	s_waitcnt vmcnt(19)
	v_cvt_pk_f16_f32 v220, v220, v221
	v_cvt_pk_f16_f32 v221, v222, v223
	ds_write_b64 v237, v[220:221] offset:17408
	s_waitcnt vmcnt(18)
	v_cvt_pk_f16_f32 v224, v224, v225
	v_cvt_pk_f16_f32 v225, v226, v227
	ds_write_b64 v237, v[224:225] offset:21760
	s_waitcnt vmcnt(17)
	v_cvt_pk_f16_f32 v228, v228, v229
	v_cvt_pk_f16_f32 v229, v230, v231
	ds_write_b64 v237, v[228:229] offset:26112
	s_waitcnt vmcnt(16)
	v_cvt_pk_f16_f32 v232, v232, v233
	v_cvt_pk_f16_f32 v233, v234, v235
	ds_write_b64 v237, v[232:233] offset:30464
	global_load_dwordx4 v[204:207], v238, s[40:41] offset:3584
	global_load_dwordx4 v[208:211], v238, s[42:43] offset:3584
	global_load_dwordx4 v[212:215], v238, s[44:45] offset:3584
	global_load_dwordx4 v[216:219], v238, s[46:47] offset:3584
	global_load_dwordx4 v[220:223], v238, s[48:49] offset:3584
	global_load_dwordx4 v[224:227], v238, s[50:51] offset:3584
	global_load_dwordx4 v[228:231], v238, s[52:53] offset:3584
	global_load_dwordx4 v[232:235], v238, s[54:55] offset:3584
	s_waitcnt vmcnt(16)
	s_waitcnt lgkmcnt(11)
	v_mfma_f32_32x32x16_f16 v[82:97], v[130:133], v[154:157], v[82:97]
	v_mfma_f32_32x32x16_f16 v[50:65], v[130:133], v[158:161], v[50:65]
	ds_read_b128 v[130:133], v236 offset:35040
	s_waitcnt lgkmcnt(11)
	v_mfma_f32_32x32x16_f16 v[114:129], v[134:137], v[154:157], v[114:129]
	v_mfma_f32_32x32x16_f16 v[34:49], v[134:137], v[158:161], v[34:49]
	ds_read_b128 v[134:137], v236 offset:39392
	s_waitcnt lgkmcnt(11)
	v_mfma_f32_32x32x16_f16 v[98:113], v[138:141], v[154:157], v[98:113]
	v_mfma_f32_32x32x16_f16 v[18:33], v[138:141], v[158:161], v[18:33]
	ds_read_b128 v[138:141], v236 offset:43744
	s_waitcnt lgkmcnt(11)
	v_mfma_f32_32x32x16_f16 v[66:81], v[142:145], v[154:157], v[66:81]
	v_mfma_f32_32x32x16_f16 v[2:17], v[142:145], v[158:161], v[2:17]
	ds_read_b128 v[142:145], v236 offset:48096
	global_load_dwordx4 v[154:157], v239, s[56:57]
	global_load_dwordx4 v[158:161], v239, s[56:57] offset:512
	s_add_u32 s56, s56, 0x4000
	s_addc_u32 s57, s57, 0
	s_waitcnt vmcnt(16)
	s_waitcnt lgkmcnt(3)
	v_mfma_f32_32x32x16_f16 v[82:97], v[130:133], v[162:165], v[82:97]
	v_mfma_f32_32x32x16_f16 v[50:65], v[130:133], v[166:169], v[50:65]
	s_waitcnt lgkmcnt(2)
	v_mfma_f32_32x32x16_f16 v[114:129], v[134:137], v[162:165], v[114:129]
	v_mfma_f32_32x32x16_f16 v[34:49], v[134:137], v[166:169], v[34:49]
	s_waitcnt lgkmcnt(1)
	v_mfma_f32_32x32x16_f16 v[98:113], v[138:141], v[162:165], v[98:113]
	v_mfma_f32_32x32x16_f16 v[18:33], v[138:141], v[166:169], v[18:33]
	s_waitcnt lgkmcnt(0)
	v_mfma_f32_32x32x16_f16 v[66:81], v[142:145], v[162:165], v[66:81]
	v_mfma_f32_32x32x16_f16 v[2:17], v[142:145], v[166:169], v[2:17]
	global_load_dwordx4 v[162:165], v239, s[56:57]
	global_load_dwordx4 v[166:169], v239, s[56:57] offset:512
	s_add_u32 s56, s56, 0x4000
	s_addc_u32 s57, s57, 0
	s_waitcnt lgkmcnt(0)
	s_barrier
	ds_read_b128 v[130:133], v236
	ds_read_b128 v[134:137], v236 offset:4352
	ds_read_b128 v[138:141], v236 offset:8704
	ds_read_b128 v[142:145], v236 offset:13056
	s_waitcnt vmcnt(16)
	s_waitcnt lgkmcnt(3)
	v_mfma_f32_32x32x16_f16 v[82:97], v[130:133], v[170:173], v[82:97]
	v_mfma_f32_32x32x16_f16 v[50:65], v[130:133], v[174:177], v[50:65]
	ds_read_b128 v[130:133], v236 offset:32
	s_waitcnt lgkmcnt(3)
	v_mfma_f32_32x32x16_f16 v[114:129], v[134:137], v[170:173], v[114:129]
	v_mfma_f32_32x32x16_f16 v[34:49], v[134:137], v[174:177], v[34:49]
	ds_read_b128 v[134:137], v236 offset:4384
	s_waitcnt lgkmcnt(3)
	v_mfma_f32_32x32x16_f16 v[98:113], v[138:141], v[170:173], v[98:113]
	v_mfma_f32_32x32x16_f16 v[18:33], v[138:141], v[174:177], v[18:33]
	ds_read_b128 v[138:141], v236 offset:8736
	s_waitcnt lgkmcnt(3)
	v_mfma_f32_32x32x16_f16 v[66:81], v[142:145], v[170:173], v[66:81]
	v_mfma_f32_32x32x16_f16 v[2:17], v[142:145], v[174:177], v[2:17]
	ds_read_b128 v[142:145], v236 offset:13088
	global_load_dwordx4 v[170:173], v239, s[56:57]
	global_load_dwordx4 v[174:177], v239, s[56:57] offset:512
	s_add_u32 s56, s56, 0x4000
	s_addc_u32 s57, s57, 0
	s_waitcnt vmcnt(16)
	s_waitcnt lgkmcnt(3)
	v_mfma_f32_32x32x16_f16 v[82:97], v[130:133], v[178:181], v[82:97]
	v_mfma_f32_32x32x16_f16 v[50:65], v[130:133], v[182:185], v[50:65]
	ds_read_b128 v[130:133], v236 offset:64
	s_waitcnt lgkmcnt(3)
	v_mfma_f32_32x32x16_f16 v[114:129], v[134:137], v[178:181], v[114:129]
	v_mfma_f32_32x32x16_f16 v[34:49], v[134:137], v[182:185], v[34:49]
	ds_read_b128 v[134:137], v236 offset:4416
	s_waitcnt lgkmcnt(3)
	v_mfma_f32_32x32x16_f16 v[98:113], v[138:141], v[178:181], v[98:113]
	v_mfma_f32_32x32x16_f16 v[18:33], v[138:141], v[182:185], v[18:33]
	ds_read_b128 v[138:141], v236 offset:8768
	s_waitcnt lgkmcnt(3)
	v_mfma_f32_32x32x16_f16 v[66:81], v[142:145], v[178:181], v[66:81]
	v_mfma_f32_32x32x16_f16 v[2:17], v[142:145], v[182:185], v[2:17]
	ds_read_b128 v[142:145], v236 offset:13120
	global_load_dwordx4 v[178:181], v239, s[56:57]
	global_load_dwordx4 v[182:185], v239, s[56:57] offset:512
	s_add_u32 s56, s56, 0x4000
	s_addc_u32 s57, s57, 0
	s_waitcnt vmcnt(16)
	s_waitcnt lgkmcnt(3)
	v_mfma_f32_32x32x16_f16 v[82:97], v[130:133], v[146:149], v[82:97]
	v_mfma_f32_32x32x16_f16 v[50:65], v[130:133], v[150:153], v[50:65]
	ds_read_b128 v[130:133], v236 offset:96
	s_waitcnt lgkmcnt(3)
	v_mfma_f32_32x32x16_f16 v[114:129], v[134:137], v[146:149], v[114:129]
	v_mfma_f32_32x32x16_f16 v[34:49], v[134:137], v[150:153], v[34:49]
	ds_read_b128 v[134:137], v236 offset:4448
	s_waitcnt lgkmcnt(3)
	v_mfma_f32_32x32x16_f16 v[98:113], v[138:141], v[146:149], v[98:113]
	v_mfma_f32_32x32x16_f16 v[18:33], v[138:141], v[150:153], v[18:33]
	ds_read_b128 v[138:141], v236 offset:8800
	s_waitcnt lgkmcnt(3)
	v_mfma_f32_32x32x16_f16 v[66:81], v[142:145], v[146:149], v[66:81]
	v_mfma_f32_32x32x16_f16 v[2:17], v[142:145], v[150:153], v[2:17]
	ds_read_b128 v[142:145], v236 offset:13152
	global_load_dwordx4 v[146:149], v239, s[56:57]
	global_load_dwordx4 v[150:153], v239, s[56:57] offset:512
	s_add_u32 s56, s56, 0x4000
	s_addc_u32 s57, s57, 0
	s_waitcnt vmcnt(8)
	s_waitcnt lgkmcnt(3)
	v_mfma_f32_32x32x16_f16 v[82:97], v[130:133], v[154:157], v[82:97]
	v_mfma_f32_32x32x16_f16 v[50:65], v[130:133], v[158:161], v[50:65]
	ds_read_b128 v[130:133], v236 offset:128
	s_waitcnt lgkmcnt(3)
	v_mfma_f32_32x32x16_f16 v[114:129], v[134:137], v[154:157], v[114:129]
	v_mfma_f32_32x32x16_f16 v[34:49], v[134:137], v[158:161], v[34:49]
	ds_read_b128 v[134:137], v236 offset:4480
	s_waitcnt lgkmcnt(3)
	v_mfma_f32_32x32x16_f16 v[98:113], v[138:141], v[154:157], v[98:113]
	v_mfma_f32_32x32x16_f16 v[18:33], v[138:141], v[158:161], v[18:33]
	ds_read_b128 v[138:141], v236 offset:8832
	s_waitcnt lgkmcnt(3)
	v_mfma_f32_32x32x16_f16 v[66:81], v[142:145], v[154:157], v[66:81]
	v_mfma_f32_32x32x16_f16 v[2:17], v[142:145], v[158:161], v[2:17]
	ds_read_b128 v[142:145], v236 offset:13184
	global_load_dwordx4 v[154:157], v239, s[56:57]
	global_load_dwordx4 v[158:161], v239, s[56:57] offset:512
	s_add_u32 s56, s56, 0x4000
	s_addc_u32 s57, s57, 0
	s_waitcnt vmcnt(8)
	s_waitcnt lgkmcnt(3)
	v_mfma_f32_32x32x16_f16 v[82:97], v[130:133], v[162:165], v[82:97]
	v_mfma_f32_32x32x16_f16 v[50:65], v[130:133], v[166:169], v[50:65]
	ds_read_b128 v[130:133], v236 offset:160
	s_waitcnt lgkmcnt(3)
	v_mfma_f32_32x32x16_f16 v[114:129], v[134:137], v[162:165], v[114:129]
	v_mfma_f32_32x32x16_f16 v[34:49], v[134:137], v[166:169], v[34:49]
	ds_read_b128 v[134:137], v236 offset:4512
	s_waitcnt lgkmcnt(3)
	v_mfma_f32_32x32x16_f16 v[98:113], v[138:141], v[162:165], v[98:113]
	v_mfma_f32_32x32x16_f16 v[18:33], v[138:141], v[166:169], v[18:33]
	ds_read_b128 v[138:141], v236 offset:8864
	s_waitcnt lgkmcnt(3)
	v_mfma_f32_32x32x16_f16 v[66:81], v[142:145], v[162:165], v[66:81]
	v_mfma_f32_32x32x16_f16 v[2:17], v[142:145], v[166:169], v[2:17]
	ds_read_b128 v[142:145], v236 offset:13216
	global_load_dwordx4 v[162:165], v239, s[56:57]
	global_load_dwordx4 v[166:169], v239, s[56:57] offset:512
	s_add_u32 s56, s56, 0x4000
	s_addc_u32 s57, s57, 0
	s_waitcnt vmcnt(8)
	s_waitcnt lgkmcnt(3)
	v_mfma_f32_32x32x16_f16 v[82:97], v[130:133], v[170:173], v[82:97]
	v_mfma_f32_32x32x16_f16 v[50:65], v[130:133], v[174:177], v[50:65]
	ds_read_b128 v[130:133], v236 offset:192
	s_waitcnt lgkmcnt(3)
	v_mfma_f32_32x32x16_f16 v[114:129], v[134:137], v[170:173], v[114:129]
	v_mfma_f32_32x32x16_f16 v[34:49], v[134:137], v[174:177], v[34:49]
	ds_read_b128 v[134:137], v236 offset:4544
	s_waitcnt lgkmcnt(3)
	v_mfma_f32_32x32x16_f16 v[98:113], v[138:141], v[170:173], v[98:113]
	v_mfma_f32_32x32x16_f16 v[18:33], v[138:141], v[174:177], v[18:33]
	ds_read_b128 v[138:141], v236 offset:8896
	s_waitcnt lgkmcnt(3)
	v_mfma_f32_32x32x16_f16 v[66:81], v[142:145], v[170:173], v[66:81]
	v_mfma_f32_32x32x16_f16 v[2:17], v[142:145], v[174:177], v[2:17]
	ds_read_b128 v[142:145], v236 offset:13248
	global_load_dwordx4 v[170:173], v239, s[56:57]
	global_load_dwordx4 v[174:177], v239, s[56:57] offset:512
	s_add_u32 s56, s56, 0x4000
	s_addc_u32 s57, s57, 0
	s_waitcnt vmcnt(23)
	v_cvt_pk_f16_f32 v204, v204, v205
	v_cvt_pk_f16_f32 v205, v206, v207
	ds_write_b64 v237, v[204:205] offset:34816
	s_waitcnt vmcnt(22)
	v_cvt_pk_f16_f32 v208, v208, v209
	v_cvt_pk_f16_f32 v209, v210, v211
	ds_write_b64 v237, v[208:209] offset:39168
	s_waitcnt vmcnt(21)
	v_cvt_pk_f16_f32 v212, v212, v213
	v_cvt_pk_f16_f32 v213, v214, v215
	ds_write_b64 v237, v[212:213] offset:43520
	s_waitcnt vmcnt(20)
	v_cvt_pk_f16_f32 v216, v216, v217
	v_cvt_pk_f16_f32 v217, v218, v219
	ds_write_b64 v237, v[216:217] offset:47872
	s_waitcnt vmcnt(19)
	v_cvt_pk_f16_f32 v220, v220, v221
	v_cvt_pk_f16_f32 v221, v222, v223
	ds_write_b64 v237, v[220:221] offset:52224
	s_waitcnt vmcnt(18)
	v_cvt_pk_f16_f32 v224, v224, v225
	v_cvt_pk_f16_f32 v225, v226, v227
	ds_write_b64 v237, v[224:225] offset:56576
	s_waitcnt vmcnt(17)
	v_cvt_pk_f16_f32 v228, v228, v229
	v_cvt_pk_f16_f32 v229, v230, v231
	ds_write_b64 v237, v[228:229] offset:60928
	s_waitcnt vmcnt(16)
	v_cvt_pk_f16_f32 v232, v232, v233
	v_cvt_pk_f16_f32 v233, v234, v235
	ds_write_b64 v237, v[232:233] offset:65280
	s_waitcnt vmcnt(8)
	s_waitcnt lgkmcnt(11)
	v_mfma_f32_32x32x16_f16 v[82:97], v[130:133], v[178:181], v[82:97]
	v_mfma_f32_32x32x16_f16 v[50:65], v[130:133], v[182:185], v[50:65]
	ds_read_b128 v[130:133], v236 offset:224
	s_waitcnt lgkmcnt(11)
	v_mfma_f32_32x32x16_f16 v[114:129], v[134:137], v[178:181], v[114:129]
	v_mfma_f32_32x32x16_f16 v[34:49], v[134:137], v[182:185], v[34:49]
	ds_read_b128 v[134:137], v236 offset:4576
	s_waitcnt lgkmcnt(11)
	v_mfma_f32_32x32x16_f16 v[98:113], v[138:141], v[178:181], v[98:113]
	v_mfma_f32_32x32x16_f16 v[18:33], v[138:141], v[182:185], v[18:33]
	ds_read_b128 v[138:141], v236 offset:8928
	s_waitcnt lgkmcnt(11)
	v_mfma_f32_32x32x16_f16 v[66:81], v[142:145], v[178:181], v[66:81]
	v_mfma_f32_32x32x16_f16 v[2:17], v[142:145], v[182:185], v[2:17]
	ds_read_b128 v[142:145], v236 offset:13280
	global_load_dwordx4 v[178:181], v239, s[56:57]
	global_load_dwordx4 v[182:185], v239, s[56:57] offset:512
	s_add_u32 s56, s56, 0x4000
	s_addc_u32 s57, s57, 0
	s_waitcnt vmcnt(8)
	s_waitcnt lgkmcnt(3)
	v_mfma_f32_32x32x16_f16 v[82:97], v[130:133], v[146:149], v[82:97]
	v_mfma_f32_32x32x16_f16 v[50:65], v[130:133], v[150:153], v[50:65]
	s_waitcnt lgkmcnt(2)
	v_mfma_f32_32x32x16_f16 v[114:129], v[134:137], v[146:149], v[114:129]
	v_mfma_f32_32x32x16_f16 v[34:49], v[134:137], v[150:153], v[34:49]
	s_waitcnt lgkmcnt(1)
	v_mfma_f32_32x32x16_f16 v[98:113], v[138:141], v[146:149], v[98:113]
	v_mfma_f32_32x32x16_f16 v[18:33], v[138:141], v[150:153], v[18:33]
	s_waitcnt lgkmcnt(0)
	v_mfma_f32_32x32x16_f16 v[66:81], v[142:145], v[146:149], v[66:81]
	v_mfma_f32_32x32x16_f16 v[2:17], v[142:145], v[150:153], v[2:17]
	global_load_dwordx4 v[146:149], v239, s[56:57]
	global_load_dwordx4 v[150:153], v239, s[56:57] offset:512
	s_add_u32 s56, s56, 0x4000
	s_addc_u32 s57, s57, 0
	s_waitcnt lgkmcnt(0)
	s_barrier
	ds_read_b128 v[130:133], v236 offset:34816
	ds_read_b128 v[134:137], v236 offset:39168
	ds_read_b128 v[138:141], v236 offset:43520
	ds_read_b128 v[142:145], v236 offset:47872
	s_waitcnt vmcnt(8)
	s_waitcnt lgkmcnt(3)
	v_mfma_f32_32x32x16_f16 v[82:97], v[130:133], v[154:157], v[82:97]
	v_mfma_f32_32x32x16_f16 v[50:65], v[130:133], v[158:161], v[50:65]
	ds_read_b128 v[130:133], v236 offset:34848
	s_waitcnt lgkmcnt(3)
	v_mfma_f32_32x32x16_f16 v[114:129], v[134:137], v[154:157], v[114:129]
	v_mfma_f32_32x32x16_f16 v[34:49], v[134:137], v[158:161], v[34:49]
	ds_read_b128 v[134:137], v236 offset:39200
	s_waitcnt lgkmcnt(3)
	v_mfma_f32_32x32x16_f16 v[98:113], v[138:141], v[154:157], v[98:113]
	v_mfma_f32_32x32x16_f16 v[18:33], v[138:141], v[158:161], v[18:33]
	ds_read_b128 v[138:141], v236 offset:43552
	s_waitcnt lgkmcnt(3)
	v_mfma_f32_32x32x16_f16 v[66:81], v[142:145], v[154:157], v[66:81]
	v_mfma_f32_32x32x16_f16 v[2:17], v[142:145], v[158:161], v[2:17]
	ds_read_b128 v[142:145], v236 offset:47904
	global_load_dwordx4 v[154:157], v239, s[56:57]
	global_load_dwordx4 v[158:161], v239, s[56:57] offset:512
	s_add_u32 s56, s56, 0x4000
	s_addc_u32 s57, s57, 0
	s_waitcnt vmcnt(8)
	s_waitcnt lgkmcnt(3)
	v_mfma_f32_32x32x16_f16 v[82:97], v[130:133], v[162:165], v[82:97]
	v_mfma_f32_32x32x16_f16 v[50:65], v[130:133], v[166:169], v[50:65]
	ds_read_b128 v[130:133], v236 offset:34880
	s_waitcnt lgkmcnt(3)
	v_mfma_f32_32x32x16_f16 v[114:129], v[134:137], v[162:165], v[114:129]
	v_mfma_f32_32x32x16_f16 v[34:49], v[134:137], v[166:169], v[34:49]
	ds_read_b128 v[134:137], v236 offset:39232
	s_waitcnt lgkmcnt(3)
	v_mfma_f32_32x32x16_f16 v[98:113], v[138:141], v[162:165], v[98:113]
	v_mfma_f32_32x32x16_f16 v[18:33], v[138:141], v[166:169], v[18:33]
	ds_read_b128 v[138:141], v236 offset:43584
	s_waitcnt lgkmcnt(3)
	v_mfma_f32_32x32x16_f16 v[66:81], v[142:145], v[162:165], v[66:81]
	v_mfma_f32_32x32x16_f16 v[2:17], v[142:145], v[166:169], v[2:17]
	ds_read_b128 v[142:145], v236 offset:47936
	global_load_dwordx4 v[162:165], v239, s[56:57]
	global_load_dwordx4 v[166:169], v239, s[56:57] offset:512
	s_add_u32 s56, s56, 0x4000
	s_addc_u32 s57, s57, 0
	s_waitcnt vmcnt(8)
	s_waitcnt lgkmcnt(3)
	v_mfma_f32_32x32x16_f16 v[82:97], v[130:133], v[170:173], v[82:97]
	v_mfma_f32_32x32x16_f16 v[50:65], v[130:133], v[174:177], v[50:65]
	ds_read_b128 v[130:133], v236 offset:34912
	s_waitcnt lgkmcnt(3)
	v_mfma_f32_32x32x16_f16 v[114:129], v[134:137], v[170:173], v[114:129]
	v_mfma_f32_32x32x16_f16 v[34:49], v[134:137], v[174:177], v[34:49]
	ds_read_b128 v[134:137], v236 offset:39264
	s_waitcnt lgkmcnt(3)
	v_mfma_f32_32x32x16_f16 v[98:113], v[138:141], v[170:173], v[98:113]
	v_mfma_f32_32x32x16_f16 v[18:33], v[138:141], v[174:177], v[18:33]
	ds_read_b128 v[138:141], v236 offset:43616
	s_waitcnt lgkmcnt(3)
	v_mfma_f32_32x32x16_f16 v[66:81], v[142:145], v[170:173], v[66:81]
	v_mfma_f32_32x32x16_f16 v[2:17], v[142:145], v[174:177], v[2:17]
	ds_read_b128 v[142:145], v236 offset:47968
	global_load_dwordx4 v[170:173], v239, s[56:57]
	global_load_dwordx4 v[174:177], v239, s[56:57] offset:512
	s_add_u32 s56, s56, 0x4000
	s_addc_u32 s57, s57, 0
	s_waitcnt vmcnt(8)
	s_waitcnt lgkmcnt(3)
	v_mfma_f32_32x32x16_f16 v[82:97], v[130:133], v[178:181], v[82:97]
	v_mfma_f32_32x32x16_f16 v[50:65], v[130:133], v[182:185], v[50:65]
	ds_read_b128 v[130:133], v236 offset:34944
	s_waitcnt lgkmcnt(3)
	v_mfma_f32_32x32x16_f16 v[114:129], v[134:137], v[178:181], v[114:129]
	v_mfma_f32_32x32x16_f16 v[34:49], v[134:137], v[182:185], v[34:49]
	ds_read_b128 v[134:137], v236 offset:39296
	s_waitcnt lgkmcnt(3)
	v_mfma_f32_32x32x16_f16 v[98:113], v[138:141], v[178:181], v[98:113]
	v_mfma_f32_32x32x16_f16 v[18:33], v[138:141], v[182:185], v[18:33]
	ds_read_b128 v[138:141], v236 offset:43648
	s_waitcnt lgkmcnt(3)
	v_mfma_f32_32x32x16_f16 v[66:81], v[142:145], v[178:181], v[66:81]
	v_mfma_f32_32x32x16_f16 v[2:17], v[142:145], v[182:185], v[2:17]
	ds_read_b128 v[142:145], v236 offset:48000
	s_waitcnt vmcnt(6)
	s_waitcnt lgkmcnt(3)
	v_mfma_f32_32x32x16_f16 v[82:97], v[130:133], v[146:149], v[82:97]
	v_mfma_f32_32x32x16_f16 v[50:65], v[130:133], v[150:153], v[50:65]
	ds_read_b128 v[130:133], v236 offset:34976
	s_waitcnt lgkmcnt(3)
	v_mfma_f32_32x32x16_f16 v[114:129], v[134:137], v[146:149], v[114:129]
	v_mfma_f32_32x32x16_f16 v[34:49], v[134:137], v[150:153], v[34:49]
	ds_read_b128 v[134:137], v236 offset:39328
	s_waitcnt lgkmcnt(3)
	v_mfma_f32_32x32x16_f16 v[98:113], v[138:141], v[146:149], v[98:113]
	v_mfma_f32_32x32x16_f16 v[18:33], v[138:141], v[150:153], v[18:33]
	ds_read_b128 v[138:141], v236 offset:43680
	s_waitcnt lgkmcnt(3)
	v_mfma_f32_32x32x16_f16 v[66:81], v[142:145], v[146:149], v[66:81]
	v_mfma_f32_32x32x16_f16 v[2:17], v[142:145], v[150:153], v[2:17]
	ds_read_b128 v[142:145], v236 offset:48032
	s_waitcnt vmcnt(4)
	s_waitcnt lgkmcnt(3)
	v_mfma_f32_32x32x16_f16 v[82:97], v[130:133], v[154:157], v[82:97]
	v_mfma_f32_32x32x16_f16 v[50:65], v[130:133], v[158:161], v[50:65]
	ds_read_b128 v[130:133], v236 offset:35008
	s_waitcnt lgkmcnt(3)
	v_mfma_f32_32x32x16_f16 v[114:129], v[134:137], v[154:157], v[114:129]
	v_mfma_f32_32x32x16_f16 v[34:49], v[134:137], v[158:161], v[34:49]
	ds_read_b128 v[134:137], v236 offset:39360
	s_waitcnt lgkmcnt(3)
	v_mfma_f32_32x32x16_f16 v[98:113], v[138:141], v[154:157], v[98:113]
	v_mfma_f32_32x32x16_f16 v[18:33], v[138:141], v[158:161], v[18:33]
	ds_read_b128 v[138:141], v236 offset:43712
	s_waitcnt lgkmcnt(3)
	v_mfma_f32_32x32x16_f16 v[66:81], v[142:145], v[154:157], v[66:81]
	v_mfma_f32_32x32x16_f16 v[2:17], v[142:145], v[158:161], v[2:17]
	ds_read_b128 v[142:145], v236 offset:48064
	s_waitcnt vmcnt(2)
	s_waitcnt lgkmcnt(3)
	v_mfma_f32_32x32x16_f16 v[82:97], v[130:133], v[162:165], v[82:97]
	v_mfma_f32_32x32x16_f16 v[50:65], v[130:133], v[166:169], v[50:65]
	ds_read_b128 v[130:133], v236 offset:35040
	s_waitcnt lgkmcnt(3)
	v_mfma_f32_32x32x16_f16 v[114:129], v[134:137], v[162:165], v[114:129]
	v_mfma_f32_32x32x16_f16 v[34:49], v[134:137], v[166:169], v[34:49]
	ds_read_b128 v[134:137], v236 offset:39392
	s_waitcnt lgkmcnt(3)
	v_mfma_f32_32x32x16_f16 v[98:113], v[138:141], v[162:165], v[98:113]
	v_mfma_f32_32x32x16_f16 v[18:33], v[138:141], v[166:169], v[18:33]
	ds_read_b128 v[138:141], v236 offset:43744
	s_waitcnt lgkmcnt(3)
	v_mfma_f32_32x32x16_f16 v[66:81], v[142:145], v[162:165], v[66:81]
	v_mfma_f32_32x32x16_f16 v[2:17], v[142:145], v[166:169], v[2:17]
	ds_read_b128 v[142:145], v236 offset:48096
	s_waitcnt vmcnt(0)
	s_waitcnt lgkmcnt(3)
	v_mfma_f32_32x32x16_f16 v[82:97], v[130:133], v[170:173], v[82:97]
	v_mfma_f32_32x32x16_f16 v[50:65], v[130:133], v[174:177], v[50:65]
	s_waitcnt lgkmcnt(2)
	v_mfma_f32_32x32x16_f16 v[114:129], v[134:137], v[170:173], v[114:129]
	v_mfma_f32_32x32x16_f16 v[34:49], v[134:137], v[174:177], v[34:49]
	s_waitcnt lgkmcnt(1)
	v_mfma_f32_32x32x16_f16 v[98:113], v[138:141], v[170:173], v[98:113]
	v_mfma_f32_32x32x16_f16 v[18:33], v[138:141], v[174:177], v[18:33]
	s_waitcnt lgkmcnt(0)
	v_mfma_f32_32x32x16_f16 v[66:81], v[142:145], v[170:173], v[66:81]
	v_mfma_f32_32x32x16_f16 v[2:17], v[142:145], v[174:177], v[2:17]
	s_waitcnt vmcnt(0) lgkmcnt(0)
	s_nop 15
	s_mov_b64 exec, -1
	v_bfe_u32 v202, v0, 5, 1
	s_lshl_b32 s34, s29, 9
	v_and_b32_e32 v203, 0x1c0, v0
	v_and_b32_e32 v204, 31, v0
	v_or3_b32 v0, s34, v203, v204
	v_lshlrev_b32_e32 v0, 2, v0
	s_waitcnt vmcnt(0) lgkmcnt(0)
	s_barrier
	v_mov_b32_e32 v131, v244
	v_mov_b32_e32 v1, v245
	s_mov_b32 s6, 0x3dcccccd
	s_mov_b32 s7, 0xbdcccccd
	v_mov_b32_e32 v132, 0
	v_mov_b32_e32 v133, 0
	v_mov_b32_e32 v134, 0
	v_mov_b32_e32 v135, 0
	v_fma_f32 v130, -v133, v131, v82
	v_fma_f32 v246, -v135, v1, v50
	v_fmac_f32_e32 v132, 0x3dcccccd, v130
	v_fmac_f32_e32 v134, 0x3dcccccd, v246
	v_fmac_f32_e32 v133, 0x3dcccccd, v132
	v_fmac_f32_e32 v135, 0x3dcccccd, v134
	v_fma_f32 v130, -v133, v131, v83
	v_fma_f32 v246, -v135, v1, v51
	v_fmac_f32_e32 v132, 0x3dcccccd, v130
	v_fmac_f32_e32 v134, 0x3dcccccd, v246
	v_fmac_f32_e32 v133, 0x3dcccccd, v132
	v_fmac_f32_e32 v135, 0x3dcccccd, v134
	v_fma_f32 v130, -v133, v131, v84
	v_fma_f32 v246, -v135, v1, v52
	v_fmac_f32_e32 v132, 0x3dcccccd, v130
	v_fmac_f32_e32 v134, 0x3dcccccd, v246
	v_fmac_f32_e32 v133, 0x3dcccccd, v132
	v_fmac_f32_e32 v135, 0x3dcccccd, v134
	v_fma_f32 v130, -v133, v131, v85
	v_fma_f32 v246, -v135, v1, v53
	v_fmac_f32_e32 v132, 0x3dcccccd, v130
	v_fmac_f32_e32 v134, 0x3dcccccd, v246
	v_fmac_f32_e32 v133, 0x3dcccccd, v132
	v_fmac_f32_e32 v135, 0x3dcccccd, v134
	v_fma_f32 v130, -v133, v131, v86
	v_fma_f32 v246, -v135, v1, v54
	v_fmac_f32_e32 v132, 0x3dcccccd, v130
	v_fmac_f32_e32 v134, 0x3dcccccd, v246
	v_fmac_f32_e32 v133, 0x3dcccccd, v132
	v_fmac_f32_e32 v135, 0x3dcccccd, v134
	v_fma_f32 v130, -v133, v131, v87
	v_fma_f32 v246, -v135, v1, v55
	v_fmac_f32_e32 v132, 0x3dcccccd, v130
	v_fmac_f32_e32 v134, 0x3dcccccd, v246
	v_fmac_f32_e32 v133, 0x3dcccccd, v132
	v_fmac_f32_e32 v135, 0x3dcccccd, v134
	v_fma_f32 v130, -v133, v131, v88
	v_fma_f32 v246, -v135, v1, v56
	v_fmac_f32_e32 v132, 0x3dcccccd, v130
	v_fmac_f32_e32 v134, 0x3dcccccd, v246
	v_fmac_f32_e32 v133, 0x3dcccccd, v132
	v_fmac_f32_e32 v135, 0x3dcccccd, v134
	v_fma_f32 v130, -v133, v131, v89
	v_fma_f32 v246, -v135, v1, v57
	v_fmac_f32_e32 v132, 0x3dcccccd, v130
	v_fmac_f32_e32 v134, 0x3dcccccd, v246
	v_fmac_f32_e32 v133, 0x3dcccccd, v132
	v_fmac_f32_e32 v135, 0x3dcccccd, v134
	v_fma_f32 v130, -v133, v131, v90
	v_fma_f32 v246, -v135, v1, v58
	v_fmac_f32_e32 v132, 0x3dcccccd, v130
	v_fmac_f32_e32 v134, 0x3dcccccd, v246
	v_fmac_f32_e32 v133, 0x3dcccccd, v132
	v_fmac_f32_e32 v135, 0x3dcccccd, v134
	v_fma_f32 v130, -v133, v131, v91
	v_fma_f32 v246, -v135, v1, v59
	v_fmac_f32_e32 v132, 0x3dcccccd, v130
	v_fmac_f32_e32 v134, 0x3dcccccd, v246
	v_fmac_f32_e32 v133, 0x3dcccccd, v132
	v_fmac_f32_e32 v135, 0x3dcccccd, v134
	v_fma_f32 v130, -v133, v131, v92
	v_fma_f32 v246, -v135, v1, v60
	v_fmac_f32_e32 v132, 0x3dcccccd, v130
	v_fmac_f32_e32 v134, 0x3dcccccd, v246
	v_fmac_f32_e32 v133, 0x3dcccccd, v132
	v_fmac_f32_e32 v135, 0x3dcccccd, v134
	v_fma_f32 v130, -v133, v131, v93
	v_fma_f32 v246, -v135, v1, v61
	v_fmac_f32_e32 v132, 0x3dcccccd, v130
	v_fmac_f32_e32 v134, 0x3dcccccd, v246
	v_fmac_f32_e32 v133, 0x3dcccccd, v132
	v_fmac_f32_e32 v135, 0x3dcccccd, v134
	v_fma_f32 v130, -v133, v131, v94
	v_fma_f32 v246, -v135, v1, v62
	v_fmac_f32_e32 v132, 0x3dcccccd, v130
	v_fmac_f32_e32 v134, 0x3dcccccd, v246
	v_fmac_f32_e32 v133, 0x3dcccccd, v132
	v_fmac_f32_e32 v135, 0x3dcccccd, v134
	v_fma_f32 v130, -v133, v131, v95
	v_fma_f32 v246, -v135, v1, v63
	v_fmac_f32_e32 v132, 0x3dcccccd, v130
	v_fmac_f32_e32 v134, 0x3dcccccd, v246
	v_fmac_f32_e32 v133, 0x3dcccccd, v132
	v_fmac_f32_e32 v135, 0x3dcccccd, v134
	v_fma_f32 v130, -v133, v131, v96
	v_fma_f32 v246, -v135, v1, v64
	v_fmac_f32_e32 v132, 0x3dcccccd, v130
	v_fmac_f32_e32 v134, 0x3dcccccd, v246
	v_fmac_f32_e32 v133, 0x3dcccccd, v132
	v_fmac_f32_e32 v135, 0x3dcccccd, v134
	v_fma_f32 v130, -v133, v131, v97
	v_fma_f32 v246, -v135, v1, v65
	v_fmac_f32_e32 v132, 0x3dcccccd, v130
	v_fmac_f32_e32 v134, 0x3dcccccd, v246
	v_fmac_f32_e32 v133, 0x3dcccccd, v132
	v_fmac_f32_e32 v135, 0x3dcccccd, v134
	v_fma_f32 v130, -v133, v131, v114
	v_fma_f32 v246, -v135, v1, v34
	v_fmac_f32_e32 v132, 0x3dcccccd, v130
	v_fmac_f32_e32 v134, 0x3dcccccd, v246
	v_fmac_f32_e32 v133, 0x3dcccccd, v132
	v_fmac_f32_e32 v135, 0x3dcccccd, v134
	v_fma_f32 v130, -v133, v131, v115
	v_fma_f32 v246, -v135, v1, v35
	v_fmac_f32_e32 v132, 0x3dcccccd, v130
	v_fmac_f32_e32 v134, 0x3dcccccd, v246
	v_fmac_f32_e32 v133, 0x3dcccccd, v132
	v_fmac_f32_e32 v135, 0x3dcccccd, v134
	v_fma_f32 v130, -v133, v131, v116
	v_fma_f32 v246, -v135, v1, v36
	v_fmac_f32_e32 v132, 0x3dcccccd, v130
	v_fmac_f32_e32 v134, 0x3dcccccd, v246
	v_fmac_f32_e32 v133, 0x3dcccccd, v132
	v_fmac_f32_e32 v135, 0x3dcccccd, v134
	v_fma_f32 v130, -v133, v131, v117
	v_fma_f32 v246, -v135, v1, v37
	v_fmac_f32_e32 v132, 0x3dcccccd, v130
	v_fmac_f32_e32 v134, 0x3dcccccd, v246
	v_fmac_f32_e32 v133, 0x3dcccccd, v132
	v_fmac_f32_e32 v135, 0x3dcccccd, v134
	v_fma_f32 v130, -v133, v131, v118
	v_fma_f32 v246, -v135, v1, v38
	v_fmac_f32_e32 v132, 0x3dcccccd, v130
	v_fmac_f32_e32 v134, 0x3dcccccd, v246
	v_fmac_f32_e32 v133, 0x3dcccccd, v132
	v_fmac_f32_e32 v135, 0x3dcccccd, v134
	v_fma_f32 v130, -v133, v131, v119
	v_fma_f32 v246, -v135, v1, v39
	v_fmac_f32_e32 v132, 0x3dcccccd, v130
	v_fmac_f32_e32 v134, 0x3dcccccd, v246
	v_fmac_f32_e32 v133, 0x3dcccccd, v132
	v_fmac_f32_e32 v135, 0x3dcccccd, v134
	v_fma_f32 v130, -v133, v131, v120
	v_fma_f32 v246, -v135, v1, v40
	v_fmac_f32_e32 v132, 0x3dcccccd, v130
	v_fmac_f32_e32 v134, 0x3dcccccd, v246
	v_fmac_f32_e32 v133, 0x3dcccccd, v132
	v_fmac_f32_e32 v135, 0x3dcccccd, v134
	v_fma_f32 v130, -v133, v131, v121
	v_fma_f32 v246, -v135, v1, v41
	v_fmac_f32_e32 v132, 0x3dcccccd, v130
	v_fmac_f32_e32 v134, 0x3dcccccd, v246
	v_fmac_f32_e32 v133, 0x3dcccccd, v132
	v_fmac_f32_e32 v135, 0x3dcccccd, v134
	v_fma_f32 v130, -v133, v131, v122
	v_fma_f32 v246, -v135, v1, v42
	v_fmac_f32_e32 v132, 0x3dcccccd, v130
	v_fmac_f32_e32 v134, 0x3dcccccd, v246
	v_fmac_f32_e32 v133, 0x3dcccccd, v132
	v_fmac_f32_e32 v135, 0x3dcccccd, v134
	v_fma_f32 v130, -v133, v131, v123
	v_fma_f32 v246, -v135, v1, v43
	v_fmac_f32_e32 v132, 0x3dcccccd, v130
	v_fmac_f32_e32 v134, 0x3dcccccd, v246
	v_fmac_f32_e32 v133, 0x3dcccccd, v132
	v_fmac_f32_e32 v135, 0x3dcccccd, v134
	v_fma_f32 v130, -v133, v131, v124
	v_fma_f32 v246, -v135, v1, v44
	v_fmac_f32_e32 v132, 0x3dcccccd, v130
	v_fmac_f32_e32 v134, 0x3dcccccd, v246
	v_fmac_f32_e32 v133, 0x3dcccccd, v132
	v_fmac_f32_e32 v135, 0x3dcccccd, v134
	v_fma_f32 v130, -v133, v131, v125
	v_fma_f32 v246, -v135, v1, v45
	v_fmac_f32_e32 v132, 0x3dcccccd, v130
	v_fmac_f32_e32 v134, 0x3dcccccd, v246
	v_fmac_f32_e32 v133, 0x3dcccccd, v132
	v_fmac_f32_e32 v135, 0x3dcccccd, v134
	v_fma_f32 v130, -v133, v131, v126
	v_fma_f32 v246, -v135, v1, v46
	v_fmac_f32_e32 v132, 0x3dcccccd, v130
	v_fmac_f32_e32 v134, 0x3dcccccd, v246
	v_fmac_f32_e32 v133, 0x3dcccccd, v132
	v_fmac_f32_e32 v135, 0x3dcccccd, v134
	v_fma_f32 v130, -v133, v131, v127
	v_fma_f32 v246, -v135, v1, v47
	v_fmac_f32_e32 v132, 0x3dcccccd, v130
	v_fmac_f32_e32 v134, 0x3dcccccd, v246
	v_fmac_f32_e32 v133, 0x3dcccccd, v132
	v_fmac_f32_e32 v135, 0x3dcccccd, v134
	v_fma_f32 v130, -v133, v131, v128
	v_fma_f32 v246, -v135, v1, v48
	v_fmac_f32_e32 v132, 0x3dcccccd, v130
	v_fmac_f32_e32 v134, 0x3dcccccd, v246
	v_fmac_f32_e32 v133, 0x3dcccccd, v132
	v_fmac_f32_e32 v135, 0x3dcccccd, v134
	v_fma_f32 v130, -v133, v131, v129
	v_fma_f32 v246, -v135, v1, v49
	v_fmac_f32_e32 v132, 0x3dcccccd, v130
	v_fmac_f32_e32 v134, 0x3dcccccd, v246
	v_fmac_f32_e32 v133, 0x3dcccccd, v132
	v_fmac_f32_e32 v135, 0x3dcccccd, v134
	v_fma_f32 v130, -v133, v131, v98
	v_fma_f32 v246, -v135, v1, v18
	v_fmac_f32_e32 v132, 0x3dcccccd, v130
	v_fmac_f32_e32 v134, 0x3dcccccd, v246
	v_fmac_f32_e32 v133, 0x3dcccccd, v132
	v_fmac_f32_e32 v135, 0x3dcccccd, v134
	v_fma_f32 v130, -v133, v131, v99
	v_fma_f32 v246, -v135, v1, v19
	v_fmac_f32_e32 v132, 0x3dcccccd, v130
	v_fmac_f32_e32 v134, 0x3dcccccd, v246
	v_fmac_f32_e32 v133, 0x3dcccccd, v132
	v_fmac_f32_e32 v135, 0x3dcccccd, v134
	v_fma_f32 v130, -v133, v131, v100
	v_fma_f32 v246, -v135, v1, v20
	v_fmac_f32_e32 v132, 0x3dcccccd, v130
	v_fmac_f32_e32 v134, 0x3dcccccd, v246
	v_fmac_f32_e32 v133, 0x3dcccccd, v132
	v_fmac_f32_e32 v135, 0x3dcccccd, v134
	v_fma_f32 v130, -v133, v131, v101
	v_fma_f32 v246, -v135, v1, v21
	v_fmac_f32_e32 v132, 0x3dcccccd, v130
	v_fmac_f32_e32 v134, 0x3dcccccd, v246
	v_fmac_f32_e32 v133, 0x3dcccccd, v132
	v_fmac_f32_e32 v135, 0x3dcccccd, v134
	v_fma_f32 v130, -v133, v131, v102
	v_fma_f32 v246, -v135, v1, v22
	v_fmac_f32_e32 v132, 0x3dcccccd, v130
	v_fmac_f32_e32 v134, 0x3dcccccd, v246
	v_fmac_f32_e32 v133, 0x3dcccccd, v132
	v_fmac_f32_e32 v135, 0x3dcccccd, v134
	v_fma_f32 v130, -v133, v131, v103
	v_fma_f32 v246, -v135, v1, v23
	v_fmac_f32_e32 v132, 0x3dcccccd, v130
	v_fmac_f32_e32 v134, 0x3dcccccd, v246
	v_fmac_f32_e32 v133, 0x3dcccccd, v132
	v_fmac_f32_e32 v135, 0x3dcccccd, v134
	v_fma_f32 v130, -v133, v131, v104
	v_fma_f32 v246, -v135, v1, v24
	v_fmac_f32_e32 v132, 0x3dcccccd, v130
	v_fmac_f32_e32 v134, 0x3dcccccd, v246
	v_fmac_f32_e32 v133, 0x3dcccccd, v132
	v_fmac_f32_e32 v135, 0x3dcccccd, v134
	v_fma_f32 v130, -v133, v131, v105
	v_fma_f32 v246, -v135, v1, v25
	v_fmac_f32_e32 v132, 0x3dcccccd, v130
	v_fmac_f32_e32 v134, 0x3dcccccd, v246
	v_fmac_f32_e32 v133, 0x3dcccccd, v132
	v_fmac_f32_e32 v135, 0x3dcccccd, v134
	v_fma_f32 v130, -v133, v131, v106
	v_fma_f32 v246, -v135, v1, v26
	v_fmac_f32_e32 v132, 0x3dcccccd, v130
	v_fmac_f32_e32 v134, 0x3dcccccd, v246
	v_fmac_f32_e32 v133, 0x3dcccccd, v132
	v_fmac_f32_e32 v135, 0x3dcccccd, v134
	v_fma_f32 v130, -v133, v131, v107
	v_fma_f32 v246, -v135, v1, v27
	v_fmac_f32_e32 v132, 0x3dcccccd, v130
	v_fmac_f32_e32 v134, 0x3dcccccd, v246
	v_fmac_f32_e32 v133, 0x3dcccccd, v132
	v_fmac_f32_e32 v135, 0x3dcccccd, v134
	v_fma_f32 v130, -v133, v131, v108
	v_fma_f32 v246, -v135, v1, v28
	v_fmac_f32_e32 v132, 0x3dcccccd, v130
	v_fmac_f32_e32 v134, 0x3dcccccd, v246
	v_fmac_f32_e32 v133, 0x3dcccccd, v132
	v_fmac_f32_e32 v135, 0x3dcccccd, v134
	v_fma_f32 v130, -v133, v131, v109
	v_fma_f32 v246, -v135, v1, v29
	v_fmac_f32_e32 v132, 0x3dcccccd, v130
	v_fmac_f32_e32 v134, 0x3dcccccd, v246
	v_fmac_f32_e32 v133, 0x3dcccccd, v132
	v_fmac_f32_e32 v135, 0x3dcccccd, v134
	v_fma_f32 v130, -v133, v131, v110
	v_fma_f32 v246, -v135, v1, v30
	v_fmac_f32_e32 v132, 0x3dcccccd, v130
	v_fmac_f32_e32 v134, 0x3dcccccd, v246
	v_fmac_f32_e32 v133, 0x3dcccccd, v132
	v_fmac_f32_e32 v135, 0x3dcccccd, v134
	v_fma_f32 v130, -v133, v131, v111
	v_fma_f32 v246, -v135, v1, v31
	v_fmac_f32_e32 v132, 0x3dcccccd, v130
	v_fmac_f32_e32 v134, 0x3dcccccd, v246
	v_fmac_f32_e32 v133, 0x3dcccccd, v132
	v_fmac_f32_e32 v135, 0x3dcccccd, v134
	v_fma_f32 v130, -v133, v131, v112
	v_fma_f32 v246, -v135, v1, v32
	v_fmac_f32_e32 v132, 0x3dcccccd, v130
	v_fmac_f32_e32 v134, 0x3dcccccd, v246
	v_fmac_f32_e32 v133, 0x3dcccccd, v132
	v_fmac_f32_e32 v135, 0x3dcccccd, v134
	v_fma_f32 v130, -v133, v131, v113
	v_fma_f32 v246, -v135, v1, v33
	v_fmac_f32_e32 v132, 0x3dcccccd, v130
	v_fmac_f32_e32 v134, 0x3dcccccd, v246
	v_fmac_f32_e32 v133, 0x3dcccccd, v132
	v_fmac_f32_e32 v135, 0x3dcccccd, v134
	v_fma_f32 v130, -v133, v131, v66
	v_fma_f32 v246, -v135, v1, v2
	v_fmac_f32_e32 v132, 0x3dcccccd, v130
	v_fmac_f32_e32 v134, 0x3dcccccd, v246
	v_fmac_f32_e32 v133, 0x3dcccccd, v132
	v_fmac_f32_e32 v135, 0x3dcccccd, v134
	v_fma_f32 v130, -v133, v131, v67
	v_fma_f32 v246, -v135, v1, v3
	v_fmac_f32_e32 v132, 0x3dcccccd, v130
	v_fmac_f32_e32 v134, 0x3dcccccd, v246
	v_fmac_f32_e32 v133, 0x3dcccccd, v132
	v_fmac_f32_e32 v135, 0x3dcccccd, v134
	v_fma_f32 v130, -v133, v131, v68
	v_fma_f32 v246, -v135, v1, v4
	v_fmac_f32_e32 v132, 0x3dcccccd, v130
	v_fmac_f32_e32 v134, 0x3dcccccd, v246
	v_fmac_f32_e32 v133, 0x3dcccccd, v132
	v_fmac_f32_e32 v135, 0x3dcccccd, v134
	v_fma_f32 v130, -v133, v131, v69
	v_fma_f32 v246, -v135, v1, v5
	v_fmac_f32_e32 v132, 0x3dcccccd, v130
	v_fmac_f32_e32 v134, 0x3dcccccd, v246
	v_fmac_f32_e32 v133, 0x3dcccccd, v132
	v_fmac_f32_e32 v135, 0x3dcccccd, v134
	v_fma_f32 v130, -v133, v131, v70
	v_fma_f32 v246, -v135, v1, v6
	v_fmac_f32_e32 v132, 0x3dcccccd, v130
	v_fmac_f32_e32 v134, 0x3dcccccd, v246
	v_fmac_f32_e32 v133, 0x3dcccccd, v132
	v_fmac_f32_e32 v135, 0x3dcccccd, v134
	v_fma_f32 v130, -v133, v131, v71
	v_fma_f32 v246, -v135, v1, v7
	v_fmac_f32_e32 v132, 0x3dcccccd, v130
	v_fmac_f32_e32 v134, 0x3dcccccd, v246
	v_fmac_f32_e32 v133, 0x3dcccccd, v132
	v_fmac_f32_e32 v135, 0x3dcccccd, v134
	v_fma_f32 v130, -v133, v131, v72
	v_fma_f32 v246, -v135, v1, v8
	v_fmac_f32_e32 v132, 0x3dcccccd, v130
	v_fmac_f32_e32 v134, 0x3dcccccd, v246
	v_fmac_f32_e32 v133, 0x3dcccccd, v132
	v_fmac_f32_e32 v135, 0x3dcccccd, v134
	v_fma_f32 v130, -v133, v131, v73
	v_fma_f32 v246, -v135, v1, v9
	v_fmac_f32_e32 v132, 0x3dcccccd, v130
	v_fmac_f32_e32 v134, 0x3dcccccd, v246
	v_fmac_f32_e32 v133, 0x3dcccccd, v132
	v_fmac_f32_e32 v135, 0x3dcccccd, v134
	v_fma_f32 v130, -v133, v131, v74
	v_fma_f32 v246, -v135, v1, v10
	v_fmac_f32_e32 v132, 0x3dcccccd, v130
	v_fmac_f32_e32 v134, 0x3dcccccd, v246
	v_fmac_f32_e32 v133, 0x3dcccccd, v132
	v_fmac_f32_e32 v135, 0x3dcccccd, v134
	v_fma_f32 v130, -v133, v131, v75
	v_fma_f32 v246, -v135, v1, v11
	v_fmac_f32_e32 v132, 0x3dcccccd, v130
	v_fmac_f32_e32 v134, 0x3dcccccd, v246
	v_fmac_f32_e32 v133, 0x3dcccccd, v132
	v_fmac_f32_e32 v135, 0x3dcccccd, v134
	v_fma_f32 v130, -v133, v131, v76
	v_fma_f32 v246, -v135, v1, v12
	v_fmac_f32_e32 v132, 0x3dcccccd, v130
	v_fmac_f32_e32 v134, 0x3dcccccd, v246
	v_fmac_f32_e32 v133, 0x3dcccccd, v132
	v_fmac_f32_e32 v135, 0x3dcccccd, v134
	v_fma_f32 v130, -v133, v131, v77
	v_fma_f32 v246, -v135, v1, v13
	v_fmac_f32_e32 v132, 0x3dcccccd, v130
	v_fmac_f32_e32 v134, 0x3dcccccd, v246
	v_fmac_f32_e32 v133, 0x3dcccccd, v132
	v_fmac_f32_e32 v135, 0x3dcccccd, v134
	v_fma_f32 v130, -v133, v131, v78
	v_fma_f32 v246, -v135, v1, v14
	v_fmac_f32_e32 v132, 0x3dcccccd, v130
	v_fmac_f32_e32 v134, 0x3dcccccd, v246
	v_fmac_f32_e32 v133, 0x3dcccccd, v132
	v_fmac_f32_e32 v135, 0x3dcccccd, v134
	v_fma_f32 v130, -v133, v131, v79
	v_fma_f32 v246, -v135, v1, v15
	v_fmac_f32_e32 v132, 0x3dcccccd, v130
	v_fmac_f32_e32 v134, 0x3dcccccd, v246
	v_fmac_f32_e32 v133, 0x3dcccccd, v132
	v_fmac_f32_e32 v135, 0x3dcccccd, v134
	v_fma_f32 v130, -v133, v131, v80
	v_fma_f32 v246, -v135, v1, v16
	v_fmac_f32_e32 v132, 0x3dcccccd, v130
	v_fmac_f32_e32 v134, 0x3dcccccd, v246
	v_fmac_f32_e32 v133, 0x3dcccccd, v132
	v_fmac_f32_e32 v135, 0x3dcccccd, v134
	v_fma_f32 v130, -v133, v131, v81
	v_fma_f32 v246, -v135, v1, v17
	v_fmac_f32_e32 v132, 0x3dcccccd, v130
	v_fmac_f32_e32 v134, 0x3dcccccd, v246
	v_fmac_f32_e32 v133, 0x3dcccccd, v132
	v_fmac_f32_e32 v135, 0x3dcccccd, v134
	v_lshlrev_b32_e32 v142, 3, v203
	v_lshlrev_b32_e32 v140, 3, v204
	v_add3_u32 v150, 0, v142, v140
	s_mov_b32 s10, 0xbc23d70b
	v_lshl_add_u32 v0, v202, 12, v150
	v_fma_f32 v130, v131, s10, 1.0
	ds_write2_b64 v0, v[132:133], v[134:135] offset1:32
	v_pk_mul_f32 v[132:133], v[130:131], s[6:7]
	s_lshl_b64 s[2:3], s[2:3], 13
	v_mov_b32_e32 v132, v130
	v_pk_mul_f32 v[136:137], v[132:133], s[6:7] op_sel_hi:[1,0]
	v_pk_mul_f32 v[138:139], v[130:131], v[132:133] op_sel_hi:[0,1]
	v_add_f32_e32 v0, 1.0, v137
	v_mov_b32_e32 v136, v137
	v_mov_b32_e32 v137, v133
	v_pk_fma_f32 v[144:145], v[130:131], v[132:133], v[136:137] op_sel_hi:[0,1,1]
	v_mov_b32_e32 v136, 0x3dcccccd
	v_mov_b32_e32 v137, v139
	v_pk_fma_f32 v[146:147], v[130:131], s[6:7], v[136:137]
	v_mov_b32_e32 v137, v138
	v_pk_fma_f32 v[132:133], v[132:133], s[6:7], v[136:137] op_sel_hi:[1,0,1]
	v_mov_b32_e32 v152, v144
	v_pk_mul_f32 v[132:133], v[144:145], v[132:133]
	v_mov_b32_e32 v145, v147
	v_mov_b32_e32 v153, v146
	v_mov_b32_e32 v138, v147
	v_mov_b32_e32 v139, v0
	v_mov_b32_e32 v148, v146
	v_mov_b32_e32 v149, v0
	v_pk_mul_f32 v[144:145], v[144:145], v[152:153]
	v_pk_fma_f32 v[132:133], v[0:1], v[146:147], v[132:133] op_sel_hi:[0,1,1]
	v_pk_fma_f32 v[138:139], v[138:139], v[148:149], v[144:145]
	s_add_u32 s8, s4, s2
	v_pk_mul_f32 v[144:145], v[132:133], v[138:139] op_sel_hi:[1,0]
	s_waitcnt lgkmcnt(0)
	v_pk_fma_f32 v[144:145], v[138:139], v[132:133], v[144:145] op_sel:[1,0,0]
	v_pk_mul_f32 v[132:133], v[132:133], v[132:133] op_sel:[1,0] op_sel_hi:[1,0]
	s_barrier
	v_pk_fma_f32 v[132:133], v[138:139], v[138:139], v[132:133]
	s_nop 0
	v_pk_mul_f32 v[138:139], v[144:145], v[132:133] op_sel_hi:[1,0]
	s_addc_u32 s3, s5, s3
	v_pk_fma_f32 v[138:139], v[132:133], v[144:145], v[138:139] op_sel:[1,0,0]
	v_pk_mul_f32 v[144:145], v[144:145], v[144:145] op_sel:[1,0] op_sel_hi:[1,0]
	s_lshl_b32 s2, s34, 3
	v_pk_fma_f32 v[132:133], v[132:133], v[132:133], v[144:145]
	ds_read_b64 v[148:149], v150
	v_pk_mul_f32 v[144:145], v[138:139], v[132:133] op_sel_hi:[1,0]
	s_add_u32 s8, s8, s2
	v_pk_fma_f32 v[144:145], v[132:133], v[138:139], v[144:145] op_sel:[1,0,0]
	v_pk_mul_f32 v[138:139], v[138:139], v[138:139] op_sel:[1,0] op_sel_hi:[1,0]
	v_mov_b32_e32 v143, 0
	v_pk_fma_f32 v[132:133], v[132:133], v[132:133], v[138:139]
	s_addc_u32 s9, s3, 0
	v_pk_mul_f32 v[138:139], v[132:133], v[132:133]
	v_pk_mul_f32 v[146:147], v[144:145], v[132:133] op_sel_hi:[1,0]
	v_mov_b32_e32 v141, v143
	v_pk_fma_f32 v[132:133], v[132:133], v[144:145], v[146:147] op_sel:[1,0,0]
	v_pk_fma_f32 v[146:147], v[144:145], v[144:145], v[138:139] op_sel:[1,0,0] op_sel_hi:[1,0,1]
	v_lshl_add_u64 v[138:139], s[8:9], 0, v[142:143]
	v_mov_b32_e32 v135, 1.0
	v_cmp_eq_u32_e64 s[0:1], 0, v202
	v_cmp_ne_u32_e32 vcc, 0, v202
	v_lshl_add_u64 v[144:145], v[138:139], 0, v[140:141]
	s_and_saveexec_b64 s[8:9], vcc
	s_cbranch_execz .LBB1_18
	ds_read_b64 v[138:139], v150 offset:4096
	v_mov_b32_e32 v152, v147
	v_mov_b32_e32 v153, v133
	s_waitcnt lgkmcnt(1)
	v_pk_mul_f32 v[152:153], v[148:149], v[152:153]
	s_nop 0
	v_add_f32_e32 v0, v152, v153
	v_mov_b32_e32 v152, v132
	v_mov_b32_e32 v153, v146
	v_pk_mul_f32 v[152:153], v[148:149], v[152:153]
	s_waitcnt lgkmcnt(0)
	v_add_f32_e32 v0, v138, v0
	v_add_f32_e32 v130, v152, v153
	v_add_f32_e32 v130, v139, v130
	v_or_b32_e32 v139, 1, v130
	v_or_b32_e32 v138, 1, v0
	global_store_dwordx2 v[144:145], v[138:139], off sc1

.Lmg_np:
	v_cndmask_b32_e64 v227, v145, v226, s[0:1]
	v_cndmask_b32_e64 v226, v144, v231, s[0:1]
	v_pk_add_f32 v[224:225], v[226:227], v[224:225]
	v_cndmask_b32_e64 v230, v135, 0, s[0:1]
	v_pk_mul_f32 v[228:229], v[224:225], v[138:139] op_sel:[1,0] op_sel_hi:[0,1]
	v_pk_mov_b32 v[226:227], v[224:225], v[224:225] op_sel:[1,0]
	v_pk_fma_f32 v[224:225], v[224:225], v[136:137], v[228:229]
	v_cndmask_b32_e64 v228, v134, 0, s[0:1]
	v_cndmask_b32_e64 v224, v224, v226, s[0:1]
	v_cndmask_b32_e64 v225, v225, v227, s[0:1]
	v_add_f32_e32 v230, v224, v230
	v_add_f32_e32 v228, v225, v228
	v_lshlrev_b32_e32 v232, 2, v150
	s_add_u32 s44, s18, 0x4000000
	s_addc_u32 s45, s19, 0
	s_add_u32 s46, s18, 0x8000000
	s_addc_u32 s47, s19, 0
	s_mov_b32 s48, 0x3dcccccd
	v_mov_b32_e32 v237, v232
	v_mov_b32_e32 v232, v237
	v_mov_b32_e32 v235, v232
	v_mov_b32_e32 v236, v232
	v_fma_f32 v233, -v130, v131, v82
	v_fmac_f32_e32 v152, 0x3dcccccd, v233
	v_fma_f32 v82, s48, v152, v130
	global_store_dword v232, v82, s[18:19]
	v_add_u32_e32 v232, 0x1000, v232
	global_store_dword v235, v152, s[44:45]
	v_add_u32_e32 v235, 0x1000, v235
	global_store_dword v236, v82, s[46:47]
	v_add_u32_e32 v236, 0x1000, v236
	v_fma_f32 v233, -v82, v131, v83
	v_fmac_f32_e32 v152, 0x3dcccccd, v233
	v_fma_f32 v83, s48, v152, v82
	global_store_dword v232, v83, s[18:19]
	v_add_u32_e32 v232, 0x1000, v232
	global_store_dword v235, v152, s[44:45]
	v_add_u32_e32 v235, 0x1000, v235
	global_store_dword v236, v83, s[46:47]
	v_add_u32_e32 v236, 0x1000, v236
	v_fma_f32 v233, -v83, v131, v84
	v_fmac_f32_e32 v152, 0x3dcccccd, v233
	v_fma_f32 v84, s48, v152, v83
	global_store_dword v232, v84, s[18:19]
	v_add_u32_e32 v232, 0x1000, v232
	global_store_dword v235, v152, s[44:45]
	v_add_u32_e32 v235, 0x1000, v235
	global_store_dword v236, v84, s[46:47]
	v_add_u32_e32 v236, 0x1000, v236
	v_fma_f32 v233, -v84, v131, v85
	v_fmac_f32_e32 v152, 0x3dcccccd, v233
	v_fma_f32 v85, s48, v152, v84
	global_store_dword v232, v85, s[18:19]
	v_add_u32_e32 v232, 0x1000, v232
	global_store_dword v235, v152, s[44:45]
	v_add_u32_e32 v235, 0x1000, v235
	global_store_dword v236, v85, s[46:47]
	v_add_u32_e32 v236, 0x1000, v236
	v_fma_f32 v233, -v85, v131, v86
	v_fmac_f32_e32 v152, 0x3dcccccd, v233
	v_fma_f32 v86, s48, v152, v85
	global_store_dword v232, v86, s[18:19]
	v_add_u32_e32 v232, 0x1000, v232
	global_store_dword v235, v152, s[44:45]
	v_add_u32_e32 v235, 0x1000, v235
	global_store_dword v236, v86, s[46:47]
	v_add_u32_e32 v236, 0x1000, v236
	v_fma_f32 v233, -v86, v131, v87
	v_fmac_f32_e32 v152, 0x3dcccccd, v233
	v_fma_f32 v87, s48, v152, v86
	global_store_dword v232, v87, s[18:19]
	v_add_u32_e32 v232, 0x1000, v232
	global_store_dword v235, v152, s[44:45]
	v_add_u32_e32 v235, 0x1000, v235
	global_store_dword v236, v87, s[46:47]
	v_add_u32_e32 v236, 0x1000, v236
	v_fma_f32 v233, -v87, v131, v88
	v_fmac_f32_e32 v152, 0x3dcccccd, v233
	v_fma_f32 v88, s48, v152, v87
	global_store_dword v232, v88, s[18:19]
	v_add_u32_e32 v232, 0x1000, v232
	global_store_dword v235, v152, s[44:45]
	v_add_u32_e32 v235, 0x1000, v235
	global_store_dword v236, v88, s[46:47]
	v_add_u32_e32 v236, 0x1000, v236
	v_fma_f32 v233, -v88, v131, v89
	v_fmac_f32_e32 v152, 0x3dcccccd, v233
	v_fma_f32 v89, s48, v152, v88
	global_store_dword v232, v89, s[18:19]
	v_add_u32_e32 v232, 0x1000, v232
	global_store_dword v235, v152, s[44:45]
	v_add_u32_e32 v235, 0x1000, v235
	global_store_dword v236, v89, s[46:47]
	v_add_u32_e32 v236, 0x1000, v236
	v_fma_f32 v233, -v89, v131, v90
	v_fmac_f32_e32 v152, 0x3dcccccd, v233
	v_fma_f32 v90, s48, v152, v89
	global_store_dword v232, v90, s[18:19]
	v_add_u32_e32 v232, 0x1000, v232
	global_store_dword v235, v152, s[44:45]
	v_add_u32_e32 v235, 0x1000, v235
	global_store_dword v236, v90, s[46:47]
	v_add_u32_e32 v236, 0x1000, v236
	v_fma_f32 v233, -v90, v131, v91
	v_fmac_f32_e32 v152, 0x3dcccccd, v233
	v_fma_f32 v91, s48, v152, v90
	global_store_dword v232, v91, s[18:19]
	v_add_u32_e32 v232, 0x1000, v232
	global_store_dword v235, v152, s[44:45]
	v_add_u32_e32 v235, 0x1000, v235
	global_store_dword v236, v91, s[46:47]
	v_add_u32_e32 v236, 0x1000, v236
	v_fma_f32 v233, -v91, v131, v92
	v_fmac_f32_e32 v152, 0x3dcccccd, v233
	v_fma_f32 v92, s48, v152, v91
	global_store_dword v232, v92, s[18:19]
	v_add_u32_e32 v232, 0x1000, v232
	global_store_dword v235, v152, s[44:45]
	v_add_u32_e32 v235, 0x1000, v235
	global_store_dword v236, v92, s[46:47]
	v_add_u32_e32 v236, 0x1000, v236
	v_fma_f32 v233, -v92, v131, v93
	v_fmac_f32_e32 v152, 0x3dcccccd, v233
	v_fma_f32 v93, s48, v152, v92
	global_store_dword v232, v93, s[18:19]
	v_add_u32_e32 v232, 0x1000, v232
	global_store_dword v235, v152, s[44:45]
	v_add_u32_e32 v235, 0x1000, v235
	global_store_dword v236, v93, s[46:47]
	v_add_u32_e32 v236, 0x1000, v236
	v_fma_f32 v233, -v93, v131, v94
	v_fmac_f32_e32 v152, 0x3dcccccd, v233
	v_fma_f32 v94, s48, v152, v93
	global_store_dword v232, v94, s[18:19]
	v_add_u32_e32 v232, 0x1000, v232
	global_store_dword v235, v152, s[44:45]
	v_add_u32_e32 v235, 0x1000, v235
	global_store_dword v236, v94, s[46:47]
	v_add_u32_e32 v236, 0x1000, v236
	v_fma_f32 v233, -v94, v131, v95
	v_fmac_f32_e32 v152, 0x3dcccccd, v233
	v_fma_f32 v95, s48, v152, v94
	global_store_dword v232, v95, s[18:19]
	v_add_u32_e32 v232, 0x1000, v232
	global_store_dword v235, v152, s[44:45]
	v_add_u32_e32 v235, 0x1000, v235
	global_store_dword v236, v95, s[46:47]
	v_add_u32_e32 v236, 0x1000, v236
	v_fma_f32 v233, -v95, v131, v96
	v_fmac_f32_e32 v152, 0x3dcccccd, v233
	v_fma_f32 v96, s48, v152, v95
	global_store_dword v232, v96, s[18:19]
	v_add_u32_e32 v232, 0x1000, v232
	global_store_dword v235, v152, s[44:45]
	v_add_u32_e32 v235, 0x1000, v235
	global_store_dword v236, v96, s[46:47]
	v_add_u32_e32 v236, 0x1000, v236
	v_fma_f32 v233, -v96, v131, v97
	v_fmac_f32_e32 v152, 0x3dcccccd, v233
	v_fma_f32 v97, s48, v152, v96
	global_store_dword v232, v97, s[18:19]
	v_add_u32_e32 v232, 0x1000, v232
	global_store_dword v235, v152, s[44:45]
	v_add_u32_e32 v235, 0x1000, v235
	global_store_dword v236, v97, s[46:47]
	v_add_u32_e32 v236, 0x1000, v236
	v_fma_f32 v233, -v97, v131, v114
	v_fmac_f32_e32 v152, 0x3dcccccd, v233
	v_fma_f32 v114, s48, v152, v97
	global_store_dword v232, v114, s[18:19]
	v_add_u32_e32 v232, 0x1000, v232
	global_store_dword v235, v152, s[44:45]
	v_add_u32_e32 v235, 0x1000, v235
	global_store_dword v236, v114, s[46:47]
	v_add_u32_e32 v236, 0x1000, v236
	v_fma_f32 v233, -v114, v131, v115
	v_fmac_f32_e32 v152, 0x3dcccccd, v233
	v_fma_f32 v115, s48, v152, v114
	global_store_dword v232, v115, s[18:19]
	v_add_u32_e32 v232, 0x1000, v232
	global_store_dword v235, v152, s[44:45]
	v_add_u32_e32 v235, 0x1000, v235
	global_store_dword v236, v115, s[46:47]
	v_add_u32_e32 v236, 0x1000, v236
	v_fma_f32 v233, -v115, v131, v116
	v_fmac_f32_e32 v152, 0x3dcccccd, v233
	v_fma_f32 v116, s48, v152, v115
	global_store_dword v232, v116, s[18:19]
	v_add_u32_e32 v232, 0x1000, v232
	global_store_dword v235, v152, s[44:45]
	v_add_u32_e32 v235, 0x1000, v235
	global_store_dword v236, v116, s[46:47]
	v_add_u32_e32 v236, 0x1000, v236
	v_fma_f32 v233, -v116, v131, v117
	v_fmac_f32_e32 v152, 0x3dcccccd, v233
	v_fma_f32 v117, s48, v152, v116
	global_store_dword v232, v117, s[18:19]
	v_add_u32_e32 v232, 0x1000, v232
	global_store_dword v235, v152, s[44:45]
	v_add_u32_e32 v235, 0x1000, v235
	global_store_dword v236, v117, s[46:47]
	v_add_u32_e32 v236, 0x1000, v236
	v_fma_f32 v233, -v117, v131, v118
	v_fmac_f32_e32 v152, 0x3dcccccd, v233
	v_fma_f32 v118, s48, v152, v117
	global_store_dword v232, v118, s[18:19]
	v_add_u32_e32 v232, 0x1000, v232
	global_store_dword v235, v152, s[44:45]
	v_add_u32_e32 v235, 0x1000, v235
	global_store_dword v236, v118, s[46:47]
	v_add_u32_e32 v236, 0x1000, v236
	v_fma_f32 v233, -v118, v131, v119
	v_fmac_f32_e32 v152, 0x3dcccccd, v233
	v_fma_f32 v119, s48, v152, v118
	global_store_dword v232, v119, s[18:19]
	v_add_u32_e32 v232, 0x1000, v232
	global_store_dword v235, v152, s[44:45]
	v_add_u32_e32 v235, 0x1000, v235
	global_store_dword v236, v119, s[46:47]
	v_add_u32_e32 v236, 0x1000, v236
	v_fma_f32 v233, -v119, v131, v120
	v_fmac_f32_e32 v152, 0x3dcccccd, v233
	v_fma_f32 v120, s48, v152, v119
	global_store_dword v232, v120, s[18:19]
	v_add_u32_e32 v232, 0x1000, v232
	global_store_dword v235, v152, s[44:45]
	v_add_u32_e32 v235, 0x1000, v235
	global_store_dword v236, v120, s[46:47]
	v_add_u32_e32 v236, 0x1000, v236
	v_fma_f32 v233, -v120, v131, v121
	v_fmac_f32_e32 v152, 0x3dcccccd, v233
	v_fma_f32 v121, s48, v152, v120
	global_store_dword v232, v121, s[18:19]
	v_add_u32_e32 v232, 0x1000, v232
	global_store_dword v235, v152, s[44:45]
	v_add_u32_e32 v235, 0x1000, v235
	global_store_dword v236, v121, s[46:47]
	v_add_u32_e32 v236, 0x1000, v236
	v_fma_f32 v233, -v121, v131, v122
	v_fmac_f32_e32 v152, 0x3dcccccd, v233
	v_fma_f32 v122, s48, v152, v121
	global_store_dword v232, v122, s[18:19]
	v_add_u32_e32 v232, 0x1000, v232
	global_store_dword v235, v152, s[44:45]
	v_add_u32_e32 v235, 0x1000, v235
	global_store_dword v236, v122, s[46:47]
	v_add_u32_e32 v236, 0x1000, v236
	v_fma_f32 v233, -v122, v131, v123
	v_fmac_f32_e32 v152, 0x3dcccccd, v233
	v_fma_f32 v123, s48, v152, v122
	global_store_dword v232, v123, s[18:19]
	v_add_u32_e32 v232, 0x1000, v232
	global_store_dword v235, v152, s[44:45]
	v_add_u32_e32 v235, 0x1000, v235
	global_store_dword v236, v123, s[46:47]
	v_add_u32_e32 v236, 0x1000, v236
	v_fma_f32 v233, -v123, v131, v124
	v_fmac_f32_e32 v152, 0x3dcccccd, v233
	v_fma_f32 v124, s48, v152, v123
	global_store_dword v232, v124, s[18:19]
	v_add_u32_e32 v232, 0x1000, v232
	global_store_dword v235, v152, s[44:45]
	v_add_u32_e32 v235, 0x1000, v235
	global_store_dword v236, v124, s[46:47]
	v_add_u32_e32 v236, 0x1000, v236
	v_fma_f32 v233, -v124, v131, v125
	v_fmac_f32_e32 v152, 0x3dcccccd, v233
	v_fma_f32 v125, s48, v152, v124
	global_store_dword v232, v125, s[18:19]
	v_add_u32_e32 v232, 0x1000, v232
	global_store_dword v235, v152, s[44:45]
	v_add_u32_e32 v235, 0x1000, v235
	global_store_dword v236, v125, s[46:47]
	v_add_u32_e32 v236, 0x1000, v236
	v_fma_f32 v233, -v125, v131, v126
	v_fmac_f32_e32 v152, 0x3dcccccd, v233
	v_fma_f32 v126, s48, v152, v125
	global_store_dword v232, v126, s[18:19]
	v_add_u32_e32 v232, 0x1000, v232
	global_store_dword v235, v152, s[44:45]
	v_add_u32_e32 v235, 0x1000, v235
	global_store_dword v236, v126, s[46:47]
	v_add_u32_e32 v236, 0x1000, v236
	v_fma_f32 v233, -v126, v131, v127
	v_fmac_f32_e32 v152, 0x3dcccccd, v233
	v_fma_f32 v127, s48, v152, v126
	global_store_dword v232, v127, s[18:19]
	v_add_u32_e32 v232, 0x1000, v232
	global_store_dword v235, v152, s[44:45]
	v_add_u32_e32 v235, 0x1000, v235
	global_store_dword v236, v127, s[46:47]
	v_add_u32_e32 v236, 0x1000, v236
	v_fma_f32 v233, -v127, v131, v128
	v_fmac_f32_e32 v152, 0x3dcccccd, v233
	v_fma_f32 v128, s48, v152, v127
	global_store_dword v232, v128, s[18:19]
	v_add_u32_e32 v232, 0x1000, v232
	global_store_dword v235, v152, s[44:45]
	v_add_u32_e32 v235, 0x1000, v235
	global_store_dword v236, v128, s[46:47]
	v_add_u32_e32 v236, 0x1000, v236
	v_fma_f32 v233, -v128, v131, v129
	v_fmac_f32_e32 v152, 0x3dcccccd, v233
	v_fma_f32 v129, s48, v152, v128
	global_store_dword v232, v129, s[18:19]
	v_add_u32_e32 v232, 0x1000, v232
	global_store_dword v235, v152, s[44:45]
	v_add_u32_e32 v235, 0x1000, v235
	global_store_dword v236, v129, s[46:47]
	v_add_u32_e32 v236, 0x1000, v236
	v_fma_f32 v233, -v129, v131, v98
	v_fmac_f32_e32 v152, 0x3dcccccd, v233
	v_fma_f32 v98, s48, v152, v129
	global_store_dword v232, v98, s[18:19]
	v_add_u32_e32 v232, 0x1000, v232
	global_store_dword v235, v152, s[44:45]
	v_add_u32_e32 v235, 0x1000, v235
	global_store_dword v236, v98, s[46:47]
	v_add_u32_e32 v236, 0x1000, v236
	v_fma_f32 v233, -v98, v131, v99
	v_fmac_f32_e32 v152, 0x3dcccccd, v233
	v_fma_f32 v99, s48, v152, v98
	global_store_dword v232, v99, s[18:19]
	v_add_u32_e32 v232, 0x1000, v232
	global_store_dword v235, v152, s[44:45]
	v_add_u32_e32 v235, 0x1000, v235
	global_store_dword v236, v99, s[46:47]
	v_add_u32_e32 v236, 0x1000, v236
	v_fma_f32 v233, -v99, v131, v100
	v_fmac_f32_e32 v152, 0x3dcccccd, v233
	v_fma_f32 v100, s48, v152, v99
	global_store_dword v232, v100, s[18:19]
	v_add_u32_e32 v232, 0x1000, v232
	global_store_dword v235, v152, s[44:45]
	v_add_u32_e32 v235, 0x1000, v235
	global_store_dword v236, v100, s[46:47]
	v_add_u32_e32 v236, 0x1000, v236
	v_fma_f32 v233, -v100, v131, v101
	v_fmac_f32_e32 v152, 0x3dcccccd, v233
	v_fma_f32 v101, s48, v152, v100
	global_store_dword v232, v101, s[18:19]
	v_add_u32_e32 v232, 0x1000, v232
	global_store_dword v235, v152, s[44:45]
	v_add_u32_e32 v235, 0x1000, v235
	global_store_dword v236, v101, s[46:47]
	v_add_u32_e32 v236, 0x1000, v236
	v_fma_f32 v233, -v101, v131, v102
	v_fmac_f32_e32 v152, 0x3dcccccd, v233
	v_fma_f32 v102, s48, v152, v101
	global_store_dword v232, v102, s[18:19]
	v_add_u32_e32 v232, 0x1000, v232
	global_store_dword v235, v152, s[44:45]
	v_add_u32_e32 v235, 0x1000, v235
	global_store_dword v236, v102, s[46:47]
	v_add_u32_e32 v236, 0x1000, v236
	v_fma_f32 v233, -v102, v131, v103
	v_fmac_f32_e32 v152, 0x3dcccccd, v233
	v_fma_f32 v103, s48, v152, v102
	global_store_dword v232, v103, s[18:19]
	v_add_u32_e32 v232, 0x1000, v232
	global_store_dword v235, v152, s[44:45]
	v_add_u32_e32 v235, 0x1000, v235
	global_store_dword v236, v103, s[46:47]
	v_add_u32_e32 v236, 0x1000, v236
	v_fma_f32 v233, -v103, v131, v104
	v_fmac_f32_e32 v152, 0x3dcccccd, v233
	v_fma_f32 v104, s48, v152, v103
	global_store_dword v232, v104, s[18:19]
	v_add_u32_e32 v232, 0x1000, v232
	global_store_dword v235, v152, s[44:45]
	v_add_u32_e32 v235, 0x1000, v235
	global_store_dword v236, v104, s[46:47]
	v_add_u32_e32 v236, 0x1000, v236
	v_fma_f32 v233, -v104, v131, v105
	v_fmac_f32_e32 v152, 0x3dcccccd, v233
	v_fma_f32 v105, s48, v152, v104
	global_store_dword v232, v105, s[18:19]
	v_add_u32_e32 v232, 0x1000, v232
	global_store_dword v235, v152, s[44:45]
	v_add_u32_e32 v235, 0x1000, v235
	global_store_dword v236, v105, s[46:47]
	v_add_u32_e32 v236, 0x1000, v236
	v_fma_f32 v233, -v105, v131, v106
	v_fmac_f32_e32 v152, 0x3dcccccd, v233
	v_fma_f32 v106, s48, v152, v105
	global_store_dword v232, v106, s[18:19]
	v_add_u32_e32 v232, 0x1000, v232
	global_store_dword v235, v152, s[44:45]
	v_add_u32_e32 v235, 0x1000, v235
	global_store_dword v236, v106, s[46:47]
	v_add_u32_e32 v236, 0x1000, v236
	v_fma_f32 v233, -v106, v131, v107
	v_fmac_f32_e32 v152, 0x3dcccccd, v233
	v_fma_f32 v107, s48, v152, v106
	global_store_dword v232, v107, s[18:19]
	v_add_u32_e32 v232, 0x1000, v232
	global_store_dword v235, v152, s[44:45]
	v_add_u32_e32 v235, 0x1000, v235
	global_store_dword v236, v107, s[46:47]
	v_add_u32_e32 v236, 0x1000, v236
	v_fma_f32 v233, -v107, v131, v108
	v_fmac_f32_e32 v152, 0x3dcccccd, v233
	v_fma_f32 v108, s48, v152, v107
	global_store_dword v232, v108, s[18:19]
	v_add_u32_e32 v232, 0x1000, v232
	global_store_dword v235, v152, s[44:45]
	v_add_u32_e32 v235, 0x1000, v235
	global_store_dword v236, v108, s[46:47]
	v_add_u32_e32 v236, 0x1000, v236
	v_fma_f32 v233, -v108, v131, v109
	v_fmac_f32_e32 v152, 0x3dcccccd, v233
	v_fma_f32 v109, s48, v152, v108
	global_store_dword v232, v109, s[18:19]
	v_add_u32_e32 v232, 0x1000, v232
	global_store_dword v235, v152, s[44:45]
	v_add_u32_e32 v235, 0x1000, v235
	global_store_dword v236, v109, s[46:47]
	v_add_u32_e32 v236, 0x1000, v236
	v_fma_f32 v233, -v109, v131, v110
	v_fmac_f32_e32 v152, 0x3dcccccd, v233
	v_fma_f32 v110, s48, v152, v109
	global_store_dword v232, v110, s[18:19]
	v_add_u32_e32 v232, 0x1000, v232
	global_store_dword v235, v152, s[44:45]
	v_add_u32_e32 v235, 0x1000, v235
	global_store_dword v236, v110, s[46:47]
	v_add_u32_e32 v236, 0x1000, v236
	v_fma_f32 v233, -v110, v131, v111
	v_fmac_f32_e32 v152, 0x3dcccccd, v233
	v_fma_f32 v111, s48, v152, v110
	global_store_dword v232, v111, s[18:19]
	v_add_u32_e32 v232, 0x1000, v232
	global_store_dword v235, v152, s[44:45]
	v_add_u32_e32 v235, 0x1000, v235
	global_store_dword v236, v111, s[46:47]
	v_add_u32_e32 v236, 0x1000, v236
	v_fma_f32 v233, -v111, v131, v112
	v_fmac_f32_e32 v152, 0x3dcccccd, v233
	v_fma_f32 v112, s48, v152, v111
	global_store_dword v232, v112, s[18:19]
	v_add_u32_e32 v232, 0x1000, v232
	global_store_dword v235, v152, s[44:45]
	v_add_u32_e32 v235, 0x1000, v235
	global_store_dword v236, v112, s[46:47]
	v_add_u32_e32 v236, 0x1000, v236
	v_fma_f32 v233, -v112, v131, v113
	v_fmac_f32_e32 v152, 0x3dcccccd, v233
	v_fma_f32 v113, s48, v152, v112
	global_store_dword v232, v113, s[18:19]
	v_add_u32_e32 v232, 0x1000, v232
	global_store_dword v235, v152, s[44:45]
	v_add_u32_e32 v235, 0x1000, v235
	global_store_dword v236, v113, s[46:47]
	v_add_u32_e32 v236, 0x1000, v236
	v_fma_f32 v233, -v113, v131, v66
	v_fmac_f32_e32 v152, 0x3dcccccd, v233
	v_fma_f32 v66, s48, v152, v113
	global_store_dword v232, v66, s[18:19]
	v_add_u32_e32 v232, 0x1000, v232
	global_store_dword v235, v152, s[44:45]
	v_add_u32_e32 v235, 0x1000, v235
	global_store_dword v236, v66, s[46:47]
	v_add_u32_e32 v236, 0x1000, v236
	v_fma_f32 v233, -v66, v131, v67
	v_fmac_f32_e32 v152, 0x3dcccccd, v233
	v_fma_f32 v67, s48, v152, v66
	global_store_dword v232, v67, s[18:19]
	v_add_u32_e32 v232, 0x1000, v232
	global_store_dword v235, v152, s[44:45]
	v_add_u32_e32 v235, 0x1000, v235
	global_store_dword v236, v67, s[46:47]
	v_add_u32_e32 v236, 0x1000, v236
	v_fma_f32 v233, -v67, v131, v68
	v_fmac_f32_e32 v152, 0x3dcccccd, v233
	v_fma_f32 v68, s48, v152, v67
	global_store_dword v232, v68, s[18:19]
	v_add_u32_e32 v232, 0x1000, v232
	global_store_dword v235, v152, s[44:45]
	v_add_u32_e32 v235, 0x1000, v235
	global_store_dword v236, v68, s[46:47]
	v_add_u32_e32 v236, 0x1000, v236
	v_fma_f32 v233, -v68, v131, v69
	v_fmac_f32_e32 v152, 0x3dcccccd, v233
	v_fma_f32 v69, s48, v152, v68
	global_store_dword v232, v69, s[18:19]
	v_add_u32_e32 v232, 0x1000, v232
	global_store_dword v235, v152, s[44:45]
	v_add_u32_e32 v235, 0x1000, v235
	global_store_dword v236, v69, s[46:47]
	v_add_u32_e32 v236, 0x1000, v236
	v_fma_f32 v233, -v69, v131, v70
	v_fmac_f32_e32 v152, 0x3dcccccd, v233
	v_fma_f32 v70, s48, v152, v69
	global_store_dword v232, v70, s[18:19]
	v_add_u32_e32 v232, 0x1000, v232
	global_store_dword v235, v152, s[44:45]
	v_add_u32_e32 v235, 0x1000, v235
	global_store_dword v236, v70, s[46:47]
	v_add_u32_e32 v236, 0x1000, v236
	v_fma_f32 v233, -v70, v131, v71
	v_fmac_f32_e32 v152, 0x3dcccccd, v233
	v_fma_f32 v71, s48, v152, v70
	global_store_dword v232, v71, s[18:19]
	v_add_u32_e32 v232, 0x1000, v232
	global_store_dword v235, v152, s[44:45]
	v_add_u32_e32 v235, 0x1000, v235
	global_store_dword v236, v71, s[46:47]
	v_add_u32_e32 v236, 0x1000, v236
	v_fma_f32 v233, -v71, v131, v72
	v_fmac_f32_e32 v152, 0x3dcccccd, v233
	v_fma_f32 v72, s48, v152, v71
	global_store_dword v232, v72, s[18:19]
	v_add_u32_e32 v232, 0x1000, v232
	global_store_dword v235, v152, s[44:45]
	v_add_u32_e32 v235, 0x1000, v235
	global_store_dword v236, v72, s[46:47]
	v_add_u32_e32 v236, 0x1000, v236
	v_fma_f32 v233, -v72, v131, v73
	v_fmac_f32_e32 v152, 0x3dcccccd, v233
	v_fma_f32 v73, s48, v152, v72
	global_store_dword v232, v73, s[18:19]
	v_add_u32_e32 v232, 0x1000, v232
	global_store_dword v235, v152, s[44:45]
	v_add_u32_e32 v235, 0x1000, v235
	global_store_dword v236, v73, s[46:47]
	v_add_u32_e32 v236, 0x1000, v236
	v_fma_f32 v233, -v73, v131, v74
	v_fmac_f32_e32 v152, 0x3dcccccd, v233
	v_fma_f32 v74, s48, v152, v73
	global_store_dword v232, v74, s[18:19]
	v_add_u32_e32 v232, 0x1000, v232
	global_store_dword v235, v152, s[44:45]
	v_add_u32_e32 v235, 0x1000, v235
	global_store_dword v236, v74, s[46:47]
	v_add_u32_e32 v236, 0x1000, v236
	v_fma_f32 v233, -v74, v131, v75
	v_fmac_f32_e32 v152, 0x3dcccccd, v233
	v_fma_f32 v75, s48, v152, v74
	global_store_dword v232, v75, s[18:19]
	v_add_u32_e32 v232, 0x1000, v232
	global_store_dword v235, v152, s[44:45]
	v_add_u32_e32 v235, 0x1000, v235
	global_store_dword v236, v75, s[46:47]
	v_add_u32_e32 v236, 0x1000, v236
	v_fma_f32 v233, -v75, v131, v76
	v_fmac_f32_e32 v152, 0x3dcccccd, v233
	v_fma_f32 v76, s48, v152, v75
	global_store_dword v232, v76, s[18:19]
	v_add_u32_e32 v232, 0x1000, v232
	global_store_dword v235, v152, s[44:45]
	v_add_u32_e32 v235, 0x1000, v235
	global_store_dword v236, v76, s[46:47]
	v_add_u32_e32 v236, 0x1000, v236
	v_fma_f32 v233, -v76, v131, v77
	v_fmac_f32_e32 v152, 0x3dcccccd, v233
	v_fma_f32 v77, s48, v152, v76
	global_store_dword v232, v77, s[18:19]
	v_add_u32_e32 v232, 0x1000, v232
	global_store_dword v235, v152, s[44:45]
	v_add_u32_e32 v235, 0x1000, v235
	global_store_dword v236, v77, s[46:47]
	v_add_u32_e32 v236, 0x1000, v236
	v_fma_f32 v233, -v77, v131, v78
	v_fmac_f32_e32 v152, 0x3dcccccd, v233
	v_fma_f32 v78, s48, v152, v77
	global_store_dword v232, v78, s[18:19]
	v_add_u32_e32 v232, 0x1000, v232
	global_store_dword v235, v152, s[44:45]
	v_add_u32_e32 v235, 0x1000, v235
	global_store_dword v236, v78, s[46:47]
	v_add_u32_e32 v236, 0x1000, v236
	v_fma_f32 v233, -v78, v131, v79
	v_fmac_f32_e32 v152, 0x3dcccccd, v233
	v_fma_f32 v79, s48, v152, v78
	global_store_dword v232, v79, s[18:19]
	v_add_u32_e32 v232, 0x1000, v232
	global_store_dword v235, v152, s[44:45]
	v_add_u32_e32 v235, 0x1000, v235
	global_store_dword v236, v79, s[46:47]
	v_add_u32_e32 v236, 0x1000, v236
	v_fma_f32 v233, -v79, v131, v80
	v_fmac_f32_e32 v152, 0x3dcccccd, v233
	v_fma_f32 v80, s48, v152, v79
	global_store_dword v232, v80, s[18:19]
	v_add_u32_e32 v232, 0x1000, v232
	global_store_dword v235, v152, s[44:45]
	v_add_u32_e32 v235, 0x1000, v235
	global_store_dword v236, v80, s[46:47]
	v_add_u32_e32 v236, 0x1000, v236
	v_fma_f32 v233, -v80, v131, v81
	v_fmac_f32_e32 v152, 0x3dcccccd, v233
	v_fma_f32 v81, s48, v152, v80
	global_store_dword v232, v81, s[18:19]
	v_add_u32_e32 v232, 0x1000, v232
	global_store_dword v235, v152, s[44:45]
	v_add_u32_e32 v235, 0x1000, v235
	global_store_dword v236, v81, s[46:47]
	v_add_u32_e32 v236, 0x1000, v236
	v_add_u32_e32 v232, 0x80, v237
	v_mov_b32_e32 v235, v232
	v_mov_b32_e32 v236, v232
	v_fma_f32 v233, -v230, v1, v50
	v_fmac_f32_e32 v228, 0x3dcccccd, v233
	v_fma_f32 v50, s48, v228, v230
	global_store_dword v232, v50, s[18:19]
	v_add_u32_e32 v232, 0x1000, v232
	global_store_dword v235, v228, s[44:45]
	v_add_u32_e32 v235, 0x1000, v235
	global_store_dword v236, v50, s[46:47]
	v_add_u32_e32 v236, 0x1000, v236
	v_fma_f32 v233, -v50, v1, v51
	v_fmac_f32_e32 v228, 0x3dcccccd, v233
	v_fma_f32 v51, s48, v228, v50
	global_store_dword v232, v51, s[18:19]
	v_add_u32_e32 v232, 0x1000, v232
	global_store_dword v235, v228, s[44:45]
	v_add_u32_e32 v235, 0x1000, v235
	global_store_dword v236, v51, s[46:47]
	v_add_u32_e32 v236, 0x1000, v236
	v_fma_f32 v233, -v51, v1, v52
	v_fmac_f32_e32 v228, 0x3dcccccd, v233
	v_fma_f32 v52, s48, v228, v51
	global_store_dword v232, v52, s[18:19]
	v_add_u32_e32 v232, 0x1000, v232
	global_store_dword v235, v228, s[44:45]
	v_add_u32_e32 v235, 0x1000, v235
	global_store_dword v236, v52, s[46:47]
	v_add_u32_e32 v236, 0x1000, v236
	v_fma_f32 v233, -v52, v1, v53
	v_fmac_f32_e32 v228, 0x3dcccccd, v233
	v_fma_f32 v53, s48, v228, v52
	global_store_dword v232, v53, s[18:19]
	v_add_u32_e32 v232, 0x1000, v232
	global_store_dword v235, v228, s[44:45]
	v_add_u32_e32 v235, 0x1000, v235
	global_store_dword v236, v53, s[46:47]
	v_add_u32_e32 v236, 0x1000, v236
	v_fma_f32 v233, -v53, v1, v54
	v_fmac_f32_e32 v228, 0x3dcccccd, v233
	v_fma_f32 v54, s48, v228, v53
	global_store_dword v232, v54, s[18:19]
	v_add_u32_e32 v232, 0x1000, v232
	global_store_dword v235, v228, s[44:45]
	v_add_u32_e32 v235, 0x1000, v235
	global_store_dword v236, v54, s[46:47]
	v_add_u32_e32 v236, 0x1000, v236
	v_fma_f32 v233, -v54, v1, v55
	v_fmac_f32_e32 v228, 0x3dcccccd, v233
	v_fma_f32 v55, s48, v228, v54
	global_store_dword v232, v55, s[18:19]
	v_add_u32_e32 v232, 0x1000, v232
	global_store_dword v235, v228, s[44:45]
	v_add_u32_e32 v235, 0x1000, v235
	global_store_dword v236, v55, s[46:47]
	v_add_u32_e32 v236, 0x1000, v236
	v_fma_f32 v233, -v55, v1, v56
	v_fmac_f32_e32 v228, 0x3dcccccd, v233
	v_fma_f32 v56, s48, v228, v55
	global_store_dword v232, v56, s[18:19]
	v_add_u32_e32 v232, 0x1000, v232
	global_store_dword v235, v228, s[44:45]
	v_add_u32_e32 v235, 0x1000, v235
	global_store_dword v236, v56, s[46:47]
	v_add_u32_e32 v236, 0x1000, v236
	v_fma_f32 v233, -v56, v1, v57
	v_fmac_f32_e32 v228, 0x3dcccccd, v233
	v_fma_f32 v57, s48, v228, v56
	global_store_dword v232, v57, s[18:19]
	v_add_u32_e32 v232, 0x1000, v232
	global_store_dword v235, v228, s[44:45]
	v_add_u32_e32 v235, 0x1000, v235
	global_store_dword v236, v57, s[46:47]
	v_add_u32_e32 v236, 0x1000, v236
	v_fma_f32 v233, -v57, v1, v58
	v_fmac_f32_e32 v228, 0x3dcccccd, v233
	v_fma_f32 v58, s48, v228, v57
	global_store_dword v232, v58, s[18:19]
	v_add_u32_e32 v232, 0x1000, v232
	global_store_dword v235, v228, s[44:45]
	v_add_u32_e32 v235, 0x1000, v235
	global_store_dword v236, v58, s[46:47]
	v_add_u32_e32 v236, 0x1000, v236
	v_fma_f32 v233, -v58, v1, v59
	v_fmac_f32_e32 v228, 0x3dcccccd, v233
	v_fma_f32 v59, s48, v228, v58
	global_store_dword v232, v59, s[18:19]
	v_add_u32_e32 v232, 0x1000, v232
	global_store_dword v235, v228, s[44:45]
	v_add_u32_e32 v235, 0x1000, v235
	global_store_dword v236, v59, s[46:47]
	v_add_u32_e32 v236, 0x1000, v236
	v_fma_f32 v233, -v59, v1, v60
	v_fmac_f32_e32 v228, 0x3dcccccd, v233
	v_fma_f32 v60, s48, v228, v59
	global_store_dword v232, v60, s[18:19]
	v_add_u32_e32 v232, 0x1000, v232
	global_store_dword v235, v228, s[44:45]
	v_add_u32_e32 v235, 0x1000, v235
	global_store_dword v236, v60, s[46:47]
	v_add_u32_e32 v236, 0x1000, v236
	v_fma_f32 v233, -v60, v1, v61
	v_fmac_f32_e32 v228, 0x3dcccccd, v233
	v_fma_f32 v61, s48, v228, v60
	global_store_dword v232, v61, s[18:19]
	v_add_u32_e32 v232, 0x1000, v232
	global_store_dword v235, v228, s[44:45]
	v_add_u32_e32 v235, 0x1000, v235
	global_store_dword v236, v61, s[46:47]
	v_add_u32_e32 v236, 0x1000, v236
	v_fma_f32 v233, -v61, v1, v62
	v_fmac_f32_e32 v228, 0x3dcccccd, v233
	v_fma_f32 v62, s48, v228, v61
	global_store_dword v232, v62, s[18:19]
	v_add_u32_e32 v232, 0x1000, v232
	global_store_dword v235, v228, s[44:45]
	v_add_u32_e32 v235, 0x1000, v235
	global_store_dword v236, v62, s[46:47]
	v_add_u32_e32 v236, 0x1000, v236
	v_fma_f32 v233, -v62, v1, v63
	v_fmac_f32_e32 v228, 0x3dcccccd, v233
	v_fma_f32 v63, s48, v228, v62
	global_store_dword v232, v63, s[18:19]
	v_add_u32_e32 v232, 0x1000, v232
	global_store_dword v235, v228, s[44:45]
	v_add_u32_e32 v235, 0x1000, v235
	global_store_dword v236, v63, s[46:47]
	v_add_u32_e32 v236, 0x1000, v236
	v_fma_f32 v233, -v63, v1, v64
	v_fmac_f32_e32 v228, 0x3dcccccd, v233
	v_fma_f32 v64, s48, v228, v63
	global_store_dword v232, v64, s[18:19]
	v_add_u32_e32 v232, 0x1000, v232
	global_store_dword v235, v228, s[44:45]
	v_add_u32_e32 v235, 0x1000, v235
	global_store_dword v236, v64, s[46:47]
	v_add_u32_e32 v236, 0x1000, v236
	v_fma_f32 v233, -v64, v1, v65
	v_fmac_f32_e32 v228, 0x3dcccccd, v233
	v_fma_f32 v65, s48, v228, v64
	global_store_dword v232, v65, s[18:19]
	v_add_u32_e32 v232, 0x1000, v232
	global_store_dword v235, v228, s[44:45]
	v_add_u32_e32 v235, 0x1000, v235
	global_store_dword v236, v65, s[46:47]
	v_add_u32_e32 v236, 0x1000, v236
	v_fma_f32 v233, -v65, v1, v34
	v_fmac_f32_e32 v228, 0x3dcccccd, v233
	v_fma_f32 v34, s48, v228, v65
	global_store_dword v232, v34, s[18:19]
	v_add_u32_e32 v232, 0x1000, v232
	global_store_dword v235, v228, s[44:45]
	v_add_u32_e32 v235, 0x1000, v235
	global_store_dword v236, v34, s[46:47]
	v_add_u32_e32 v236, 0x1000, v236
	v_fma_f32 v233, -v34, v1, v35
	v_fmac_f32_e32 v228, 0x3dcccccd, v233
	v_fma_f32 v35, s48, v228, v34
	global_store_dword v232, v35, s[18:19]
	v_add_u32_e32 v232, 0x1000, v232
	global_store_dword v235, v228, s[44:45]
	v_add_u32_e32 v235, 0x1000, v235
	global_store_dword v236, v35, s[46:47]
	v_add_u32_e32 v236, 0x1000, v236
	v_fma_f32 v233, -v35, v1, v36
	v_fmac_f32_e32 v228, 0x3dcccccd, v233
	v_fma_f32 v36, s48, v228, v35
	global_store_dword v232, v36, s[18:19]
	v_add_u32_e32 v232, 0x1000, v232
	global_store_dword v235, v228, s[44:45]
	v_add_u32_e32 v235, 0x1000, v235
	global_store_dword v236, v36, s[46:47]
	v_add_u32_e32 v236, 0x1000, v236
	v_fma_f32 v233, -v36, v1, v37
	v_fmac_f32_e32 v228, 0x3dcccccd, v233
	v_fma_f32 v37, s48, v228, v36
	global_store_dword v232, v37, s[18:19]
	v_add_u32_e32 v232, 0x1000, v232
	global_store_dword v235, v228, s[44:45]
	v_add_u32_e32 v235, 0x1000, v235
	global_store_dword v236, v37, s[46:47]
	v_add_u32_e32 v236, 0x1000, v236
	v_fma_f32 v233, -v37, v1, v38
	v_fmac_f32_e32 v228, 0x3dcccccd, v233
	v_fma_f32 v38, s48, v228, v37
	global_store_dword v232, v38, s[18:19]
	v_add_u32_e32 v232, 0x1000, v232
	global_store_dword v235, v228, s[44:45]
	v_add_u32_e32 v235, 0x1000, v235
	global_store_dword v236, v38, s[46:47]
	v_add_u32_e32 v236, 0x1000, v236
	v_fma_f32 v233, -v38, v1, v39
	v_fmac_f32_e32 v228, 0x3dcccccd, v233
	v_fma_f32 v39, s48, v228, v38
	global_store_dword v232, v39, s[18:19]
	v_add_u32_e32 v232, 0x1000, v232
	global_store_dword v235, v228, s[44:45]
	v_add_u32_e32 v235, 0x1000, v235
	global_store_dword v236, v39, s[46:47]
	v_add_u32_e32 v236, 0x1000, v236
	v_fma_f32 v233, -v39, v1, v40
	v_fmac_f32_e32 v228, 0x3dcccccd, v233
	v_fma_f32 v40, s48, v228, v39
	global_store_dword v232, v40, s[18:19]
	v_add_u32_e32 v232, 0x1000, v232
	global_store_dword v235, v228, s[44:45]
	v_add_u32_e32 v235, 0x1000, v235
	global_store_dword v236, v40, s[46:47]
	v_add_u32_e32 v236, 0x1000, v236
	v_fma_f32 v233, -v40, v1, v41
	v_fmac_f32_e32 v228, 0x3dcccccd, v233
	v_fma_f32 v41, s48, v228, v40
	global_store_dword v232, v41, s[18:19]
	v_add_u32_e32 v232, 0x1000, v232
	global_store_dword v235, v228, s[44:45]
	v_add_u32_e32 v235, 0x1000, v235
	global_store_dword v236, v41, s[46:47]
	v_add_u32_e32 v236, 0x1000, v236
	v_fma_f32 v233, -v41, v1, v42
	v_fmac_f32_e32 v228, 0x3dcccccd, v233
	v_fma_f32 v42, s48, v228, v41
	global_store_dword v232, v42, s[18:19]
	v_add_u32_e32 v232, 0x1000, v232
	global_store_dword v235, v228, s[44:45]
	v_add_u32_e32 v235, 0x1000, v235
	global_store_dword v236, v42, s[46:47]
	v_add_u32_e32 v236, 0x1000, v236
	v_fma_f32 v233, -v42, v1, v43
	v_fmac_f32_e32 v228, 0x3dcccccd, v233
	v_fma_f32 v43, s48, v228, v42
	global_store_dword v232, v43, s[18:19]
	v_add_u32_e32 v232, 0x1000, v232
	global_store_dword v235, v228, s[44:45]
	v_add_u32_e32 v235, 0x1000, v235
	global_store_dword v236, v43, s[46:47]
	v_add_u32_e32 v236, 0x1000, v236
	v_fma_f32 v233, -v43, v1, v44
	v_fmac_f32_e32 v228, 0x3dcccccd, v233
	v_fma_f32 v44, s48, v228, v43
	global_store_dword v232, v44, s[18:19]
	v_add_u32_e32 v232, 0x1000, v232
	global_store_dword v235, v228, s[44:45]
	v_add_u32_e32 v235, 0x1000, v235
	global_store_dword v236, v44, s[46:47]
	v_add_u32_e32 v236, 0x1000, v236
	v_fma_f32 v233, -v44, v1, v45
	v_fmac_f32_e32 v228, 0x3dcccccd, v233
	v_fma_f32 v45, s48, v228, v44
	global_store_dword v232, v45, s[18:19]
	v_add_u32_e32 v232, 0x1000, v232
	global_store_dword v235, v228, s[44:45]
	v_add_u32_e32 v235, 0x1000, v235
	global_store_dword v236, v45, s[46:47]
	v_add_u32_e32 v236, 0x1000, v236
	v_fma_f32 v233, -v45, v1, v46
	v_fmac_f32_e32 v228, 0x3dcccccd, v233
	v_fma_f32 v46, s48, v228, v45
	global_store_dword v232, v46, s[18:19]
	v_add_u32_e32 v232, 0x1000, v232
	global_store_dword v235, v228, s[44:45]
	v_add_u32_e32 v235, 0x1000, v235
	global_store_dword v236, v46, s[46:47]
	v_add_u32_e32 v236, 0x1000, v236
	v_fma_f32 v233, -v46, v1, v47
	v_fmac_f32_e32 v228, 0x3dcccccd, v233
	v_fma_f32 v47, s48, v228, v46
	global_store_dword v232, v47, s[18:19]
	v_add_u32_e32 v232, 0x1000, v232
	global_store_dword v235, v228, s[44:45]
	v_add_u32_e32 v235, 0x1000, v235
	global_store_dword v236, v47, s[46:47]
	v_add_u32_e32 v236, 0x1000, v236
	v_fma_f32 v233, -v47, v1, v48
	v_fmac_f32_e32 v228, 0x3dcccccd, v233
	v_fma_f32 v48, s48, v228, v47
	global_store_dword v232, v48, s[18:19]
	v_add_u32_e32 v232, 0x1000, v232
	global_store_dword v235, v228, s[44:45]
	v_add_u32_e32 v235, 0x1000, v235
	global_store_dword v236, v48, s[46:47]
	v_add_u32_e32 v236, 0x1000, v236
	v_fma_f32 v233, -v48, v1, v49
	v_fmac_f32_e32 v228, 0x3dcccccd, v233
	v_fma_f32 v49, s48, v228, v48
	global_store_dword v232, v49, s[18:19]
	v_add_u32_e32 v232, 0x1000, v232
	global_store_dword v235, v228, s[44:45]
	v_add_u32_e32 v235, 0x1000, v235
	global_store_dword v236, v49, s[46:47]
	v_add_u32_e32 v236, 0x1000, v236
	v_fma_f32 v233, -v49, v1, v18
	v_fmac_f32_e32 v228, 0x3dcccccd, v233
	v_fma_f32 v18, s48, v228, v49
	global_store_dword v232, v18, s[18:19]
	v_add_u32_e32 v232, 0x1000, v232
	global_store_dword v235, v228, s[44:45]
	v_add_u32_e32 v235, 0x1000, v235
	global_store_dword v236, v18, s[46:47]
	v_add_u32_e32 v236, 0x1000, v236
	v_fma_f32 v233, -v18, v1, v19
	v_fmac_f32_e32 v228, 0x3dcccccd, v233
	v_fma_f32 v19, s48, v228, v18
	global_store_dword v232, v19, s[18:19]
	v_add_u32_e32 v232, 0x1000, v232
	global_store_dword v235, v228, s[44:45]
	v_add_u32_e32 v235, 0x1000, v235
	global_store_dword v236, v19, s[46:47]
	v_add_u32_e32 v236, 0x1000, v236
	v_fma_f32 v233, -v19, v1, v20
	v_fmac_f32_e32 v228, 0x3dcccccd, v233
	v_fma_f32 v20, s48, v228, v19
	global_store_dword v232, v20, s[18:19]
	v_add_u32_e32 v232, 0x1000, v232
	global_store_dword v235, v228, s[44:45]
	v_add_u32_e32 v235, 0x1000, v235
	global_store_dword v236, v20, s[46:47]
	v_add_u32_e32 v236, 0x1000, v236
	v_fma_f32 v233, -v20, v1, v21
	v_fmac_f32_e32 v228, 0x3dcccccd, v233
	v_fma_f32 v21, s48, v228, v20
	global_store_dword v232, v21, s[18:19]
	v_add_u32_e32 v232, 0x1000, v232
	global_store_dword v235, v228, s[44:45]
	v_add_u32_e32 v235, 0x1000, v235
	global_store_dword v236, v21, s[46:47]
	v_add_u32_e32 v236, 0x1000, v236
	v_fma_f32 v233, -v21, v1, v22
	v_fmac_f32_e32 v228, 0x3dcccccd, v233
	v_fma_f32 v22, s48, v228, v21
	global_store_dword v232, v22, s[18:19]
	v_add_u32_e32 v232, 0x1000, v232
	global_store_dword v235, v228, s[44:45]
	v_add_u32_e32 v235, 0x1000, v235
	global_store_dword v236, v22, s[46:47]
	v_add_u32_e32 v236, 0x1000, v236
	v_fma_f32 v233, -v22, v1, v23
	v_fmac_f32_e32 v228, 0x3dcccccd, v233
	v_fma_f32 v23, s48, v228, v22
	global_store_dword v232, v23, s[18:19]
	v_add_u32_e32 v232, 0x1000, v232
	global_store_dword v235, v228, s[44:45]
	v_add_u32_e32 v235, 0x1000, v235
	global_store_dword v236, v23, s[46:47]
	v_add_u32_e32 v236, 0x1000, v236
	v_fma_f32 v233, -v23, v1, v24
	v_fmac_f32_e32 v228, 0x3dcccccd, v233
	v_fma_f32 v24, s48, v228, v23
	global_store_dword v232, v24, s[18:19]
	v_add_u32_e32 v232, 0x1000, v232
	global_store_dword v235, v228, s[44:45]
	v_add_u32_e32 v235, 0x1000, v235
	global_store_dword v236, v24, s[46:47]
	v_add_u32_e32 v236, 0x1000, v236
	v_fma_f32 v233, -v24, v1, v25
	v_fmac_f32_e32 v228, 0x3dcccccd, v233
	v_fma_f32 v25, s48, v228, v24
	global_store_dword v232, v25, s[18:19]
	v_add_u32_e32 v232, 0x1000, v232
	global_store_dword v235, v228, s[44:45]
	v_add_u32_e32 v235, 0x1000, v235
	global_store_dword v236, v25, s[46:47]
	v_add_u32_e32 v236, 0x1000, v236
	v_fma_f32 v233, -v25, v1, v26
	v_fmac_f32_e32 v228, 0x3dcccccd, v233
	v_fma_f32 v26, s48, v228, v25
	global_store_dword v232, v26, s[18:19]
	v_add_u32_e32 v232, 0x1000, v232
	global_store_dword v235, v228, s[44:45]
	v_add_u32_e32 v235, 0x1000, v235
	global_store_dword v236, v26, s[46:47]
	v_add_u32_e32 v236, 0x1000, v236
	v_fma_f32 v233, -v26, v1, v27
	v_fmac_f32_e32 v228, 0x3dcccccd, v233
	v_fma_f32 v27, s48, v228, v26
	global_store_dword v232, v27, s[18:19]
	v_add_u32_e32 v232, 0x1000, v232
	global_store_dword v235, v228, s[44:45]
	v_add_u32_e32 v235, 0x1000, v235
	global_store_dword v236, v27, s[46:47]
	v_add_u32_e32 v236, 0x1000, v236
	v_fma_f32 v233, -v27, v1, v28
	v_fmac_f32_e32 v228, 0x3dcccccd, v233
	v_fma_f32 v28, s48, v228, v27
	global_store_dword v232, v28, s[18:19]
	v_add_u32_e32 v232, 0x1000, v232
	global_store_dword v235, v228, s[44:45]
	v_add_u32_e32 v235, 0x1000, v235
	global_store_dword v236, v28, s[46:47]
	v_add_u32_e32 v236, 0x1000, v236
	v_fma_f32 v233, -v28, v1, v29
	v_fmac_f32_e32 v228, 0x3dcccccd, v233
	v_fma_f32 v29, s48, v228, v28
	global_store_dword v232, v29, s[18:19]
	v_add_u32_e32 v232, 0x1000, v232
	global_store_dword v235, v228, s[44:45]
	v_add_u32_e32 v235, 0x1000, v235
	global_store_dword v236, v29, s[46:47]
	v_add_u32_e32 v236, 0x1000, v236
	v_fma_f32 v233, -v29, v1, v30
	v_fmac_f32_e32 v228, 0x3dcccccd, v233
	v_fma_f32 v30, s48, v228, v29
	global_store_dword v232, v30, s[18:19]
	v_add_u32_e32 v232, 0x1000, v232
	global_store_dword v235, v228, s[44:45]
	v_add_u32_e32 v235, 0x1000, v235
	global_store_dword v236, v30, s[46:47]
	v_add_u32_e32 v236, 0x1000, v236
	v_fma_f32 v233, -v30, v1, v31
	v_fmac_f32_e32 v228, 0x3dcccccd, v233
	v_fma_f32 v31, s48, v228, v30
	global_store_dword v232, v31, s[18:19]
	v_add_u32_e32 v232, 0x1000, v232
	global_store_dword v235, v228, s[44:45]
	v_add_u32_e32 v235, 0x1000, v235
	global_store_dword v236, v31, s[46:47]
	v_add_u32_e32 v236, 0x1000, v236
	v_fma_f32 v233, -v31, v1, v32
	v_fmac_f32_e32 v228, 0x3dcccccd, v233
	v_fma_f32 v32, s48, v228, v31
	global_store_dword v232, v32, s[18:19]
	v_add_u32_e32 v232, 0x1000, v232
	global_store_dword v235, v228, s[44:45]
	v_add_u32_e32 v235, 0x1000, v235
	global_store_dword v236, v32, s[46:47]
	v_add_u32_e32 v236, 0x1000, v236
	v_fma_f32 v233, -v32, v1, v33
	v_fmac_f32_e32 v228, 0x3dcccccd, v233
	v_fma_f32 v33, s48, v228, v32
	global_store_dword v232, v33, s[18:19]
	v_add_u32_e32 v232, 0x1000, v232
	global_store_dword v235, v228, s[44:45]
	v_add_u32_e32 v235, 0x1000, v235
	global_store_dword v236, v33, s[46:47]
	v_add_u32_e32 v236, 0x1000, v236
	v_fma_f32 v233, -v33, v1, v2
	v_fmac_f32_e32 v228, 0x3dcccccd, v233
	v_fma_f32 v2, s48, v228, v33
	global_store_dword v232, v2, s[18:19]
	v_add_u32_e32 v232, 0x1000, v232
	global_store_dword v235, v228, s[44:45]
	v_add_u32_e32 v235, 0x1000, v235
	global_store_dword v236, v2, s[46:47]
	v_add_u32_e32 v236, 0x1000, v236
	v_fma_f32 v233, -v2, v1, v3
	v_fmac_f32_e32 v228, 0x3dcccccd, v233
	v_fma_f32 v3, s48, v228, v2
	global_store_dword v232, v3, s[18:19]
	v_add_u32_e32 v232, 0x1000, v232
	global_store_dword v235, v228, s[44:45]
	v_add_u32_e32 v235, 0x1000, v235
	global_store_dword v236, v3, s[46:47]
	v_add_u32_e32 v236, 0x1000, v236
	v_fma_f32 v233, -v3, v1, v4
	v_fmac_f32_e32 v228, 0x3dcccccd, v233
	v_fma_f32 v4, s48, v228, v3
	global_store_dword v232, v4, s[18:19]
	v_add_u32_e32 v232, 0x1000, v232
	global_store_dword v235, v228, s[44:45]
	v_add_u32_e32 v235, 0x1000, v235
	global_store_dword v236, v4, s[46:47]
	v_add_u32_e32 v236, 0x1000, v236
	v_fma_f32 v233, -v4, v1, v5
	v_fmac_f32_e32 v228, 0x3dcccccd, v233
	v_fma_f32 v5, s48, v228, v4
	global_store_dword v232, v5, s[18:19]
	v_add_u32_e32 v232, 0x1000, v232
	global_store_dword v235, v228, s[44:45]
	v_add_u32_e32 v235, 0x1000, v235
	global_store_dword v236, v5, s[46:47]
	v_add_u32_e32 v236, 0x1000, v236
	v_fma_f32 v233, -v5, v1, v6
	v_fmac_f32_e32 v228, 0x3dcccccd, v233
	v_fma_f32 v6, s48, v228, v5
	global_store_dword v232, v6, s[18:19]
	v_add_u32_e32 v232, 0x1000, v232
	global_store_dword v235, v228, s[44:45]
	v_add_u32_e32 v235, 0x1000, v235
	global_store_dword v236, v6, s[46:47]
	v_add_u32_e32 v236, 0x1000, v236
	v_fma_f32 v233, -v6, v1, v7
	v_fmac_f32_e32 v228, 0x3dcccccd, v233
	v_fma_f32 v7, s48, v228, v6
	global_store_dword v232, v7, s[18:19]
	v_add_u32_e32 v232, 0x1000, v232
	global_store_dword v235, v228, s[44:45]
	v_add_u32_e32 v235, 0x1000, v235
	global_store_dword v236, v7, s[46:47]
	v_add_u32_e32 v236, 0x1000, v236
	v_fma_f32 v233, -v7, v1, v8
	v_fmac_f32_e32 v228, 0x3dcccccd, v233
	v_fma_f32 v8, s48, v228, v7
	global_store_dword v232, v8, s[18:19]
	v_add_u32_e32 v232, 0x1000, v232
	global_store_dword v235, v228, s[44:45]
	v_add_u32_e32 v235, 0x1000, v235
	global_store_dword v236, v8, s[46:47]
	v_add_u32_e32 v236, 0x1000, v236
	v_fma_f32 v233, -v8, v1, v9
	v_fmac_f32_e32 v228, 0x3dcccccd, v233
	v_fma_f32 v9, s48, v228, v8
	global_store_dword v232, v9, s[18:19]
	v_add_u32_e32 v232, 0x1000, v232
	global_store_dword v235, v228, s[44:45]
	v_add_u32_e32 v235, 0x1000, v235
	global_store_dword v236, v9, s[46:47]
	v_add_u32_e32 v236, 0x1000, v236
	v_fma_f32 v233, -v9, v1, v10
	v_fmac_f32_e32 v228, 0x3dcccccd, v233
	v_fma_f32 v10, s48, v228, v9
	global_store_dword v232, v10, s[18:19]
	v_add_u32_e32 v232, 0x1000, v232
	global_store_dword v235, v228, s[44:45]
	v_add_u32_e32 v235, 0x1000, v235
	global_store_dword v236, v10, s[46:47]
	v_add_u32_e32 v236, 0x1000, v236
	v_fma_f32 v233, -v10, v1, v11
	v_fmac_f32_e32 v228, 0x3dcccccd, v233
	v_fma_f32 v11, s48, v228, v10
	global_store_dword v232, v11, s[18:19]
	v_add_u32_e32 v232, 0x1000, v232
	global_store_dword v235, v228, s[44:45]
	v_add_u32_e32 v235, 0x1000, v235
	global_store_dword v236, v11, s[46:47]
	v_add_u32_e32 v236, 0x1000, v236
	v_fma_f32 v233, -v11, v1, v12
	v_fmac_f32_e32 v228, 0x3dcccccd, v233
	v_fma_f32 v12, s48, v228, v11
	global_store_dword v232, v12, s[18:19]
	v_add_u32_e32 v232, 0x1000, v232
	global_store_dword v235, v228, s[44:45]
	v_add_u32_e32 v235, 0x1000, v235
	global_store_dword v236, v12, s[46:47]
	v_add_u32_e32 v236, 0x1000, v236
	v_fma_f32 v233, -v12, v1, v13
	v_fmac_f32_e32 v228, 0x3dcccccd, v233
	v_fma_f32 v13, s48, v228, v12
	global_store_dword v232, v13, s[18:19]
	v_add_u32_e32 v232, 0x1000, v232
	global_store_dword v235, v228, s[44:45]
	v_add_u32_e32 v235, 0x1000, v235
	global_store_dword v236, v13, s[46:47]
	v_add_u32_e32 v236, 0x1000, v236
	v_fma_f32 v233, -v13, v1, v14
	v_fmac_f32_e32 v228, 0x3dcccccd, v233
	v_fma_f32 v14, s48, v228, v13
	global_store_dword v232, v14, s[18:19]
	v_add_u32_e32 v232, 0x1000, v232
	global_store_dword v235, v228, s[44:45]
	v_add_u32_e32 v235, 0x1000, v235
	global_store_dword v236, v14, s[46:47]
	v_add_u32_e32 v236, 0x1000, v236
	v_fma_f32 v233, -v14, v1, v15
	v_fmac_f32_e32 v228, 0x3dcccccd, v233
	v_fma_f32 v15, s48, v228, v14
	global_store_dword v232, v15, s[18:19]
	v_add_u32_e32 v232, 0x1000, v232
	global_store_dword v235, v228, s[44:45]
	v_add_u32_e32 v235, 0x1000, v235
	global_store_dword v236, v15, s[46:47]
	v_add_u32_e32 v236, 0x1000, v236
	v_fma_f32 v233, -v15, v1, v16
	v_fmac_f32_e32 v228, 0x3dcccccd, v233
	v_fma_f32 v16, s48, v228, v15
	global_store_dword v232, v16, s[18:19]
	v_add_u32_e32 v232, 0x1000, v232
	global_store_dword v235, v228, s[44:45]
	v_add_u32_e32 v235, 0x1000, v235
	global_store_dword v236, v16, s[46:47]
	v_add_u32_e32 v236, 0x1000, v236
	v_fma_f32 v233, -v16, v1, v17
	v_fmac_f32_e32 v228, 0x3dcccccd, v233
	v_fma_f32 v17, s48, v228, v16
	global_store_dword v232, v17, s[18:19]
	v_add_u32_e32 v232, 0x1000, v232
	global_store_dword v235, v228, s[44:45]
	v_add_u32_e32 v235, 0x1000, v235
	global_store_dword v236, v17, s[46:47]
	v_add_u32_e32 v236, 0x1000, v236
	s_endpgm
